# phase-level GEMMs: one static s_setprio 1 for waves 4-7 at GEMM entry (reset at exit) instead of the per-MFMA-block priority toggles
# speedup vs baseline: 1.0084x; 1.0036x over previous
.LBB0_415:
	v_and_b32_e32 v9, 15, v8
	v_and_b32_e32 v18, 48, v8
	v_lshlrev_b32_e32 v8, 2, v8
	v_mov_b32_e32 v155, v131
	s_sext_i32_i8 s17, s6
	s_and_b32 s8, s8, 3
	v_lshl_or_b32 v19, s7, 6, v9
	s_lshl_b32 s6, s7, 13
	v_lshl_or_b32 v9, v9, 6, v18
	v_and_b32_e32 v8, 32, v8
	v_lshl_add_u64 v[10:11], s[68:69], 0, v[154:155]
	v_mov_b32_e32 v151, v131
	v_bitop3_b32 v20, v9, s6, v8 bitop3:0xde
	s_lshl_b32 s6, s8, 12
	v_lshl_add_u64 v[12:13], s[68:69], 0, v[150:151]
	v_mov_b32_e32 v153, v131
	v_bitop3_b32 v168, v9, s6, v8 bitop3:0xde
	s_add_i32 m0, s39, 0x18000
	v_lshl_add_u64 v[8:9], v[10:11], 0, s[30:31]
	v_lshl_add_u64 v[14:15], s[66:67], 0, v[152:153]
	v_mov_b32_e32 v149, v131
	s_waitcnt vmcnt(4)
	s_barrier
	v_readfirstlane_b32 s100, v0
	s_cmp_lt_u32 s100, 0x100
	s_cbranch_scc1 .Lmy_sp_gate
	s_setprio 1
.Lmy_sp_gate:
	global_load_lds_dwordx4 v[8:9], off
	v_lshl_add_u64 v[8:9], v[12:13], 0, s[30:31]
	s_add_i32 m0, s39, 0x1a000
	s_add_i32 s45, s39, 0x8000
	s_add_i32 s46, s39, 0xa000
	v_lshl_add_u64 v[16:17], s[66:67], 0, v[148:149]
	global_load_lds_dwordx4 v[8:9], off
	v_lshl_add_u64 v[8:9], v[14:15], 0, s[30:31]
	s_mov_b32 m0, s45
	s_add_u32 s6, s68, 0x2080
	global_load_lds_dwordx4 v[8:9], off
	v_lshl_add_u64 v[8:9], v[16:17], 0, s[30:31]
	s_mov_b32 m0, s46
	s_addc_u32 s7, s69, 0
	global_load_lds_dwordx4 v[8:9], off
	s_add_i32 m0, s39, 0x1c000
	v_lshl_add_u64 v[8:9], s[6:7], 0, v[154:155]
	global_load_lds_dwordx4 v[8:9], off
	v_lshl_add_u64 v[8:9], s[6:7], 0, v[150:151]
	s_add_i32 m0, s39, 0x1e000
	s_movk_i32 s6, 0x1e00
	global_load_lds_dwordx4 v[8:9], off
	v_mul_lo_u32 v8, v19, s6
	s_lshl_b32 s6, s8, 6
	v_or3_b32 v169, v8, s6, v18
	v_lshlrev_b32_e32 v8, 13, v6
	v_and_b32_e32 v8, 0xffffc000, v8
	v_lshl_add_u32 v5, v5, 10, v8
	v_and_b32_e32 v6, 1, v6
	v_lshl_or_b32 v5, v6, 6, v5
	v_lshl_add_u32 v156, v7, 1, v5
	v_lshlrev_b32_e32 v5, 13, v2
	v_and_b32_e32 v5, 0xffffc000, v5
	s_waitcnt vmcnt(6)
	v_lshl_add_u32 v3, v3, 10, v5
	v_and_b32_e32 v2, 1, v2
	v_lshl_or_b32 v2, v2, 6, v3
	v_mov_b32_e32 v157, v131
	v_lshl_add_u32 v158, v4, 1, v2
	v_mov_b32_e32 v159, v131
	s_mov_b32 s47, 0
	v_add_u32_e32 v170, 0, v20
	s_barrier
	s_waitcnt vmcnt(0)

.LBB0_418:
	s_add_i32 s60, 0, 0x10000
	v_add_u32_e32 v130, s60, v168
	ds_read_b128 v[2:5], v130
	ds_read_b128 v[6:9], v130 offset:1024
	ds_read_b128 v[10:13], v130 offset:2048
	ds_read_b128 v[14:17], v130 offset:3072
	s_add_u32 s58, s66, 0x20080
	s_addc_u32 s59, s67, 0
	s_add_i32 s9, s39, 0xc000
	v_lshl_add_u64 v[50:51], s[58:59], 0, v[152:153]
	s_mov_b32 m0, s9
	s_add_i32 s51, s39, 0xe000
	ds_read_b128 v[18:21], v170
	ds_read_b128 v[22:25], v170 offset:1024
	ds_read_b128 v[26:29], v170 offset:2048
	ds_read_b128 v[30:33], v170 offset:3072
	ds_read_b128 v[34:37], v170 offset:4096
	ds_read_b128 v[38:41], v170 offset:5120
	ds_read_b128 v[42:45], v170 offset:6144
	ds_read_b128 v[46:49], v170 offset:7168
	global_load_lds_dwordx4 v[50:51], off
	v_lshl_add_u64 v[50:51], s[58:59], 0, v[148:149]
	s_mov_b32 m0, s51
	s_nop 0
	global_load_lds_dwordx4 v[50:51], off
	s_waitcnt lgkmcnt(8)
	s_waitcnt vmcnt(10)
	s_barrier
	s_waitcnt lgkmcnt(6)
	v_mfma_scale_f32_16x16x128_f8f6f4 v[136:139], v[2:9], v[18:25], 0, v205, v205 op_sel_hi:[0,0,0]
	v_mfma_scale_f32_16x16x128_f8f6f4 v[132:135], v[10:17], v[18:25], 0, v205, v205 op_sel_hi:[0,0,0]
	s_waitcnt lgkmcnt(4)
	v_mfma_scale_f32_16x16x128_f8f6f4 v[118:121], v[2:9], v[26:33], 0, v205, v205 op_sel_hi:[0,0,0]
	v_mfma_scale_f32_16x16x128_f8f6f4 v[114:117], v[10:17], v[26:33], 0, v205, v205 op_sel_hi:[0,0,0]
	s_waitcnt lgkmcnt(2)
	v_mfma_scale_f32_16x16x128_f8f6f4 v[106:109], v[2:9], v[34:41], 0, v205, v205 op_sel_hi:[0,0,0]
	v_mfma_scale_f32_16x16x128_f8f6f4 v[98:101], v[10:17], v[34:41], 0, v205, v205 op_sel_hi:[0,0,0]
	s_waitcnt lgkmcnt(0)
	v_mfma_scale_f32_16x16x128_f8f6f4 v[86:89], v[2:9], v[42:49], 0, v205, v205 op_sel_hi:[0,0,0]
	v_mfma_scale_f32_16x16x128_f8f6f4 v[70:73], v[10:17], v[42:49], 0, v205, v205 op_sel_hi:[0,0,0]
	s_barrier
	s_add_i32 s61, 0, 0x14000
	v_lshl_add_u64 v[164:165], s[68:69], 0, v[154:155]
	s_mov_b64 s[62:63], 0x100
	s_add_i32 s58, s60, s37
	v_add_u32_e32 v171, s61, v168
	v_lshl_add_u64 v[50:51], v[164:165], 0, s[62:63]
	s_mov_b32 m0, s58
	v_lshl_add_u64 v[166:167], s[68:69], 0, v[150:151]
	s_add_i32 s59, s58, 0x2000
	ds_read_b128 v[178:181], v171
	ds_read_b128 v[182:185], v171 offset:1024
	ds_read_b128 v[186:189], v171 offset:2048
	ds_read_b128 v[190:193], v171 offset:3072
	global_load_lds_dwordx4 v[50:51], off
	v_lshl_add_u64 v[50:51], v[166:167], 0, s[62:63]
	s_mov_b32 m0, s59
	s_nop 0
	global_load_lds_dwordx4 v[50:51], off
	s_waitcnt vmcnt(10)
	s_barrier
	s_waitcnt lgkmcnt(2)
	v_mfma_scale_f32_16x16x128_f8f6f4 v[144:147], v[178:185], v[18:25], 0, v205, v205 op_sel_hi:[0,0,0]
	s_waitcnt lgkmcnt(0)
	v_mfma_scale_f32_16x16x128_f8f6f4 v[140:143], v[186:193], v[18:25], 0, v205, v205 op_sel_hi:[0,0,0]
	v_mfma_scale_f32_16x16x128_f8f6f4 v[126:129], v[178:185], v[26:33], 0, v205, v205 op_sel_hi:[0,0,0]
	v_mfma_scale_f32_16x16x128_f8f6f4 v[122:125], v[186:193], v[26:33], 0, v205, v205 op_sel_hi:[0,0,0]
	v_mfma_scale_f32_16x16x128_f8f6f4 v[110:113], v[178:185], v[34:41], 0, v205, v205 op_sel_hi:[0,0,0]
	v_mfma_scale_f32_16x16x128_f8f6f4 v[102:105], v[186:193], v[34:41], 0, v205, v205 op_sel_hi:[0,0,0]
	v_mfma_scale_f32_16x16x128_f8f6f4 v[94:97], v[178:185], v[42:49], 0, v205, v205 op_sel_hi:[0,0,0]
	v_mfma_scale_f32_16x16x128_f8f6f4 v[78:81], v[186:193], v[42:49], 0, v205, v205 op_sel_hi:[0,0,0]
	v_lshl_add_u64 v[160:161], s[66:67], 0, v[152:153]
	s_mov_b32 m0, s39
	v_lshl_add_u64 v[18:19], v[160:161], 0, s[62:63]
	v_lshl_add_u64 v[162:163], s[66:67], 0, v[148:149]
	s_barrier
	ds_read_b128 v[194:197], v170 offset:16384
	ds_read_b128 v[198:201], v170 offset:17408
	ds_read_b128 v[218:221], v170 offset:18432
	ds_read_b128 v[222:225], v170 offset:19456
	ds_read_b128 v[226:229], v170 offset:20480
	ds_read_b128 v[230:233], v170 offset:21504
	ds_read_b128 v[234:237], v170 offset:22528
	ds_read_b128 v[238:241], v170 offset:23552
	global_load_lds_dwordx4 v[18:19], off
	v_lshl_add_u64 v[18:19], v[162:163], 0, s[62:63]
	s_mov_b32 m0, s42
	s_nop 0
	global_load_lds_dwordx4 v[18:19], off
	s_barrier
	s_waitcnt lgkmcnt(6)
	v_mfma_scale_f32_16x16x128_f8f6f4 v[82:85], v[2:9], v[194:201], 0, v205, v205 op_sel_hi:[0,0,0]
	v_mfma_scale_f32_16x16x128_f8f6f4 v[66:69], v[10:17], v[194:201], 0, v205, v205 op_sel_hi:[0,0,0]
	s_waitcnt lgkmcnt(4)
	v_mfma_scale_f32_16x16x128_f8f6f4 v[58:61], v[2:9], v[218:225], 0, v205, v205 op_sel_hi:[0,0,0]
	v_mfma_scale_f32_16x16x128_f8f6f4 v[50:53], v[10:17], v[218:225], 0, v205, v205 op_sel_hi:[0,0,0]
	s_waitcnt lgkmcnt(2)
	v_mfma_scale_f32_16x16x128_f8f6f4 v[46:49], v[2:9], v[226:233], 0, v205, v205 op_sel_hi:[0,0,0]
	v_mfma_scale_f32_16x16x128_f8f6f4 v[38:41], v[10:17], v[226:233], 0, v205, v205 op_sel_hi:[0,0,0]
	s_waitcnt lgkmcnt(0)
	v_mfma_scale_f32_16x16x128_f8f6f4 v[30:33], v[2:9], v[234:241], 0, v205, v205 op_sel_hi:[0,0,0]
	v_mfma_scale_f32_16x16x128_f8f6f4 v[22:25], v[10:17], v[234:241], 0, v205, v205 op_sel_hi:[0,0,0]
	s_barrier
	s_add_u32 s62, s68, 0x2100
	s_addc_u32 s63, s69, 0
	s_add_i32 s60, s61, s37
	v_lshl_add_u64 v[2:3], s[62:63], 0, v[154:155]
	s_mov_b32 m0, s60
	s_add_i32 s61, s60, 0x2000
	global_load_lds_dwordx4 v[2:3], off
	v_lshl_add_u64 v[2:3], s[62:63], 0, v[150:151]
	s_mov_b32 m0, s61
	s_nop 0
	global_load_lds_dwordx4 v[2:3], off
	s_waitcnt vmcnt(10)
	s_barrier
	v_mfma_scale_f32_16x16x128_f8f6f4 v[90:93], v[178:185], v[194:201], 0, v205, v205 op_sel_hi:[0,0,0]
	v_mfma_scale_f32_16x16x128_f8f6f4 v[74:77], v[186:193], v[194:201], 0, v205, v205 op_sel_hi:[0,0,0]
	v_mfma_scale_f32_16x16x128_f8f6f4 v[62:65], v[178:185], v[218:225], 0, v205, v205 op_sel_hi:[0,0,0]
	v_mfma_scale_f32_16x16x128_f8f6f4 v[54:57], v[186:193], v[218:225], 0, v205, v205 op_sel_hi:[0,0,0]
	v_mfma_scale_f32_16x16x128_f8f6f4 v[42:45], v[178:185], v[226:233], 0, v205, v205 op_sel_hi:[0,0,0]
	v_mfma_scale_f32_16x16x128_f8f6f4 v[34:37], v[186:193], v[226:233], 0, v205, v205 op_sel_hi:[0,0,0]
	v_mfma_scale_f32_16x16x128_f8f6f4 v[26:29], v[178:185], v[234:241], 0, v205, v205 op_sel_hi:[0,0,0]
	v_mfma_scale_f32_16x16x128_f8f6f4 v[18:21], v[186:193], v[234:241], 0, v205, v205 op_sel_hi:[0,0,0]
	s_add_i32 s70, 0, 0x18000
	v_add_u32_e32 v172, s70, v168
	s_barrier
	ds_read_b128 v[10:13], v172
	ds_read_b128 v[14:17], v172 offset:1024
	ds_read_b128 v[2:5], v172 offset:2048
	ds_read_b128 v[6:9], v172 offset:3072
	s_add_u32 s62, s66, 0x20100
	s_addc_u32 s63, s67, 0
	s_mov_b32 m0, s43
	v_lshl_add_u64 v[174:175], s[62:63], 0, v[152:153]
	ds_read_b128 v[178:181], v170 offset:32768
	ds_read_b128 v[182:185], v170 offset:33792
	ds_read_b128 v[186:189], v170 offset:34816
	ds_read_b128 v[190:193], v170 offset:35840
	ds_read_b128 v[194:197], v170 offset:36864
	ds_read_b128 v[198:201], v170 offset:37888
	ds_read_b128 v[218:221], v170 offset:38912
	ds_read_b128 v[222:225], v170 offset:39936
	global_load_lds_dwordx4 v[174:175], off
	v_lshl_add_u64 v[174:175], s[62:63], 0, v[148:149]
	s_mov_b32 m0, s44
	s_nop 0
	global_load_lds_dwordx4 v[174:175], off
	s_waitcnt lgkmcnt(8)
	s_waitcnt vmcnt(10)
	s_barrier
	s_waitcnt lgkmcnt(6)
	v_mfma_scale_f32_16x16x128_f8f6f4 v[136:139], v[10:17], v[178:185], v[136:139], v205, v205 op_sel_hi:[0,0,0]
	v_mfma_scale_f32_16x16x128_f8f6f4 v[132:135], v[2:9], v[178:185], v[132:135], v205, v205 op_sel_hi:[0,0,0]
	s_waitcnt lgkmcnt(4)
	v_mfma_scale_f32_16x16x128_f8f6f4 v[118:121], v[10:17], v[186:193], v[118:121], v205, v205 op_sel_hi:[0,0,0]
	v_mfma_scale_f32_16x16x128_f8f6f4 v[114:117], v[2:9], v[186:193], v[114:117], v205, v205 op_sel_hi:[0,0,0]
	s_waitcnt lgkmcnt(2)
	v_mfma_scale_f32_16x16x128_f8f6f4 v[106:109], v[10:17], v[194:201], v[106:109], v205, v205 op_sel_hi:[0,0,0]
	v_mfma_scale_f32_16x16x128_f8f6f4 v[98:101], v[2:9], v[194:201], v[98:101], v205, v205 op_sel_hi:[0,0,0]
	s_waitcnt lgkmcnt(0)
	v_mfma_scale_f32_16x16x128_f8f6f4 v[86:89], v[10:17], v[218:225], v[86:89], v205, v205 op_sel_hi:[0,0,0]
	v_mfma_scale_f32_16x16x128_f8f6f4 v[70:73], v[2:9], v[218:225], v[70:73], v205, v205 op_sel_hi:[0,0,0]
	s_barrier
	s_add_i32 s72, 0, 0x1c000
	s_mov_b64 s[74:75], 0x180
	s_add_i32 s62, s70, s37
	v_add_u32_e32 v173, s72, v168
	v_lshl_add_u64 v[164:165], v[164:165], 0, s[74:75]
	s_mov_b32 m0, s62
	s_add_i32 s63, s62, 0x2000
	ds_read_b128 v[226:229], v173
	ds_read_b128 v[230:233], v173 offset:1024
	ds_read_b128 v[234:237], v173 offset:2048
	ds_read_b128 v[238:241], v173 offset:3072
	global_load_lds_dwordx4 v[164:165], off
	v_lshl_add_u64 v[164:165], v[166:167], 0, s[74:75]
	s_mov_b32 m0, s63
	s_nop 0
	global_load_lds_dwordx4 v[164:165], off
	s_waitcnt vmcnt(10)
	s_barrier
	s_waitcnt lgkmcnt(2)
	v_mfma_scale_f32_16x16x128_f8f6f4 v[144:147], v[226:233], v[178:185], v[144:147], v205, v205 op_sel_hi:[0,0,0]
	s_waitcnt lgkmcnt(0)
	v_mfma_scale_f32_16x16x128_f8f6f4 v[140:143], v[234:241], v[178:185], v[140:143], v205, v205 op_sel_hi:[0,0,0]
	v_mfma_scale_f32_16x16x128_f8f6f4 v[126:129], v[226:233], v[186:193], v[126:129], v205, v205 op_sel_hi:[0,0,0]
	v_mfma_scale_f32_16x16x128_f8f6f4 v[122:125], v[234:241], v[186:193], v[122:125], v205, v205 op_sel_hi:[0,0,0]
	v_mfma_scale_f32_16x16x128_f8f6f4 v[110:113], v[226:233], v[194:201], v[110:113], v205, v205 op_sel_hi:[0,0,0]
	v_mfma_scale_f32_16x16x128_f8f6f4 v[102:105], v[234:241], v[194:201], v[102:105], v205, v205 op_sel_hi:[0,0,0]
	v_mfma_scale_f32_16x16x128_f8f6f4 v[94:97], v[226:233], v[218:225], v[94:97], v205, v205 op_sel_hi:[0,0,0]
	v_mfma_scale_f32_16x16x128_f8f6f4 v[78:81], v[234:241], v[218:225], v[78:81], v205, v205 op_sel_hi:[0,0,0]
	s_mov_b32 m0, s45
	v_lshl_add_u64 v[160:161], v[160:161], 0, s[74:75]
	s_barrier
	ds_read_b128 v[178:181], v170 offset:49152
	ds_read_b128 v[182:185], v170 offset:50176
	ds_read_b128 v[186:189], v170 offset:51200
	ds_read_b128 v[190:193], v170 offset:52224
	ds_read_b128 v[194:197], v170 offset:53248
	ds_read_b128 v[198:201], v170 offset:54272
	ds_read_b128 v[218:221], v170 offset:55296
	ds_read_b128 v[222:225], v170 offset:56320
	global_load_lds_dwordx4 v[160:161], off
	v_lshl_add_u64 v[160:161], v[162:163], 0, s[74:75]
	s_mov_b32 m0, s46
	s_nop 0
	global_load_lds_dwordx4 v[160:161], off
	s_barrier
	s_waitcnt lgkmcnt(6)
	v_mfma_scale_f32_16x16x128_f8f6f4 v[82:85], v[10:17], v[178:185], v[82:85], v205, v205 op_sel_hi:[0,0,0]
	v_mfma_scale_f32_16x16x128_f8f6f4 v[66:69], v[2:9], v[178:185], v[66:69], v205, v205 op_sel_hi:[0,0,0]
	s_waitcnt lgkmcnt(4)
	v_mfma_scale_f32_16x16x128_f8f6f4 v[58:61], v[10:17], v[186:193], v[58:61], v205, v205 op_sel_hi:[0,0,0]
	v_mfma_scale_f32_16x16x128_f8f6f4 v[50:53], v[2:9], v[186:193], v[50:53], v205, v205 op_sel_hi:[0,0,0]
	s_waitcnt lgkmcnt(2)
	v_mfma_scale_f32_16x16x128_f8f6f4 v[46:49], v[10:17], v[194:201], v[46:49], v205, v205 op_sel_hi:[0,0,0]
	v_mfma_scale_f32_16x16x128_f8f6f4 v[38:41], v[2:9], v[194:201], v[38:41], v205, v205 op_sel_hi:[0,0,0]
	s_waitcnt lgkmcnt(0)
	v_mfma_scale_f32_16x16x128_f8f6f4 v[30:33], v[10:17], v[218:225], v[30:33], v205, v205 op_sel_hi:[0,0,0]
	v_mfma_scale_f32_16x16x128_f8f6f4 v[22:25], v[2:9], v[218:225], v[22:25], v205, v205 op_sel_hi:[0,0,0]
	s_barrier
	s_add_u32 s70, s68, 0x2180
	s_addc_u32 s71, s69, 0
	s_add_i32 s72, s72, s37
	v_lshl_add_u64 v[2:3], s[70:71], 0, v[154:155]
	s_mov_b32 m0, s72
	s_add_i32 s73, s72, 0x2000
	global_load_lds_dwordx4 v[2:3], off
	v_lshl_add_u64 v[2:3], s[70:71], 0, v[150:151]
	s_mov_b32 m0, s73
	s_nop 0
	global_load_lds_dwordx4 v[2:3], off
	s_waitcnt vmcnt(10)
	s_barrier
	v_mfma_scale_f32_16x16x128_f8f6f4 v[90:93], v[226:233], v[178:185], v[90:93], v205, v205 op_sel_hi:[0,0,0]
	v_mfma_scale_f32_16x16x128_f8f6f4 v[74:77], v[234:241], v[178:185], v[74:77], v205, v205 op_sel_hi:[0,0,0]
	v_mfma_scale_f32_16x16x128_f8f6f4 v[62:65], v[226:233], v[186:193], v[62:65], v205, v205 op_sel_hi:[0,0,0]
	v_mfma_scale_f32_16x16x128_f8f6f4 v[54:57], v[234:241], v[186:193], v[54:57], v205, v205 op_sel_hi:[0,0,0]
	v_mfma_scale_f32_16x16x128_f8f6f4 v[42:45], v[226:233], v[194:201], v[42:45], v205, v205 op_sel_hi:[0,0,0]
	v_mfma_scale_f32_16x16x128_f8f6f4 v[34:37], v[234:241], v[194:201], v[34:37], v205, v205 op_sel_hi:[0,0,0]
	v_mfma_scale_f32_16x16x128_f8f6f4 v[26:29], v[226:233], v[218:225], v[26:29], v205, v205 op_sel_hi:[0,0,0]
	v_mfma_scale_f32_16x16x128_f8f6f4 v[18:21], v[234:241], v[218:225], v[18:21], v205, v205 op_sel_hi:[0,0,0]
	s_add_u32 s66, s66, 0x20180
	s_addc_u32 s67, s67, 0
	s_add_u32 s74, s68, 0x200
	s_addc_u32 s75, s69, 0
	s_mov_b32 s76, 0
	s_barrier
.LBB0_419:
	ds_read_b128 v[10:13], v130
	ds_read_b128 v[14:17], v130 offset:1024
	ds_read_b128 v[160:163], v130 offset:2048
	ds_read_b128 v[164:167], v130 offset:3072
	s_add_u32 s68, s66, 0xfffe0080
	s_addc_u32 s69, s67, -1
	s_cmp_eq_u32 s76, 4
	s_cselect_b32 s71, s19, s69
	s_cselect_b32 s70, s18, s68
	s_cselect_b32 s69, s65, s75
	s_cselect_b32 s68, s64, s74
	s_mov_b32 m0, s9
	v_lshl_add_u64 v[2:3], s[66:67], 0, v[156:157]
	ds_read_b128 v[178:181], v170
	ds_read_b128 v[182:185], v170 offset:1024
	ds_read_b128 v[186:189], v170 offset:2048
	ds_read_b128 v[190:193], v170 offset:3072
	ds_read_b128 v[194:197], v170 offset:4096
	ds_read_b128 v[198:201], v170 offset:5120
	ds_read_b128 v[218:221], v170 offset:6144
	ds_read_b128 v[222:225], v170 offset:7168
	global_load_lds_dwordx4 v[2:3], off
	v_lshl_add_u64 v[2:3], s[66:67], 0, v[158:159]
	s_mov_b32 m0, s51
	s_nop 0
	global_load_lds_dwordx4 v[2:3], off
	s_waitcnt lgkmcnt(8)
	s_waitcnt vmcnt(10)
	s_barrier
	s_waitcnt lgkmcnt(6)
	v_mfma_scale_f32_16x16x128_f8f6f4 v[136:139], v[10:17], v[178:185], v[136:139], v205, v205 op_sel_hi:[0,0,0]
	v_mfma_scale_f32_16x16x128_f8f6f4 v[132:135], v[160:167], v[178:185], v[132:135], v205, v205 op_sel_hi:[0,0,0]
	s_waitcnt lgkmcnt(4)
	v_mfma_scale_f32_16x16x128_f8f6f4 v[118:121], v[10:17], v[186:193], v[118:121], v205, v205 op_sel_hi:[0,0,0]
	v_mfma_scale_f32_16x16x128_f8f6f4 v[114:117], v[160:167], v[186:193], v[114:117], v205, v205 op_sel_hi:[0,0,0]
	s_waitcnt lgkmcnt(2)
	v_mfma_scale_f32_16x16x128_f8f6f4 v[106:109], v[10:17], v[194:201], v[106:109], v205, v205 op_sel_hi:[0,0,0]
	v_mfma_scale_f32_16x16x128_f8f6f4 v[98:101], v[160:167], v[194:201], v[98:101], v205, v205 op_sel_hi:[0,0,0]
	s_waitcnt lgkmcnt(0)
	v_mfma_scale_f32_16x16x128_f8f6f4 v[86:89], v[10:17], v[218:225], v[86:89], v205, v205 op_sel_hi:[0,0,0]
	v_mfma_scale_f32_16x16x128_f8f6f4 v[70:73], v[160:167], v[218:225], v[70:73], v205, v205 op_sel_hi:[0,0,0]
	s_barrier
	s_mov_b32 m0, s58
	v_lshl_add_u64 v[6:7], s[68:69], 0, v[154:155]
	ds_read_b128 v[226:229], v171
	ds_read_b128 v[230:233], v171 offset:1024
	ds_read_b128 v[234:237], v171 offset:2048
	ds_read_b128 v[238:241], v171 offset:3072
	global_load_lds_dwordx4 v[6:7], off
	v_lshl_add_u64 v[8:9], s[68:69], 0, v[150:151]
	s_mov_b32 m0, s59
	s_nop 0
	global_load_lds_dwordx4 v[8:9], off
	s_waitcnt vmcnt(10)
	s_barrier
	s_waitcnt lgkmcnt(2)
	v_mfma_scale_f32_16x16x128_f8f6f4 v[144:147], v[226:233], v[178:185], v[144:147], v205, v205 op_sel_hi:[0,0,0]
	s_waitcnt lgkmcnt(0)
	v_mfma_scale_f32_16x16x128_f8f6f4 v[140:143], v[234:241], v[178:185], v[140:143], v205, v205 op_sel_hi:[0,0,0]
	v_mfma_scale_f32_16x16x128_f8f6f4 v[126:129], v[226:233], v[186:193], v[126:129], v205, v205 op_sel_hi:[0,0,0]
	v_mfma_scale_f32_16x16x128_f8f6f4 v[122:125], v[234:241], v[186:193], v[122:125], v205, v205 op_sel_hi:[0,0,0]
	v_mfma_scale_f32_16x16x128_f8f6f4 v[110:113], v[226:233], v[194:201], v[110:113], v205, v205 op_sel_hi:[0,0,0]
	v_mfma_scale_f32_16x16x128_f8f6f4 v[102:105], v[234:241], v[194:201], v[102:105], v205, v205 op_sel_hi:[0,0,0]
	v_mfma_scale_f32_16x16x128_f8f6f4 v[94:97], v[226:233], v[218:225], v[94:97], v205, v205 op_sel_hi:[0,0,0]
	v_mfma_scale_f32_16x16x128_f8f6f4 v[78:81], v[234:241], v[218:225], v[78:81], v205, v205 op_sel_hi:[0,0,0]
	s_mov_b32 m0, s39
	v_lshl_add_u64 v[2:3], s[70:71], 0, v[152:153]
	s_barrier
	ds_read_b128 v[178:181], v170 offset:16384
	ds_read_b128 v[182:185], v170 offset:17408
	ds_read_b128 v[186:189], v170 offset:18432
	ds_read_b128 v[190:193], v170 offset:19456
	ds_read_b128 v[194:197], v170 offset:20480
	ds_read_b128 v[198:201], v170 offset:21504
	ds_read_b128 v[218:221], v170 offset:22528
	ds_read_b128 v[222:225], v170 offset:23552
	global_load_lds_dwordx4 v[2:3], off
	v_lshl_add_u64 v[4:5], s[70:71], 0, v[148:149]
	s_mov_b32 m0, s42
	s_nop 0
	global_load_lds_dwordx4 v[4:5], off
	s_barrier
	s_waitcnt lgkmcnt(6)
	v_mfma_scale_f32_16x16x128_f8f6f4 v[82:85], v[10:17], v[178:185], v[82:85], v205, v205 op_sel_hi:[0,0,0]
	v_mfma_scale_f32_16x16x128_f8f6f4 v[66:69], v[160:167], v[178:185], v[66:69], v205, v205 op_sel_hi:[0,0,0]
	s_waitcnt lgkmcnt(4)
	v_mfma_scale_f32_16x16x128_f8f6f4 v[58:61], v[10:17], v[186:193], v[58:61], v205, v205 op_sel_hi:[0,0,0]
	v_mfma_scale_f32_16x16x128_f8f6f4 v[50:53], v[160:167], v[186:193], v[50:53], v205, v205 op_sel_hi:[0,0,0]
	s_waitcnt lgkmcnt(2)
	v_mfma_scale_f32_16x16x128_f8f6f4 v[46:49], v[10:17], v[194:201], v[46:49], v205, v205 op_sel_hi:[0,0,0]
	v_mfma_scale_f32_16x16x128_f8f6f4 v[38:41], v[160:167], v[194:201], v[38:41], v205, v205 op_sel_hi:[0,0,0]
	s_waitcnt lgkmcnt(0)
	v_mfma_scale_f32_16x16x128_f8f6f4 v[30:33], v[10:17], v[218:225], v[30:33], v205, v205 op_sel_hi:[0,0,0]
	v_mfma_scale_f32_16x16x128_f8f6f4 v[22:25], v[160:167], v[218:225], v[22:25], v205, v205 op_sel_hi:[0,0,0]
	s_barrier
	s_add_u32 s78, s68, 0x2000
	s_addc_u32 s79, s69, 0
	s_mov_b32 m0, s60
	v_lshl_add_u64 v[10:11], s[78:79], 0, v[154:155]
	global_load_lds_dwordx4 v[10:11], off
	v_lshl_add_u64 v[10:11], s[78:79], 0, v[150:151]
	s_mov_b32 m0, s61
	s_nop 0
	global_load_lds_dwordx4 v[10:11], off
	s_waitcnt vmcnt(10)
	s_barrier
	v_mfma_scale_f32_16x16x128_f8f6f4 v[90:93], v[226:233], v[178:185], v[90:93], v205, v205 op_sel_hi:[0,0,0]
	v_mfma_scale_f32_16x16x128_f8f6f4 v[74:77], v[234:241], v[178:185], v[74:77], v205, v205 op_sel_hi:[0,0,0]
	v_mfma_scale_f32_16x16x128_f8f6f4 v[62:65], v[226:233], v[186:193], v[62:65], v205, v205 op_sel_hi:[0,0,0]
	v_mfma_scale_f32_16x16x128_f8f6f4 v[54:57], v[234:241], v[186:193], v[54:57], v205, v205 op_sel_hi:[0,0,0]
	v_mfma_scale_f32_16x16x128_f8f6f4 v[42:45], v[226:233], v[194:201], v[42:45], v205, v205 op_sel_hi:[0,0,0]
	v_mfma_scale_f32_16x16x128_f8f6f4 v[34:37], v[234:241], v[194:201], v[34:37], v205, v205 op_sel_hi:[0,0,0]
	v_mfma_scale_f32_16x16x128_f8f6f4 v[26:29], v[226:233], v[218:225], v[26:29], v205, v205 op_sel_hi:[0,0,0]
	v_mfma_scale_f32_16x16x128_f8f6f4 v[18:21], v[234:241], v[218:225], v[18:21], v205, v205 op_sel_hi:[0,0,0]
	s_barrier
	ds_read_b128 v[10:13], v172
	ds_read_b128 v[14:17], v172 offset:1024
	ds_read_b128 v[160:163], v172 offset:2048
	ds_read_b128 v[164:167], v172 offset:3072
	s_add_u32 s70, s70, 0x20000
	s_addc_u32 s71, s71, 0
	s_mov_b32 m0, s43
	v_lshl_add_u64 v[174:175], s[70:71], 0, v[152:153]
	ds_read_b128 v[178:181], v170 offset:32768
	ds_read_b128 v[182:185], v170 offset:33792
	ds_read_b128 v[186:189], v170 offset:34816
	ds_read_b128 v[190:193], v170 offset:35840
	ds_read_b128 v[194:197], v170 offset:36864
	ds_read_b128 v[198:201], v170 offset:37888
	ds_read_b128 v[218:221], v170 offset:38912
	ds_read_b128 v[222:225], v170 offset:39936
	global_load_lds_dwordx4 v[174:175], off
	v_lshl_add_u64 v[174:175], s[70:71], 0, v[148:149]
	s_mov_b32 m0, s44
	s_nop 0
	global_load_lds_dwordx4 v[174:175], off
	s_waitcnt lgkmcnt(8)
	s_waitcnt vmcnt(10)
	s_barrier
	s_waitcnt lgkmcnt(6)
	v_mfma_scale_f32_16x16x128_f8f6f4 v[136:139], v[10:17], v[178:185], v[136:139], v205, v205 op_sel_hi:[0,0,0]
	v_mfma_scale_f32_16x16x128_f8f6f4 v[132:135], v[160:167], v[178:185], v[132:135], v205, v205 op_sel_hi:[0,0,0]
	s_waitcnt lgkmcnt(4)
	v_mfma_scale_f32_16x16x128_f8f6f4 v[118:121], v[10:17], v[186:193], v[118:121], v205, v205 op_sel_hi:[0,0,0]
	v_mfma_scale_f32_16x16x128_f8f6f4 v[114:117], v[160:167], v[186:193], v[114:117], v205, v205 op_sel_hi:[0,0,0]
	s_waitcnt lgkmcnt(2)
	v_mfma_scale_f32_16x16x128_f8f6f4 v[106:109], v[10:17], v[194:201], v[106:109], v205, v205 op_sel_hi:[0,0,0]
	v_mfma_scale_f32_16x16x128_f8f6f4 v[98:101], v[160:167], v[194:201], v[98:101], v205, v205 op_sel_hi:[0,0,0]
	s_waitcnt lgkmcnt(0)
	v_mfma_scale_f32_16x16x128_f8f6f4 v[86:89], v[10:17], v[218:225], v[86:89], v205, v205 op_sel_hi:[0,0,0]
	v_mfma_scale_f32_16x16x128_f8f6f4 v[70:73], v[160:167], v[218:225], v[70:73], v205, v205 op_sel_hi:[0,0,0]
	s_barrier
	s_mov_b32 m0, s62
	v_lshl_add_u64 v[6:7], v[6:7], 0, s[30:31]
	ds_read_b128 v[226:229], v173
	ds_read_b128 v[230:233], v173 offset:1024
	ds_read_b128 v[234:237], v173 offset:2048
	ds_read_b128 v[238:241], v173 offset:3072
	global_load_lds_dwordx4 v[6:7], off
	v_lshl_add_u64 v[6:7], v[8:9], 0, s[30:31]
	s_mov_b32 m0, s63
	s_nop 0
	global_load_lds_dwordx4 v[6:7], off
	s_waitcnt vmcnt(10)
	s_barrier
	s_waitcnt lgkmcnt(2)
	v_mfma_scale_f32_16x16x128_f8f6f4 v[144:147], v[226:233], v[178:185], v[144:147], v205, v205 op_sel_hi:[0,0,0]
	s_waitcnt lgkmcnt(0)
	v_mfma_scale_f32_16x16x128_f8f6f4 v[140:143], v[234:241], v[178:185], v[140:143], v205, v205 op_sel_hi:[0,0,0]
	v_mfma_scale_f32_16x16x128_f8f6f4 v[126:129], v[226:233], v[186:193], v[126:129], v205, v205 op_sel_hi:[0,0,0]
	v_mfma_scale_f32_16x16x128_f8f6f4 v[122:125], v[234:241], v[186:193], v[122:125], v205, v205 op_sel_hi:[0,0,0]
	v_mfma_scale_f32_16x16x128_f8f6f4 v[110:113], v[226:233], v[194:201], v[110:113], v205, v205 op_sel_hi:[0,0,0]
	v_mfma_scale_f32_16x16x128_f8f6f4 v[102:105], v[234:241], v[194:201], v[102:105], v205, v205 op_sel_hi:[0,0,0]
	v_mfma_scale_f32_16x16x128_f8f6f4 v[94:97], v[226:233], v[218:225], v[94:97], v205, v205 op_sel_hi:[0,0,0]
	v_mfma_scale_f32_16x16x128_f8f6f4 v[78:81], v[234:241], v[218:225], v[78:81], v205, v205 op_sel_hi:[0,0,0]
	s_mov_b32 m0, s45
	v_lshl_add_u64 v[2:3], v[2:3], 0, s[30:31]
	s_barrier
	ds_read_b128 v[178:181], v170 offset:49152
	ds_read_b128 v[182:185], v170 offset:50176
	ds_read_b128 v[186:189], v170 offset:51200
	ds_read_b128 v[190:193], v170 offset:52224
	ds_read_b128 v[194:197], v170 offset:53248
	ds_read_b128 v[198:201], v170 offset:54272
	ds_read_b128 v[218:221], v170 offset:55296
	ds_read_b128 v[222:225], v170 offset:56320
	global_load_lds_dwordx4 v[2:3], off
	v_lshl_add_u64 v[2:3], v[4:5], 0, s[30:31]
	s_mov_b32 m0, s46
	s_nop 0
	global_load_lds_dwordx4 v[2:3], off
	s_barrier
	s_waitcnt lgkmcnt(6)
	v_mfma_scale_f32_16x16x128_f8f6f4 v[82:85], v[10:17], v[178:185], v[82:85], v205, v205 op_sel_hi:[0,0,0]
	v_mfma_scale_f32_16x16x128_f8f6f4 v[66:69], v[160:167], v[178:185], v[66:69], v205, v205 op_sel_hi:[0,0,0]
	s_waitcnt lgkmcnt(4)
	v_mfma_scale_f32_16x16x128_f8f6f4 v[58:61], v[10:17], v[186:193], v[58:61], v205, v205 op_sel_hi:[0,0,0]
	v_mfma_scale_f32_16x16x128_f8f6f4 v[50:53], v[160:167], v[186:193], v[50:53], v205, v205 op_sel_hi:[0,0,0]
	s_waitcnt lgkmcnt(2)
	v_mfma_scale_f32_16x16x128_f8f6f4 v[46:49], v[10:17], v[194:201], v[46:49], v205, v205 op_sel_hi:[0,0,0]
	v_mfma_scale_f32_16x16x128_f8f6f4 v[38:41], v[160:167], v[194:201], v[38:41], v205, v205 op_sel_hi:[0,0,0]
	s_waitcnt lgkmcnt(0)
	v_mfma_scale_f32_16x16x128_f8f6f4 v[30:33], v[10:17], v[218:225], v[30:33], v205, v205 op_sel_hi:[0,0,0]
	v_mfma_scale_f32_16x16x128_f8f6f4 v[22:25], v[160:167], v[218:225], v[22:25], v205, v205 op_sel_hi:[0,0,0]
	s_barrier
	s_add_u32 s68, s68, 0x2080
	s_addc_u32 s69, s69, 0
	s_mov_b32 m0, s72
	v_lshl_add_u64 v[2:3], s[68:69], 0, v[154:155]
	global_load_lds_dwordx4 v[2:3], off
	v_lshl_add_u64 v[2:3], s[68:69], 0, v[150:151]
	s_mov_b32 m0, s73
	s_nop 0
	global_load_lds_dwordx4 v[2:3], off
	s_waitcnt vmcnt(10)
	s_barrier
	v_mfma_scale_f32_16x16x128_f8f6f4 v[90:93], v[226:233], v[178:185], v[90:93], v205, v205 op_sel_hi:[0,0,0]
	v_mfma_scale_f32_16x16x128_f8f6f4 v[74:77], v[234:241], v[178:185], v[74:77], v205, v205 op_sel_hi:[0,0,0]
	v_mfma_scale_f32_16x16x128_f8f6f4 v[62:65], v[226:233], v[186:193], v[62:65], v205, v205 op_sel_hi:[0,0,0]
	v_mfma_scale_f32_16x16x128_f8f6f4 v[54:57], v[234:241], v[186:193], v[54:57], v205, v205 op_sel_hi:[0,0,0]
	v_mfma_scale_f32_16x16x128_f8f6f4 v[42:45], v[226:233], v[194:201], v[42:45], v205, v205 op_sel_hi:[0,0,0]
	v_mfma_scale_f32_16x16x128_f8f6f4 v[34:37], v[234:241], v[194:201], v[34:37], v205, v205 op_sel_hi:[0,0,0]
	v_mfma_scale_f32_16x16x128_f8f6f4 v[26:29], v[226:233], v[218:225], v[26:29], v205, v205 op_sel_hi:[0,0,0]
	v_mfma_scale_f32_16x16x128_f8f6f4 v[18:21], v[234:241], v[218:225], v[18:21], v205, v205 op_sel_hi:[0,0,0]
	s_add_i32 s76, s76, 2
	s_add_u32 s66, s66, 0x100
	s_addc_u32 s67, s67, 0
	s_add_u32 s74, s74, 0x100
	s_addc_u32 s75, s75, 0
	s_cmp_gt_u32 s76, 5
	s_barrier
	s_cbranch_scc0 .LBB0_419
	v_mul_f32_e32 v4, 0xbcb8aa3b, v136
	v_mul_f32_e32 v5, 0xbcb8aa3b, v137
	v_exp_f32_e32 v4, v4
	v_exp_f32_e32 v5, v5
	v_mul_f32_e32 v6, 0xbcb8aa3b, v138
	v_mul_f32_e32 v7, 0xbcb8aa3b, v139
	v_exp_f32_e32 v6, v6
	v_exp_f32_e32 v7, v7
	v_med3_f32 v8, v4, s26, v209
	v_med3_f32 v5, v5, s26, v209
	v_mov_b32_e32 v4, v131
	v_cvt_pk_fp8_f32 v4, v8, v5
	v_med3_f32 v5, v6, s26, v209
	v_med3_f32 v6, v7, s26, v209
	v_mul_f32_e32 v7, 0xbcb8aa3b, v134
	v_cvt_pk_fp8_f32 v4, v5, v6 op_sel:[0,0,1]
	v_mul_f32_e32 v5, 0xbcb8aa3b, v132
	v_mul_f32_e32 v6, 0xbcb8aa3b, v133
	v_exp_f32_e32 v5, v5
	v_exp_f32_e32 v6, v6
	v_mul_f32_e32 v8, 0xbcb8aa3b, v135
	v_exp_f32_e32 v7, v7
	v_exp_f32_e32 v8, v8
	v_med3_f32 v9, v5, s26, v209
	v_med3_f32 v6, v6, s26, v209
	v_mov_b32_e32 v5, v131
	v_cvt_pk_fp8_f32 v5, v9, v6
	v_med3_f32 v6, v7, s26, v209
	v_med3_f32 v7, v8, s26, v209
	v_mul_f32_e32 v8, 0xbcb8aa3b, v146
	v_cvt_pk_fp8_f32 v5, v6, v7 op_sel:[0,0,1]
	v_mul_f32_e32 v6, 0xbcb8aa3b, v144
	v_mul_f32_e32 v7, 0xbcb8aa3b, v145
	v_exp_f32_e32 v6, v6
	v_exp_f32_e32 v7, v7
	v_mul_f32_e32 v9, 0xbcb8aa3b, v147
	v_exp_f32_e32 v8, v8
	v_exp_f32_e32 v9, v9
	v_med3_f32 v10, v6, s26, v209
	v_med3_f32 v7, v7, s26, v209
	v_mov_b32_e32 v6, v131
	v_cvt_pk_fp8_f32 v6, v10, v7
	v_med3_f32 v7, v8, s26, v209
	v_med3_f32 v8, v9, s26, v209
	v_mul_f32_e32 v9, 0xbcb8aa3b, v142
	v_cvt_pk_fp8_f32 v6, v7, v8 op_sel:[0,0,1]
	v_mul_f32_e32 v7, 0xbcb8aa3b, v140
	v_mul_f32_e32 v8, 0xbcb8aa3b, v141
	v_exp_f32_e32 v7, v7
	v_exp_f32_e32 v8, v8
	v_mul_f32_e32 v10, 0xbcb8aa3b, v143
	v_exp_f32_e32 v9, v9
	v_exp_f32_e32 v10, v10
	v_med3_f32 v11, v7, s26, v209
	v_med3_f32 v8, v8, s26, v209
	v_mov_b32_e32 v7, v131
	v_cvt_pk_fp8_f32 v7, v11, v8
	s_lshl_b32 s9, s16, 8
	s_mul_i32 s16, s16, 0x1e0000
	s_mul_hi_i32 s9, s9, 0x1e00
	s_add_u32 s16, s53, s16
	v_med3_f32 v8, v9, s26, v209
	v_med3_f32 v9, v10, s26, v209
	s_addc_u32 s9, s57, s9
	s_lshl_b32 s17, s17, 8
	v_cvt_pk_fp8_f32 v7, v8, v9 op_sel:[0,0,1]
	s_ashr_i32 s18, s17, 31
	s_add_u32 s16, s16, s17
	s_addc_u32 s17, s9, s18
	v_mov_b32_e32 v130, v169
	s_nop 15
	s_nop 15
	global_store_dwordx4 v130, v[4:7], s[16:17] offset:1536 nt
	v_lshl_add_u64 v[2:3], s[16:17], 0, v[130:131]
	s_mov_b32 s9, 0x1e000
	v_mul_f32_e32 v4, 0xbcb8aa3b, v118
	v_mul_f32_e32 v5, 0xbcb8aa3b, v119
	v_exp_f32_e32 v4, v4
	v_exp_f32_e32 v5, v5
	v_mul_f32_e32 v6, 0xbcb8aa3b, v120
	v_mul_f32_e32 v7, 0xbcb8aa3b, v121
	v_exp_f32_e32 v6, v6
	v_exp_f32_e32 v7, v7
	v_med3_f32 v8, v4, s26, v209
	v_med3_f32 v5, v5, s26, v209
	v_mov_b32_e32 v4, v131
	v_cvt_pk_fp8_f32 v4, v8, v5
	v_med3_f32 v5, v6, s26, v209
	v_med3_f32 v6, v7, s26, v209
	v_mul_f32_e32 v7, 0xbcb8aa3b, v116
	v_cvt_pk_fp8_f32 v4, v5, v6 op_sel:[0,0,1]
	v_mul_f32_e32 v5, 0xbcb8aa3b, v114
	v_mul_f32_e32 v6, 0xbcb8aa3b, v115
	v_exp_f32_e32 v5, v5
	v_exp_f32_e32 v6, v6
	v_mul_f32_e32 v8, 0xbcb8aa3b, v117
	v_exp_f32_e32 v7, v7
	v_exp_f32_e32 v8, v8
	v_med3_f32 v9, v5, s26, v209
	v_med3_f32 v6, v6, s26, v209
	v_mov_b32_e32 v5, v131
	v_cvt_pk_fp8_f32 v5, v9, v6
	v_med3_f32 v6, v7, s26, v209
	v_med3_f32 v7, v8, s26, v209
	v_mul_f32_e32 v8, 0xbcb8aa3b, v128
	v_cvt_pk_fp8_f32 v5, v6, v7 op_sel:[0,0,1]
	v_mul_f32_e32 v6, 0xbcb8aa3b, v126
	v_mul_f32_e32 v7, 0xbcb8aa3b, v127
	v_exp_f32_e32 v6, v6
	v_exp_f32_e32 v7, v7
	v_mul_f32_e32 v9, 0xbcb8aa3b, v129
	v_exp_f32_e32 v8, v8
	v_exp_f32_e32 v9, v9
	v_med3_f32 v10, v6, s26, v209
	v_med3_f32 v7, v7, s26, v209
	v_mov_b32_e32 v6, v131
	v_cvt_pk_fp8_f32 v6, v10, v7
	v_med3_f32 v7, v8, s26, v209
	v_med3_f32 v8, v9, s26, v209
	v_mul_f32_e32 v9, 0xbcb8aa3b, v124
	v_cvt_pk_fp8_f32 v6, v7, v8 op_sel:[0,0,1]
	v_mul_f32_e32 v7, 0xbcb8aa3b, v122
	v_mul_f32_e32 v8, 0xbcb8aa3b, v123
	v_exp_f32_e32 v7, v7
	v_exp_f32_e32 v8, v8
	v_mul_f32_e32 v10, 0xbcb8aa3b, v125
	v_exp_f32_e32 v9, v9
	v_exp_f32_e32 v10, v10
	v_med3_f32 v11, v7, s26, v209
	v_med3_f32 v8, v8, s26, v209
	v_mov_b32_e32 v7, v131
	v_cvt_pk_fp8_f32 v7, v11, v8
	v_med3_f32 v8, v9, s26, v209
	v_med3_f32 v9, v10, s26, v209
	s_mov_b32 s16, s8
	v_cvt_pk_fp8_f32 v7, v8, v9 op_sel:[0,0,1]
	v_add_co_u32_e32 v8, vcc, s9, v2
	s_mov_b32 s9, 0x3c000
	s_nop 0
	v_addc_co_u32_e32 v9, vcc, 0, v3, vcc
	global_store_dwordx4 v[8:9], v[4:7], off offset:1536 nt
	s_mov_b32 s17, s50
	s_mov_b64 s[68:69], s[10:11]
	v_mul_f32_e32 v4, 0xbcb8aa3b, v106
	v_mul_f32_e32 v5, 0xbcb8aa3b, v107
	v_exp_f32_e32 v4, v4
	v_exp_f32_e32 v5, v5
	v_mul_f32_e32 v6, 0xbcb8aa3b, v108
	v_mul_f32_e32 v7, 0xbcb8aa3b, v109
	v_exp_f32_e32 v6, v6
	v_exp_f32_e32 v7, v7
	v_med3_f32 v8, v4, s26, v209
	v_med3_f32 v5, v5, s26, v209
	v_mov_b32_e32 v4, v131
	v_cvt_pk_fp8_f32 v4, v8, v5
	v_med3_f32 v5, v6, s26, v209
	v_med3_f32 v6, v7, s26, v209
	v_mul_f32_e32 v7, 0xbcb8aa3b, v100
	v_cvt_pk_fp8_f32 v4, v5, v6 op_sel:[0,0,1]
	v_mul_f32_e32 v5, 0xbcb8aa3b, v98
	v_mul_f32_e32 v6, 0xbcb8aa3b, v99
	v_exp_f32_e32 v5, v5
	v_exp_f32_e32 v6, v6
	v_mul_f32_e32 v8, 0xbcb8aa3b, v101
	v_exp_f32_e32 v7, v7
	v_exp_f32_e32 v8, v8
	v_med3_f32 v9, v5, s26, v209
	v_med3_f32 v6, v6, s26, v209
	v_mov_b32_e32 v5, v131
	v_cvt_pk_fp8_f32 v5, v9, v6
	v_med3_f32 v6, v7, s26, v209
	v_med3_f32 v7, v8, s26, v209
	v_mul_f32_e32 v8, 0xbcb8aa3b, v112
	v_cvt_pk_fp8_f32 v5, v6, v7 op_sel:[0,0,1]
	v_mul_f32_e32 v6, 0xbcb8aa3b, v110
	v_mul_f32_e32 v7, 0xbcb8aa3b, v111
	v_exp_f32_e32 v6, v6
	v_exp_f32_e32 v7, v7
	v_mul_f32_e32 v9, 0xbcb8aa3b, v113
	v_exp_f32_e32 v8, v8
	v_exp_f32_e32 v9, v9
	v_med3_f32 v10, v6, s26, v209
	v_med3_f32 v7, v7, s26, v209
	v_mov_b32_e32 v6, v131
	v_cvt_pk_fp8_f32 v6, v10, v7
	v_med3_f32 v7, v8, s26, v209
	v_med3_f32 v8, v9, s26, v209
	v_mul_f32_e32 v9, 0xbcb8aa3b, v104
	v_cvt_pk_fp8_f32 v6, v7, v8 op_sel:[0,0,1]
	v_mul_f32_e32 v7, 0xbcb8aa3b, v102
	v_mul_f32_e32 v8, 0xbcb8aa3b, v103
	v_exp_f32_e32 v7, v7
	v_exp_f32_e32 v8, v8
	v_mul_f32_e32 v10, 0xbcb8aa3b, v105
	v_exp_f32_e32 v9, v9
	v_exp_f32_e32 v10, v10
	v_med3_f32 v11, v7, s26, v209
	v_med3_f32 v8, v8, s26, v209
	v_mov_b32_e32 v7, v131
	v_cvt_pk_fp8_f32 v7, v11, v8
	v_med3_f32 v8, v9, s26, v209
	v_med3_f32 v9, v10, s26, v209
	s_mov_b64 s[66:67], s[14:15]
	v_cvt_pk_fp8_f32 v7, v8, v9 op_sel:[0,0,1]
	v_add_co_u32_e32 v8, vcc, s9, v2
	s_mov_b32 s9, 0x5a000
	s_nop 0
	v_addc_co_u32_e32 v9, vcc, 0, v3, vcc
	global_store_dwordx4 v[8:9], v[4:7], off offset:1536 nt
	s_nop 1
	v_mul_f32_e32 v4, 0xbcb8aa3b, v86
	v_mul_f32_e32 v5, 0xbcb8aa3b, v87
	v_exp_f32_e32 v4, v4
	v_exp_f32_e32 v5, v5
	v_mul_f32_e32 v6, 0xbcb8aa3b, v88
	v_mul_f32_e32 v7, 0xbcb8aa3b, v89
	v_exp_f32_e32 v6, v6
	v_exp_f32_e32 v7, v7
	v_med3_f32 v8, v4, s26, v209
	v_med3_f32 v5, v5, s26, v209
	v_mov_b32_e32 v4, v131
	v_cvt_pk_fp8_f32 v4, v8, v5
	v_med3_f32 v5, v6, s26, v209
	v_med3_f32 v6, v7, s26, v209
	v_mul_f32_e32 v7, 0xbcb8aa3b, v72
	v_cvt_pk_fp8_f32 v4, v5, v6 op_sel:[0,0,1]
	v_mul_f32_e32 v5, 0xbcb8aa3b, v70
	v_mul_f32_e32 v6, 0xbcb8aa3b, v71
	v_exp_f32_e32 v5, v5
	v_exp_f32_e32 v6, v6
	v_mul_f32_e32 v8, 0xbcb8aa3b, v73
	v_exp_f32_e32 v7, v7
	v_exp_f32_e32 v8, v8
	v_med3_f32 v9, v5, s26, v209
	v_med3_f32 v6, v6, s26, v209
	v_mov_b32_e32 v5, v131
	v_cvt_pk_fp8_f32 v5, v9, v6
	v_med3_f32 v6, v7, s26, v209
	v_med3_f32 v7, v8, s26, v209
	v_mul_f32_e32 v8, 0xbcb8aa3b, v96
	v_cvt_pk_fp8_f32 v5, v6, v7 op_sel:[0,0,1]
	v_mul_f32_e32 v6, 0xbcb8aa3b, v94
	v_mul_f32_e32 v7, 0xbcb8aa3b, v95
	v_exp_f32_e32 v6, v6
	v_exp_f32_e32 v7, v7
	v_mul_f32_e32 v9, 0xbcb8aa3b, v97
	v_exp_f32_e32 v8, v8
	v_exp_f32_e32 v9, v9
	v_med3_f32 v10, v6, s26, v209
	v_med3_f32 v7, v7, s26, v209
	v_mov_b32_e32 v6, v131
	v_cvt_pk_fp8_f32 v6, v10, v7
	v_med3_f32 v7, v8, s26, v209
	v_med3_f32 v8, v9, s26, v209
	v_mul_f32_e32 v9, 0xbcb8aa3b, v80
	v_cvt_pk_fp8_f32 v6, v7, v8 op_sel:[0,0,1]
	v_mul_f32_e32 v7, 0xbcb8aa3b, v78
	v_mul_f32_e32 v8, 0xbcb8aa3b, v79
	v_exp_f32_e32 v7, v7
	v_exp_f32_e32 v8, v8
	v_mul_f32_e32 v10, 0xbcb8aa3b, v81
	v_exp_f32_e32 v9, v9
	v_exp_f32_e32 v10, v10
	v_med3_f32 v11, v7, s26, v209
	v_med3_f32 v8, v8, s26, v209
	v_mov_b32_e32 v7, v131
	v_cvt_pk_fp8_f32 v7, v11, v8
	v_med3_f32 v8, v9, s26, v209
	v_med3_f32 v9, v10, s26, v209
	v_cvt_pk_fp8_f32 v7, v8, v9 op_sel:[0,0,1]
	v_add_co_u32_e32 v8, vcc, s9, v2
	s_mov_b32 s9, 0xf0000
	s_nop 0
	v_addc_co_u32_e32 v9, vcc, 0, v3, vcc
	global_store_dwordx4 v[8:9], v[4:7], off offset:1536 nt
	s_nop 1
	v_mul_f32_e32 v4, 0xbcb8aa3b, v82
	v_mul_f32_e32 v5, 0xbcb8aa3b, v83
	v_exp_f32_e32 v4, v4
	v_exp_f32_e32 v5, v5
	v_mul_f32_e32 v6, 0xbcb8aa3b, v84
	v_mul_f32_e32 v7, 0xbcb8aa3b, v85
	v_exp_f32_e32 v6, v6
	v_exp_f32_e32 v7, v7
	v_med3_f32 v8, v4, s26, v209
	v_med3_f32 v5, v5, s26, v209
	v_mov_b32_e32 v4, v131
	v_cvt_pk_fp8_f32 v4, v8, v5
	v_med3_f32 v5, v6, s26, v209
	v_med3_f32 v6, v7, s26, v209
	v_mul_f32_e32 v7, 0xbcb8aa3b, v68
	v_cvt_pk_fp8_f32 v4, v5, v6 op_sel:[0,0,1]
	v_mul_f32_e32 v5, 0xbcb8aa3b, v66
	v_mul_f32_e32 v6, 0xbcb8aa3b, v67
	v_exp_f32_e32 v5, v5
	v_exp_f32_e32 v6, v6
	v_mul_f32_e32 v8, 0xbcb8aa3b, v69
	v_exp_f32_e32 v7, v7
	v_exp_f32_e32 v8, v8
	v_med3_f32 v9, v5, s26, v209
	v_med3_f32 v6, v6, s26, v209
	v_mov_b32_e32 v5, v131
	v_cvt_pk_fp8_f32 v5, v9, v6
	v_med3_f32 v6, v7, s26, v209
	v_med3_f32 v7, v8, s26, v209
	v_mul_f32_e32 v8, 0xbcb8aa3b, v92
	v_cvt_pk_fp8_f32 v5, v6, v7 op_sel:[0,0,1]
	v_mul_f32_e32 v6, 0xbcb8aa3b, v90
	v_mul_f32_e32 v7, 0xbcb8aa3b, v91
	v_exp_f32_e32 v6, v6
	v_exp_f32_e32 v7, v7
	v_mul_f32_e32 v9, 0xbcb8aa3b, v93
	v_exp_f32_e32 v8, v8
	v_exp_f32_e32 v9, v9
	v_med3_f32 v10, v6, s26, v209
	v_med3_f32 v7, v7, s26, v209
	v_mov_b32_e32 v6, v131
	v_cvt_pk_fp8_f32 v6, v10, v7
	v_med3_f32 v7, v8, s26, v209
	v_med3_f32 v8, v9, s26, v209
	v_mul_f32_e32 v9, 0xbcb8aa3b, v76
	v_cvt_pk_fp8_f32 v6, v7, v8 op_sel:[0,0,1]
	v_mul_f32_e32 v7, 0xbcb8aa3b, v74
	v_mul_f32_e32 v8, 0xbcb8aa3b, v75
	v_exp_f32_e32 v7, v7
	v_exp_f32_e32 v8, v8
	v_mul_f32_e32 v10, 0xbcb8aa3b, v77
	v_exp_f32_e32 v9, v9
	v_exp_f32_e32 v10, v10
	v_med3_f32 v11, v7, s26, v209
	v_med3_f32 v8, v8, s26, v209
	v_mov_b32_e32 v7, v131
	v_cvt_pk_fp8_f32 v7, v11, v8
	v_med3_f32 v8, v9, s26, v209
	v_med3_f32 v9, v10, s26, v209
	v_cvt_pk_fp8_f32 v7, v8, v9 op_sel:[0,0,1]
	v_add_co_u32_e32 v8, vcc, s9, v2
	s_mov_b32 s9, 0x10e000
	s_nop 0
	v_addc_co_u32_e32 v9, vcc, 0, v3, vcc
	global_store_dwordx4 v[8:9], v[4:7], off offset:1536 nt
	s_nop 1
	v_mul_f32_e32 v4, 0xbcb8aa3b, v58
	v_mul_f32_e32 v5, 0xbcb8aa3b, v59
	v_exp_f32_e32 v4, v4
	v_exp_f32_e32 v5, v5
	v_mul_f32_e32 v6, 0xbcb8aa3b, v60
	v_mul_f32_e32 v7, 0xbcb8aa3b, v61
	v_exp_f32_e32 v6, v6
	v_exp_f32_e32 v7, v7
	v_med3_f32 v8, v4, s26, v209
	v_med3_f32 v5, v5, s26, v209
	v_mov_b32_e32 v4, v131
	v_cvt_pk_fp8_f32 v4, v8, v5
	v_med3_f32 v5, v6, s26, v209
	v_med3_f32 v6, v7, s26, v209
	v_mul_f32_e32 v7, 0xbcb8aa3b, v52
	v_cvt_pk_fp8_f32 v4, v5, v6 op_sel:[0,0,1]
	v_mul_f32_e32 v5, 0xbcb8aa3b, v50
	v_mul_f32_e32 v6, 0xbcb8aa3b, v51
	v_exp_f32_e32 v5, v5
	v_exp_f32_e32 v6, v6
	v_mul_f32_e32 v8, 0xbcb8aa3b, v53
	v_exp_f32_e32 v7, v7
	v_exp_f32_e32 v8, v8
	v_med3_f32 v9, v5, s26, v209
	v_med3_f32 v6, v6, s26, v209
	v_mov_b32_e32 v5, v131
	v_cvt_pk_fp8_f32 v5, v9, v6
	v_med3_f32 v6, v7, s26, v209
	v_med3_f32 v7, v8, s26, v209
	v_mul_f32_e32 v8, 0xbcb8aa3b, v64
	v_cvt_pk_fp8_f32 v5, v6, v7 op_sel:[0,0,1]
	v_mul_f32_e32 v6, 0xbcb8aa3b, v62
	v_mul_f32_e32 v7, 0xbcb8aa3b, v63
	v_exp_f32_e32 v6, v6
	v_exp_f32_e32 v7, v7
	v_mul_f32_e32 v9, 0xbcb8aa3b, v65
	v_exp_f32_e32 v8, v8
	v_exp_f32_e32 v9, v9
	v_med3_f32 v10, v6, s26, v209
	v_med3_f32 v7, v7, s26, v209
	v_mov_b32_e32 v6, v131
	v_cvt_pk_fp8_f32 v6, v10, v7
	v_med3_f32 v7, v8, s26, v209
	v_med3_f32 v8, v9, s26, v209
	v_mul_f32_e32 v9, 0xbcb8aa3b, v56
	v_cvt_pk_fp8_f32 v6, v7, v8 op_sel:[0,0,1]
	v_mul_f32_e32 v7, 0xbcb8aa3b, v54
	v_mul_f32_e32 v8, 0xbcb8aa3b, v55
	v_exp_f32_e32 v7, v7
	v_exp_f32_e32 v8, v8
	v_mul_f32_e32 v10, 0xbcb8aa3b, v57
	v_exp_f32_e32 v9, v9
	v_exp_f32_e32 v10, v10
	v_med3_f32 v11, v7, s26, v209
	v_med3_f32 v8, v8, s26, v209
	v_mov_b32_e32 v7, v131
	v_cvt_pk_fp8_f32 v7, v11, v8
	v_med3_f32 v8, v9, s26, v209
	v_med3_f32 v9, v10, s26, v209
	v_cvt_pk_fp8_f32 v7, v8, v9 op_sel:[0,0,1]
	v_add_co_u32_e32 v8, vcc, s9, v2
	s_mov_b32 s9, 0x12c000
	s_nop 0
	v_addc_co_u32_e32 v9, vcc, 0, v3, vcc
	global_store_dwordx4 v[8:9], v[4:7], off offset:1536 nt
	s_nop 1
	v_mul_f32_e32 v4, 0xbcb8aa3b, v46
	v_mul_f32_e32 v5, 0xbcb8aa3b, v47
	v_exp_f32_e32 v4, v4
	v_exp_f32_e32 v5, v5
	v_mul_f32_e32 v6, 0xbcb8aa3b, v48
	v_mul_f32_e32 v7, 0xbcb8aa3b, v49
	v_exp_f32_e32 v6, v6
	v_exp_f32_e32 v7, v7
	v_med3_f32 v8, v4, s26, v209
	v_med3_f32 v5, v5, s26, v209
	v_mov_b32_e32 v4, v131
	v_cvt_pk_fp8_f32 v4, v8, v5
	v_med3_f32 v5, v6, s26, v209
	v_med3_f32 v6, v7, s26, v209
	v_mul_f32_e32 v7, 0xbcb8aa3b, v40
	v_cvt_pk_fp8_f32 v4, v5, v6 op_sel:[0,0,1]
	v_mul_f32_e32 v5, 0xbcb8aa3b, v38
	v_mul_f32_e32 v6, 0xbcb8aa3b, v39
	v_exp_f32_e32 v5, v5
	v_exp_f32_e32 v6, v6
	v_mul_f32_e32 v8, 0xbcb8aa3b, v41
	v_exp_f32_e32 v7, v7
	v_exp_f32_e32 v8, v8
	v_med3_f32 v9, v5, s26, v209
	v_med3_f32 v6, v6, s26, v209
	v_mov_b32_e32 v5, v131
	v_cvt_pk_fp8_f32 v5, v9, v6
	v_med3_f32 v6, v7, s26, v209
	v_med3_f32 v7, v8, s26, v209
	v_mul_f32_e32 v8, 0xbcb8aa3b, v44
	v_cvt_pk_fp8_f32 v5, v6, v7 op_sel:[0,0,1]
	v_mul_f32_e32 v6, 0xbcb8aa3b, v42
	v_mul_f32_e32 v7, 0xbcb8aa3b, v43
	v_exp_f32_e32 v6, v6
	v_exp_f32_e32 v7, v7
	v_mul_f32_e32 v9, 0xbcb8aa3b, v45
	v_exp_f32_e32 v8, v8
	v_exp_f32_e32 v9, v9
	v_med3_f32 v10, v6, s26, v209
	v_med3_f32 v7, v7, s26, v209
	v_mov_b32_e32 v6, v131
	v_cvt_pk_fp8_f32 v6, v10, v7
	v_med3_f32 v7, v8, s26, v209
	v_med3_f32 v8, v9, s26, v209
	v_mul_f32_e32 v9, 0xbcb8aa3b, v36
	v_cvt_pk_fp8_f32 v6, v7, v8 op_sel:[0,0,1]
	v_mul_f32_e32 v7, 0xbcb8aa3b, v34
	v_mul_f32_e32 v8, 0xbcb8aa3b, v35
	v_exp_f32_e32 v7, v7
	v_exp_f32_e32 v8, v8
	v_mul_f32_e32 v10, 0xbcb8aa3b, v37
	v_exp_f32_e32 v9, v9
	v_exp_f32_e32 v10, v10
	v_med3_f32 v11, v7, s26, v209
	v_med3_f32 v8, v8, s26, v209
	v_mov_b32_e32 v7, v131
	v_cvt_pk_fp8_f32 v7, v11, v8
	v_med3_f32 v8, v9, s26, v209
	v_med3_f32 v9, v10, s26, v209
	v_cvt_pk_fp8_f32 v7, v8, v9 op_sel:[0,0,1]
	v_add_co_u32_e32 v8, vcc, s9, v2
	s_nop 1
	v_addc_co_u32_e32 v9, vcc, 0, v3, vcc
	global_store_dwordx4 v[8:9], v[4:7], off offset:1536 nt
	v_add_co_u32_e32 v2, vcc, 0x14a000, v2
	s_nop 0
	v_mul_f32_e32 v4, 0xbcb8aa3b, v30
	v_mul_f32_e32 v5, 0xbcb8aa3b, v31
	v_exp_f32_e32 v4, v4
	v_exp_f32_e32 v5, v5
	v_mul_f32_e32 v6, 0xbcb8aa3b, v32
	v_mul_f32_e32 v7, 0xbcb8aa3b, v33
	v_exp_f32_e32 v6, v6
	v_exp_f32_e32 v7, v7
	v_med3_f32 v8, v4, s26, v209
	v_med3_f32 v5, v5, s26, v209
	v_mov_b32_e32 v4, v131
	v_cvt_pk_fp8_f32 v4, v8, v5
	v_med3_f32 v5, v6, s26, v209
	v_med3_f32 v6, v7, s26, v209
	v_mul_f32_e32 v7, 0xbcb8aa3b, v24
	v_cvt_pk_fp8_f32 v4, v5, v6 op_sel:[0,0,1]
	v_mul_f32_e32 v5, 0xbcb8aa3b, v22
	v_mul_f32_e32 v6, 0xbcb8aa3b, v23
	v_exp_f32_e32 v5, v5
	v_exp_f32_e32 v6, v6
	v_mul_f32_e32 v8, 0xbcb8aa3b, v25
	v_exp_f32_e32 v7, v7
	v_exp_f32_e32 v8, v8
	v_med3_f32 v9, v5, s26, v209
	v_med3_f32 v6, v6, s26, v209
	v_mov_b32_e32 v5, v131
	v_cvt_pk_fp8_f32 v5, v9, v6
	v_med3_f32 v6, v7, s26, v209
	v_med3_f32 v7, v8, s26, v209
	v_mul_f32_e32 v8, 0xbcb8aa3b, v28
	v_cvt_pk_fp8_f32 v5, v6, v7 op_sel:[0,0,1]
	v_mul_f32_e32 v6, 0xbcb8aa3b, v26
	v_mul_f32_e32 v7, 0xbcb8aa3b, v27
	v_exp_f32_e32 v6, v6
	v_exp_f32_e32 v7, v7
	v_mul_f32_e32 v9, 0xbcb8aa3b, v29
	v_exp_f32_e32 v8, v8
	v_exp_f32_e32 v9, v9
	v_med3_f32 v10, v6, s26, v209
	v_med3_f32 v7, v7, s26, v209
	v_mov_b32_e32 v6, v131
	v_cvt_pk_fp8_f32 v6, v10, v7
	v_med3_f32 v7, v8, s26, v209
	v_med3_f32 v8, v9, s26, v209
	v_mul_f32_e32 v9, 0xbcb8aa3b, v20
	v_cvt_pk_fp8_f32 v6, v7, v8 op_sel:[0,0,1]
	v_mul_f32_e32 v7, 0xbcb8aa3b, v18
	v_mul_f32_e32 v8, 0xbcb8aa3b, v19
	v_exp_f32_e32 v7, v7
	v_exp_f32_e32 v8, v8
	v_mul_f32_e32 v10, 0xbcb8aa3b, v21
	v_exp_f32_e32 v9, v9
	v_exp_f32_e32 v10, v10
	v_med3_f32 v11, v7, s26, v209
	v_med3_f32 v8, v8, s26, v209
	v_mov_b32_e32 v7, v131
	v_cvt_pk_fp8_f32 v7, v11, v8
	v_med3_f32 v8, v9, s26, v209
	v_med3_f32 v9, v10, s26, v209
	v_addc_co_u32_e32 v3, vcc, 0, v3, vcc
	v_cvt_pk_fp8_f32 v7, v8, v9 op_sel:[0,0,1]
	s_and_b64 vcc, exec, s[6:7]
	global_store_dwordx4 v[2:3], v[4:7], off offset:1536 nt
	s_cbranch_vccz .LBB0_416
	s_waitcnt vmcnt(0)
	s_setprio 0
	s_cmpk_gt_u32 s33, 0xff
	s_cbranch_scc1 .LBB0_423
	s_barrier

.LBB0_440:
	s_add_u32 s43, s12, 0x5c068000
	s_addc_u32 s44, s13, 0
	s_add_u32 s14, s12, 0x339a8000
	s_addc_u32 s15, s13, 0
	s_and_b32 s50, s16, 3
	s_add_i32 m0, s37, 0x18000
	v_lshl_add_u64 v[8:9], v[8:9], 0, s[30:31]
	s_lshl_b32 s16, s17, 13
	s_lshl_b32 s47, s50, 12
	s_waitcnt vmcnt(4)
	s_barrier
	v_readfirstlane_b32 s100, v0
	s_cmp_lt_u32 s100, 0x100
	s_cbranch_scc1 .Lmy_sp_g1a
	s_setprio 1
.Lmy_sp_g1a:
	global_load_lds_dwordx4 v[8:9], off
	v_lshl_add_u64 v[6:7], v[6:7], 0, s[30:31]
	s_add_i32 m0, s37, 0x1a000
	s_add_i32 s45, s37, 0x8000
	s_add_i32 s46, s37, 0xa000
	global_load_lds_dwordx4 v[6:7], off
	v_lshl_add_u64 v[4:5], v[4:5], 0, s[30:31]
	s_mov_b32 m0, s45
	s_add_u32 s18, s74, 0x2080
	global_load_lds_dwordx4 v[4:5], off
	v_lshl_add_u64 v[2:3], v[2:3], 0, s[30:31]
	s_mov_b32 m0, s46
	s_addc_u32 s19, s75, 0
	global_load_lds_dwordx4 v[2:3], off
	s_add_i32 m0, s37, 0x1c000
	v_lshl_add_u64 v[2:3], s[18:19], 0, v[148:149]
	global_load_lds_dwordx4 v[2:3], off
	v_lshl_add_u64 v[2:3], s[18:19], 0, v[152:153]
	s_add_i32 m0, s37, 0x1e000
	s_movk_i32 s18, 0xf00
	global_load_lds_dwordx4 v[2:3], off
	v_bfe_u32 v3, v10, 4, 2
	v_and_b32_e32 v2, 15, v10
	v_lshlrev_b32_e32 v158, 3, v3
	v_lshlrev_b32_e32 v160, 4, v3
	v_lshlrev_b32_e32 v3, 2, v10
	v_lshl_or_b32 v156, s17, 6, v2
	v_lshl_or_b32 v2, v2, 6, v160
	v_and_b32_e32 v3, 32, v3
	v_bitop3_b32 v4, v2, s16, v3 bitop3:0xde
	v_bitop3_b32 v157, v2, s47, v3 bitop3:0xde
	v_mul_lo_u32 v2, v156, s18
	v_or_b32_e32 v159, v2, v160
	v_lshlrev_b32_e32 v2, 13, v11
	s_cmp_gt_u32 s50, 1
	v_and_b32_e32 v2, 0xffffc000, v2
	s_cselect_b64 s[16:17], -1, 0
	s_lshl_b32 s47, s50, 6
	s_lshl_b32 s18, s50, 7
	v_lshl_add_u32 v2, v12, 10, v2
	v_and_b32_e32 v3, 1, v11
	s_add_u32 s19, s12, s18
	v_lshl_or_b32 v2, v3, 6, v2
	s_addc_u32 s51, s13, 0
	v_lshl_add_u32 v178, v14, 1, v2
	v_lshlrev_b32_e32 v2, 13, v13
	s_add_u32 s50, s19, 0x5e468000
	v_and_b32_e32 v2, 0xffffc000, v2
	s_waitcnt vmcnt(6)
	s_addc_u32 s51, s51, 0
	v_lshl_add_u32 v2, v15, 10, v2
	v_and_b32_e32 v3, 1, v13
	s_add_u32 s53, s53, s18
	v_lshl_or_b32 v2, v3, 6, v2
	v_or_b32_e32 v162, 16, v156
	v_or_b32_e32 v164, 32, v156
	v_or_b32_e32 v166, 48, v156
	v_add_u32_e32 v250, 0x80, v156
	v_add_u32_e32 v252, 0x90, v156
	v_add_u32_e32 v202, 0xa0, v156
	v_add_u32_e32 v210, 0xb0, v156
	s_addc_u32 s57, s57, 0
	v_mov_b32_e32 v179, v131
	v_lshl_add_u32 v180, v16, 1, v2
	v_mov_b32_e32 v181, v131
	s_mov_b32 s58, 0
	v_add_u32_e32 v161, 0, v4
	s_barrier
	s_branch .LBB0_442

.LBB0_456:
	s_xor_b64 s[72:73], s[76:77], -1
	s_and_b64 s[60:61], s[76:77], exec
	s_cselect_b32 s59, s19, s7
	s_cselect_b32 s60, s18, s6
	s_add_i32 s69, 0, 0x10000
	v_add_u32_e32 v130, s69, v157
	ds_read_b128 v[2:5], v130
	ds_read_b128 v[6:9], v130 offset:1024
	ds_read_b128 v[10:13], v130 offset:2048
	ds_read_b128 v[14:17], v130 offset:3072
	s_and_b64 s[62:63], s[76:77], exec
	s_cselect_b32 s61, s67, s75
	s_cselect_b32 s62, s66, s74
	s_add_u32 s64, s6, 0x20080
	s_addc_u32 s65, s7, 0
	s_add_i32 s63, s37, 0xc000
	v_lshl_add_u64 v[42:43], s[64:65], 0, v[150:151]
	s_mov_b32 m0, s63
	ds_read_b128 v[18:21], v161
	ds_read_b128 v[22:25], v161 offset:1024
	ds_read_b128 v[26:29], v161 offset:2048
	ds_read_b128 v[30:33], v161 offset:3072
	ds_read_b128 v[34:37], v161 offset:4096
	ds_read_b128 v[38:41], v161 offset:5120
	ds_read_b128 v[54:57], v161 offset:6144
	ds_read_b128 v[58:61], v161 offset:7168
	global_load_lds_dwordx4 v[42:43], off
	v_lshl_add_u64 v[42:43], s[64:65], 0, v[154:155]
	s_add_i32 s64, s37, 0xe000
	s_mov_b32 m0, s64
	s_nop 0
	global_load_lds_dwordx4 v[42:43], off
	s_waitcnt lgkmcnt(8)
	s_waitcnt vmcnt(10)
	s_barrier
	s_waitcnt lgkmcnt(6)
	v_mfma_scale_f32_16x16x128_f8f6f4 v[114:117], v[2:9], v[18:25], 0, v205, v205 op_sel_hi:[0,0,0]
	v_mfma_scale_f32_16x16x128_f8f6f4 v[126:129], v[10:17], v[18:25], 0, v205, v205 op_sel_hi:[0,0,0]
	s_waitcnt lgkmcnt(4)
	v_mfma_scale_f32_16x16x128_f8f6f4 v[102:105], v[2:9], v[26:33], 0, v205, v205 op_sel_hi:[0,0,0]
	v_mfma_scale_f32_16x16x128_f8f6f4 v[98:101], v[10:17], v[26:33], 0, v205, v205 op_sel_hi:[0,0,0]
	s_waitcnt lgkmcnt(2)
	v_mfma_scale_f32_16x16x128_f8f6f4 v[78:81], v[2:9], v[34:41], 0, v205, v205 op_sel_hi:[0,0,0]
	v_mfma_scale_f32_16x16x128_f8f6f4 v[70:73], v[10:17], v[34:41], 0, v205, v205 op_sel_hi:[0,0,0]
	s_waitcnt lgkmcnt(0)
	v_mfma_scale_f32_16x16x128_f8f6f4 v[50:53], v[2:9], v[54:61], 0, v205, v205 op_sel_hi:[0,0,0]
	v_mfma_scale_f32_16x16x128_f8f6f4 v[42:45], v[10:17], v[54:61], 0, v205, v205 op_sel_hi:[0,0,0]
	s_barrier
	s_add_i32 s71, 0, 0x14000
	v_lshl_add_u64 v[186:187], s[74:75], 0, v[148:149]
	s_mov_b64 s[76:77], 0x100
	s_add_i32 s65, s69, s36
	v_add_u32_e32 v163, s71, v157
	v_lshl_add_u64 v[46:47], v[186:187], 0, s[76:77]
	s_mov_b32 m0, s65
	v_lshl_add_u64 v[188:189], s[74:75], 0, v[152:153]
	s_add_i32 s69, s65, 0x2000
	ds_read_b128 v[190:193], v163
	ds_read_b128 v[194:197], v163 offset:1024
	ds_read_b128 v[218:221], v163 offset:2048
	ds_read_b128 v[222:225], v163 offset:3072
	global_load_lds_dwordx4 v[46:47], off
	v_lshl_add_u64 v[46:47], v[188:189], 0, s[76:77]
	s_mov_b32 m0, s69
	s_nop 0
	global_load_lds_dwordx4 v[46:47], off
	s_waitcnt vmcnt(10)
	s_barrier
	s_waitcnt lgkmcnt(2)
	v_mfma_scale_f32_16x16x128_f8f6f4 v[140:143], v[190:197], v[18:25], 0, v205, v205 op_sel_hi:[0,0,0]
	s_waitcnt lgkmcnt(0)
	v_mfma_scale_f32_16x16x128_f8f6f4 v[144:147], v[218:225], v[18:25], 0, v205, v205 op_sel_hi:[0,0,0]
	v_mfma_scale_f32_16x16x128_f8f6f4 v[136:139], v[190:197], v[26:33], 0, v205, v205 op_sel_hi:[0,0,0]
	v_mfma_scale_f32_16x16x128_f8f6f4 v[132:135], v[218:225], v[26:33], 0, v205, v205 op_sel_hi:[0,0,0]
	v_mfma_scale_f32_16x16x128_f8f6f4 v[110:113], v[190:197], v[34:41], 0, v205, v205 op_sel_hi:[0,0,0]
	v_mfma_scale_f32_16x16x128_f8f6f4 v[106:109], v[218:225], v[34:41], 0, v205, v205 op_sel_hi:[0,0,0]
	v_mfma_scale_f32_16x16x128_f8f6f4 v[74:77], v[190:197], v[54:61], 0, v205, v205 op_sel_hi:[0,0,0]
	v_mfma_scale_f32_16x16x128_f8f6f4 v[66:69], v[218:225], v[54:61], 0, v205, v205 op_sel_hi:[0,0,0]
	v_lshl_add_u64 v[182:183], s[6:7], 0, v[150:151]
	s_mov_b32 m0, s37
	v_lshl_add_u64 v[18:19], v[182:183], 0, s[76:77]
	v_lshl_add_u64 v[184:185], s[6:7], 0, v[154:155]
	s_barrier
	ds_read_b128 v[26:29], v161 offset:16384
	ds_read_b128 v[30:33], v161 offset:17408
	ds_read_b128 v[226:229], v161 offset:18432
	ds_read_b128 v[230:233], v161 offset:19456
	ds_read_b128 v[234:237], v161 offset:20480
	ds_read_b128 v[238:241], v161 offset:21504
	ds_read_b128 v[242:245], v161 offset:22528
	ds_read_b128 v[246:249], v161 offset:23552
	global_load_lds_dwordx4 v[18:19], off
	v_lshl_add_u64 v[18:19], v[184:185], 0, s[76:77]
	s_mov_b32 m0, s38
	s_nop 0
	global_load_lds_dwordx4 v[18:19], off
	s_barrier
	s_waitcnt lgkmcnt(6)
	v_mfma_scale_f32_16x16x128_f8f6f4 v[94:97], v[2:9], v[26:33], 0, v205, v205 op_sel_hi:[0,0,0]
	v_mfma_scale_f32_16x16x128_f8f6f4 v[90:93], v[10:17], v[26:33], 0, v205, v205 op_sel_hi:[0,0,0]
	s_waitcnt lgkmcnt(4)
	v_mfma_scale_f32_16x16x128_f8f6f4 v[62:65], v[2:9], v[226:233], 0, v205, v205 op_sel_hi:[0,0,0]
	v_mfma_scale_f32_16x16x128_f8f6f4 v[58:61], v[10:17], v[226:233], 0, v205, v205 op_sel_hi:[0,0,0]
	s_waitcnt lgkmcnt(2)
	v_mfma_scale_f32_16x16x128_f8f6f4 v[38:41], v[2:9], v[234:241], 0, v205, v205 op_sel_hi:[0,0,0]
	v_mfma_scale_f32_16x16x128_f8f6f4 v[34:37], v[10:17], v[234:241], 0, v205, v205 op_sel_hi:[0,0,0]
	s_waitcnt lgkmcnt(0)
	v_mfma_scale_f32_16x16x128_f8f6f4 v[22:25], v[2:9], v[242:249], 0, v205, v205 op_sel_hi:[0,0,0]
	v_mfma_scale_f32_16x16x128_f8f6f4 v[18:21], v[10:17], v[242:249], 0, v205, v205 op_sel_hi:[0,0,0]
	s_barrier
	s_add_u32 s76, s74, 0x2100
	s_addc_u32 s77, s75, 0
	s_add_i32 s71, s71, s36
	v_lshl_add_u64 v[2:3], s[76:77], 0, v[148:149]
	s_mov_b32 m0, s71
	s_add_i32 s79, s71, 0x2000
	global_load_lds_dwordx4 v[2:3], off
	v_lshl_add_u64 v[2:3], s[76:77], 0, v[152:153]
	s_mov_b32 m0, s79
	s_nop 0
	global_load_lds_dwordx4 v[2:3], off
	s_waitcnt vmcnt(10)
	s_barrier
	v_mfma_scale_f32_16x16x128_f8f6f4 v[122:125], v[190:197], v[26:33], 0, v205, v205 op_sel_hi:[0,0,0]
	v_mfma_scale_f32_16x16x128_f8f6f4 v[118:121], v[218:225], v[26:33], 0, v205, v205 op_sel_hi:[0,0,0]
	v_mfma_scale_f32_16x16x128_f8f6f4 v[86:89], v[190:197], v[226:233], 0, v205, v205 op_sel_hi:[0,0,0]
	v_mfma_scale_f32_16x16x128_f8f6f4 v[82:85], v[218:225], v[226:233], 0, v205, v205 op_sel_hi:[0,0,0]
	v_mfma_scale_f32_16x16x128_f8f6f4 v[54:57], v[190:197], v[234:241], 0, v205, v205 op_sel_hi:[0,0,0]
	v_mfma_scale_f32_16x16x128_f8f6f4 v[46:49], v[218:225], v[234:241], 0, v205, v205 op_sel_hi:[0,0,0]
	v_mfma_scale_f32_16x16x128_f8f6f4 v[30:33], v[190:197], v[242:249], 0, v205, v205 op_sel_hi:[0,0,0]
	v_mfma_scale_f32_16x16x128_f8f6f4 v[26:29], v[218:225], v[242:249], 0, v205, v205 op_sel_hi:[0,0,0]
	s_add_i32 s81, 0, 0x18000
	v_add_u32_e32 v165, s81, v157
	s_barrier
	ds_read_b128 v[10:13], v165
	ds_read_b128 v[14:17], v165 offset:1024
	ds_read_b128 v[2:5], v165 offset:2048
	ds_read_b128 v[6:9], v165 offset:3072
	s_add_u32 s76, s6, 0x20100
	s_addc_u32 s77, s7, 0
	s_mov_b32 m0, s39
	v_lshl_add_u64 v[168:169], s[76:77], 0, v[150:151]
	ds_read_b128 v[190:193], v161 offset:32768
	ds_read_b128 v[194:197], v161 offset:33792
	ds_read_b128 v[218:221], v161 offset:34816
	ds_read_b128 v[222:225], v161 offset:35840
	ds_read_b128 v[226:229], v161 offset:36864
	ds_read_b128 v[230:233], v161 offset:37888
	ds_read_b128 v[234:237], v161 offset:38912
	ds_read_b128 v[238:241], v161 offset:39936
	global_load_lds_dwordx4 v[168:169], off
	v_lshl_add_u64 v[168:169], s[76:77], 0, v[154:155]
	s_mov_b32 m0, s42
	s_nop 0
	global_load_lds_dwordx4 v[168:169], off
	s_waitcnt lgkmcnt(8)
	s_waitcnt vmcnt(10)
	s_barrier
	s_waitcnt lgkmcnt(6)
	v_mfma_scale_f32_16x16x128_f8f6f4 v[114:117], v[10:17], v[190:197], v[114:117], v205, v205 op_sel_hi:[0,0,0]
	v_mfma_scale_f32_16x16x128_f8f6f4 v[126:129], v[2:9], v[190:197], v[126:129], v205, v205 op_sel_hi:[0,0,0]
	s_waitcnt lgkmcnt(4)
	v_mfma_scale_f32_16x16x128_f8f6f4 v[102:105], v[10:17], v[218:225], v[102:105], v205, v205 op_sel_hi:[0,0,0]
	v_mfma_scale_f32_16x16x128_f8f6f4 v[98:101], v[2:9], v[218:225], v[98:101], v205, v205 op_sel_hi:[0,0,0]
	s_waitcnt lgkmcnt(2)
	v_mfma_scale_f32_16x16x128_f8f6f4 v[78:81], v[10:17], v[226:233], v[78:81], v205, v205 op_sel_hi:[0,0,0]
	v_mfma_scale_f32_16x16x128_f8f6f4 v[70:73], v[2:9], v[226:233], v[70:73], v205, v205 op_sel_hi:[0,0,0]
	s_waitcnt lgkmcnt(0)
	v_mfma_scale_f32_16x16x128_f8f6f4 v[50:53], v[10:17], v[234:241], v[50:53], v205, v205 op_sel_hi:[0,0,0]
	v_mfma_scale_f32_16x16x128_f8f6f4 v[42:45], v[2:9], v[234:241], v[42:45], v205, v205 op_sel_hi:[0,0,0]
	s_barrier
	s_add_i32 s83, 0, 0x1c000
	s_mov_b64 s[76:77], 0x180
	s_add_i32 s81, s81, s36
	v_add_u32_e32 v167, s83, v157
	v_lshl_add_u64 v[186:187], v[186:187], 0, s[76:77]
	s_mov_b32 m0, s81
	s_add_i32 s82, s81, 0x2000
	ds_read_b128 v[242:245], v167
	ds_read_b128 v[246:249], v167 offset:1024
	ds_read_b128 v[168:171], v167 offset:2048
	ds_read_b128 v[172:175], v167 offset:3072
	global_load_lds_dwordx4 v[186:187], off
	v_lshl_add_u64 v[186:187], v[188:189], 0, s[76:77]
	s_mov_b32 m0, s82
	s_nop 0
	global_load_lds_dwordx4 v[186:187], off
	s_waitcnt vmcnt(10)
	s_barrier
	s_waitcnt lgkmcnt(2)
	v_mfma_scale_f32_16x16x128_f8f6f4 v[140:143], v[242:249], v[190:197], v[140:143], v205, v205 op_sel_hi:[0,0,0]
	s_waitcnt lgkmcnt(0)
	v_mfma_scale_f32_16x16x128_f8f6f4 v[144:147], v[168:175], v[190:197], v[144:147], v205, v205 op_sel_hi:[0,0,0]
	v_mfma_scale_f32_16x16x128_f8f6f4 v[136:139], v[242:249], v[218:225], v[136:139], v205, v205 op_sel_hi:[0,0,0]
	v_mfma_scale_f32_16x16x128_f8f6f4 v[132:135], v[168:175], v[218:225], v[132:135], v205, v205 op_sel_hi:[0,0,0]
	v_mfma_scale_f32_16x16x128_f8f6f4 v[110:113], v[242:249], v[226:233], v[110:113], v205, v205 op_sel_hi:[0,0,0]
	v_mfma_scale_f32_16x16x128_f8f6f4 v[106:109], v[168:175], v[226:233], v[106:109], v205, v205 op_sel_hi:[0,0,0]
	v_mfma_scale_f32_16x16x128_f8f6f4 v[74:77], v[242:249], v[234:241], v[74:77], v205, v205 op_sel_hi:[0,0,0]
	v_mfma_scale_f32_16x16x128_f8f6f4 v[66:69], v[168:175], v[234:241], v[66:69], v205, v205 op_sel_hi:[0,0,0]
	s_mov_b32 m0, s45
	v_lshl_add_u64 v[182:183], v[182:183], 0, s[76:77]
	s_barrier
	ds_read_b128 v[186:189], v161 offset:49152
	ds_read_b128 v[190:193], v161 offset:50176
	ds_read_b128 v[194:197], v161 offset:51200
	ds_read_b128 v[198:201], v161 offset:52224
	ds_read_b128 v[218:221], v161 offset:53248
	ds_read_b128 v[222:225], v161 offset:54272
	ds_read_b128 v[226:229], v161 offset:55296
	ds_read_b128 v[230:233], v161 offset:56320
	global_load_lds_dwordx4 v[182:183], off
	v_lshl_add_u64 v[182:183], v[184:185], 0, s[76:77]
	s_mov_b32 m0, s46
	s_nop 0
	global_load_lds_dwordx4 v[182:183], off
	s_barrier
	s_waitcnt lgkmcnt(6)
	v_mfma_scale_f32_16x16x128_f8f6f4 v[94:97], v[10:17], v[186:193], v[94:97], v205, v205 op_sel_hi:[0,0,0]
	v_mfma_scale_f32_16x16x128_f8f6f4 v[90:93], v[2:9], v[186:193], v[90:93], v205, v205 op_sel_hi:[0,0,0]
	s_waitcnt lgkmcnt(4)
	v_mfma_scale_f32_16x16x128_f8f6f4 v[62:65], v[10:17], v[194:201], v[62:65], v205, v205 op_sel_hi:[0,0,0]
	v_mfma_scale_f32_16x16x128_f8f6f4 v[58:61], v[2:9], v[194:201], v[58:61], v205, v205 op_sel_hi:[0,0,0]
	s_waitcnt lgkmcnt(2)
	v_mfma_scale_f32_16x16x128_f8f6f4 v[38:41], v[10:17], v[218:225], v[38:41], v205, v205 op_sel_hi:[0,0,0]
	v_mfma_scale_f32_16x16x128_f8f6f4 v[34:37], v[2:9], v[218:225], v[34:37], v205, v205 op_sel_hi:[0,0,0]
	s_waitcnt lgkmcnt(0)
	v_mfma_scale_f32_16x16x128_f8f6f4 v[22:25], v[10:17], v[226:233], v[22:25], v205, v205 op_sel_hi:[0,0,0]
	v_mfma_scale_f32_16x16x128_f8f6f4 v[18:21], v[2:9], v[226:233], v[18:21], v205, v205 op_sel_hi:[0,0,0]
	s_barrier
	s_add_u32 s76, s74, 0x2180
	s_addc_u32 s77, s75, 0
	s_add_i32 s83, s83, s36
	v_lshl_add_u64 v[2:3], s[76:77], 0, v[148:149]
	s_mov_b32 m0, s83
	s_add_i32 s84, s83, 0x2000
	global_load_lds_dwordx4 v[2:3], off
	v_lshl_add_u64 v[2:3], s[76:77], 0, v[152:153]
	s_mov_b32 m0, s84
	s_nop 0
	global_load_lds_dwordx4 v[2:3], off
	s_waitcnt vmcnt(10)
	s_barrier
	v_mfma_scale_f32_16x16x128_f8f6f4 v[122:125], v[242:249], v[186:193], v[122:125], v205, v205 op_sel_hi:[0,0,0]
	v_mfma_scale_f32_16x16x128_f8f6f4 v[118:121], v[168:175], v[186:193], v[118:121], v205, v205 op_sel_hi:[0,0,0]
	v_mfma_scale_f32_16x16x128_f8f6f4 v[86:89], v[242:249], v[194:201], v[86:89], v205, v205 op_sel_hi:[0,0,0]
	v_mfma_scale_f32_16x16x128_f8f6f4 v[82:85], v[168:175], v[194:201], v[82:85], v205, v205 op_sel_hi:[0,0,0]
	v_mfma_scale_f32_16x16x128_f8f6f4 v[54:57], v[242:249], v[218:225], v[54:57], v205, v205 op_sel_hi:[0,0,0]
	v_mfma_scale_f32_16x16x128_f8f6f4 v[46:49], v[168:175], v[218:225], v[46:49], v205, v205 op_sel_hi:[0,0,0]
	v_mfma_scale_f32_16x16x128_f8f6f4 v[30:33], v[242:249], v[226:233], v[30:33], v205, v205 op_sel_hi:[0,0,0]
	v_mfma_scale_f32_16x16x128_f8f6f4 v[26:29], v[168:175], v[226:233], v[26:29], v205, v205 op_sel_hi:[0,0,0]
	s_add_u32 s6, s6, 0x20180
	s_addc_u32 s7, s7, 0
	s_add_u32 s85, s74, 0x200
	s_addc_u32 s86, s75, 0
	s_mov_b32 s87, 0
	s_barrier
.LBB0_457:
	ds_read_b128 v[10:13], v130
	ds_read_b128 v[14:17], v130 offset:1024
	ds_read_b128 v[168:171], v130 offset:2048
	ds_read_b128 v[172:175], v130 offset:3072
	s_add_u32 s74, s6, 0xfffe0080
	s_addc_u32 s75, s7, -1
	s_cmp_eq_u32 s87, 4
	s_cselect_b32 s77, s59, s75
	s_cselect_b32 s76, s60, s74
	s_cselect_b32 s75, s61, s86
	s_cselect_b32 s74, s62, s85
	s_mov_b32 m0, s63
	v_lshl_add_u64 v[2:3], s[6:7], 0, v[178:179]
	ds_read_b128 v[182:185], v161
	ds_read_b128 v[186:189], v161 offset:1024
	ds_read_b128 v[190:193], v161 offset:2048
	ds_read_b128 v[194:197], v161 offset:3072
	ds_read_b128 v[218:221], v161 offset:4096
	ds_read_b128 v[222:225], v161 offset:5120
	ds_read_b128 v[226:229], v161 offset:6144
	ds_read_b128 v[230:233], v161 offset:7168
	global_load_lds_dwordx4 v[2:3], off
	v_lshl_add_u64 v[2:3], s[6:7], 0, v[180:181]
	s_mov_b32 m0, s64
	s_nop 0
	global_load_lds_dwordx4 v[2:3], off
	s_waitcnt lgkmcnt(8)
	s_waitcnt vmcnt(10)
	s_barrier
	s_waitcnt lgkmcnt(6)
	v_mfma_scale_f32_16x16x128_f8f6f4 v[114:117], v[10:17], v[182:189], v[114:117], v205, v205 op_sel_hi:[0,0,0]
	v_mfma_scale_f32_16x16x128_f8f6f4 v[126:129], v[168:175], v[182:189], v[126:129], v205, v205 op_sel_hi:[0,0,0]
	s_waitcnt lgkmcnt(4)
	v_mfma_scale_f32_16x16x128_f8f6f4 v[102:105], v[10:17], v[190:197], v[102:105], v205, v205 op_sel_hi:[0,0,0]
	v_mfma_scale_f32_16x16x128_f8f6f4 v[98:101], v[168:175], v[190:197], v[98:101], v205, v205 op_sel_hi:[0,0,0]
	s_waitcnt lgkmcnt(2)
	v_mfma_scale_f32_16x16x128_f8f6f4 v[78:81], v[10:17], v[218:225], v[78:81], v205, v205 op_sel_hi:[0,0,0]
	v_mfma_scale_f32_16x16x128_f8f6f4 v[70:73], v[168:175], v[218:225], v[70:73], v205, v205 op_sel_hi:[0,0,0]
	s_waitcnt lgkmcnt(0)
	v_mfma_scale_f32_16x16x128_f8f6f4 v[50:53], v[10:17], v[226:233], v[50:53], v205, v205 op_sel_hi:[0,0,0]
	v_mfma_scale_f32_16x16x128_f8f6f4 v[42:45], v[168:175], v[226:233], v[42:45], v205, v205 op_sel_hi:[0,0,0]
	s_barrier
	s_mov_b32 m0, s65
	v_lshl_add_u64 v[6:7], s[74:75], 0, v[148:149]
	ds_read_b128 v[234:237], v163
	ds_read_b128 v[238:241], v163 offset:1024
	ds_read_b128 v[242:245], v163 offset:2048
	ds_read_b128 v[246:249], v163 offset:3072
	global_load_lds_dwordx4 v[6:7], off
	v_lshl_add_u64 v[8:9], s[74:75], 0, v[152:153]
	s_mov_b32 m0, s69
	s_nop 0
	global_load_lds_dwordx4 v[8:9], off
	s_waitcnt vmcnt(10)
	s_barrier
	s_waitcnt lgkmcnt(2)
	v_mfma_scale_f32_16x16x128_f8f6f4 v[140:143], v[234:241], v[182:189], v[140:143], v205, v205 op_sel_hi:[0,0,0]
	s_waitcnt lgkmcnt(0)
	v_mfma_scale_f32_16x16x128_f8f6f4 v[144:147], v[242:249], v[182:189], v[144:147], v205, v205 op_sel_hi:[0,0,0]
	v_mfma_scale_f32_16x16x128_f8f6f4 v[136:139], v[234:241], v[190:197], v[136:139], v205, v205 op_sel_hi:[0,0,0]
	v_mfma_scale_f32_16x16x128_f8f6f4 v[132:135], v[242:249], v[190:197], v[132:135], v205, v205 op_sel_hi:[0,0,0]
	v_mfma_scale_f32_16x16x128_f8f6f4 v[110:113], v[234:241], v[218:225], v[110:113], v205, v205 op_sel_hi:[0,0,0]
	v_mfma_scale_f32_16x16x128_f8f6f4 v[106:109], v[242:249], v[218:225], v[106:109], v205, v205 op_sel_hi:[0,0,0]
	v_mfma_scale_f32_16x16x128_f8f6f4 v[74:77], v[234:241], v[226:233], v[74:77], v205, v205 op_sel_hi:[0,0,0]
	v_mfma_scale_f32_16x16x128_f8f6f4 v[66:69], v[242:249], v[226:233], v[66:69], v205, v205 op_sel_hi:[0,0,0]
	s_mov_b32 m0, s37
	v_lshl_add_u64 v[2:3], s[76:77], 0, v[150:151]
	s_barrier
	ds_read_b128 v[182:185], v161 offset:16384
	ds_read_b128 v[186:189], v161 offset:17408
	ds_read_b128 v[190:193], v161 offset:18432
	ds_read_b128 v[194:197], v161 offset:19456
	ds_read_b128 v[218:221], v161 offset:20480
	ds_read_b128 v[222:225], v161 offset:21504
	ds_read_b128 v[226:229], v161 offset:22528
	ds_read_b128 v[230:233], v161 offset:23552
	global_load_lds_dwordx4 v[2:3], off
	v_lshl_add_u64 v[4:5], s[76:77], 0, v[154:155]
	s_mov_b32 m0, s38
	s_nop 0
	global_load_lds_dwordx4 v[4:5], off
	s_barrier
	s_waitcnt lgkmcnt(6)
	v_mfma_scale_f32_16x16x128_f8f6f4 v[94:97], v[10:17], v[182:189], v[94:97], v205, v205 op_sel_hi:[0,0,0]
	v_mfma_scale_f32_16x16x128_f8f6f4 v[90:93], v[168:175], v[182:189], v[90:93], v205, v205 op_sel_hi:[0,0,0]
	s_waitcnt lgkmcnt(4)
	v_mfma_scale_f32_16x16x128_f8f6f4 v[62:65], v[10:17], v[190:197], v[62:65], v205, v205 op_sel_hi:[0,0,0]
	v_mfma_scale_f32_16x16x128_f8f6f4 v[58:61], v[168:175], v[190:197], v[58:61], v205, v205 op_sel_hi:[0,0,0]
	s_waitcnt lgkmcnt(2)
	v_mfma_scale_f32_16x16x128_f8f6f4 v[38:41], v[10:17], v[218:225], v[38:41], v205, v205 op_sel_hi:[0,0,0]
	v_mfma_scale_f32_16x16x128_f8f6f4 v[34:37], v[168:175], v[218:225], v[34:37], v205, v205 op_sel_hi:[0,0,0]
	s_waitcnt lgkmcnt(0)
	v_mfma_scale_f32_16x16x128_f8f6f4 v[22:25], v[10:17], v[226:233], v[22:25], v205, v205 op_sel_hi:[0,0,0]
	v_mfma_scale_f32_16x16x128_f8f6f4 v[18:21], v[168:175], v[226:233], v[18:21], v205, v205 op_sel_hi:[0,0,0]
	s_barrier
	s_add_u32 s88, s74, 0x2000
	s_addc_u32 s89, s75, 0
	s_mov_b32 m0, s71
	v_lshl_add_u64 v[10:11], s[88:89], 0, v[148:149]
	global_load_lds_dwordx4 v[10:11], off
	v_lshl_add_u64 v[10:11], s[88:89], 0, v[152:153]
	s_mov_b32 m0, s79
	s_nop 0
	global_load_lds_dwordx4 v[10:11], off
	s_waitcnt vmcnt(10)
	s_barrier
	v_mfma_scale_f32_16x16x128_f8f6f4 v[122:125], v[234:241], v[182:189], v[122:125], v205, v205 op_sel_hi:[0,0,0]
	v_mfma_scale_f32_16x16x128_f8f6f4 v[118:121], v[242:249], v[182:189], v[118:121], v205, v205 op_sel_hi:[0,0,0]
	v_mfma_scale_f32_16x16x128_f8f6f4 v[86:89], v[234:241], v[190:197], v[86:89], v205, v205 op_sel_hi:[0,0,0]
	v_mfma_scale_f32_16x16x128_f8f6f4 v[82:85], v[242:249], v[190:197], v[82:85], v205, v205 op_sel_hi:[0,0,0]
	v_mfma_scale_f32_16x16x128_f8f6f4 v[54:57], v[234:241], v[218:225], v[54:57], v205, v205 op_sel_hi:[0,0,0]
	v_mfma_scale_f32_16x16x128_f8f6f4 v[46:49], v[242:249], v[218:225], v[46:49], v205, v205 op_sel_hi:[0,0,0]
	v_mfma_scale_f32_16x16x128_f8f6f4 v[30:33], v[234:241], v[226:233], v[30:33], v205, v205 op_sel_hi:[0,0,0]
	v_mfma_scale_f32_16x16x128_f8f6f4 v[26:29], v[242:249], v[226:233], v[26:29], v205, v205 op_sel_hi:[0,0,0]
	s_barrier
	ds_read_b128 v[10:13], v165
	ds_read_b128 v[14:17], v165 offset:1024
	ds_read_b128 v[168:171], v165 offset:2048
	ds_read_b128 v[172:175], v165 offset:3072
	s_add_u32 s76, s76, 0x20000
	s_addc_u32 s77, s77, 0
	s_mov_b32 m0, s39
	v_lshl_add_u64 v[198:199], s[76:77], 0, v[150:151]
	ds_read_b128 v[182:185], v161 offset:32768
	ds_read_b128 v[186:189], v161 offset:33792
	ds_read_b128 v[190:193], v161 offset:34816
	ds_read_b128 v[194:197], v161 offset:35840
	ds_read_b128 v[218:221], v161 offset:36864
	ds_read_b128 v[222:225], v161 offset:37888
	ds_read_b128 v[226:229], v161 offset:38912
	ds_read_b128 v[230:233], v161 offset:39936
	global_load_lds_dwordx4 v[198:199], off
	v_lshl_add_u64 v[198:199], s[76:77], 0, v[154:155]
	s_mov_b32 m0, s42
	s_nop 0
	global_load_lds_dwordx4 v[198:199], off
	s_waitcnt lgkmcnt(8)
	s_waitcnt vmcnt(10)
	s_barrier
	s_waitcnt lgkmcnt(6)
	v_mfma_scale_f32_16x16x128_f8f6f4 v[114:117], v[10:17], v[182:189], v[114:117], v205, v205 op_sel_hi:[0,0,0]
	v_mfma_scale_f32_16x16x128_f8f6f4 v[126:129], v[168:175], v[182:189], v[126:129], v205, v205 op_sel_hi:[0,0,0]
	s_waitcnt lgkmcnt(4)
	v_mfma_scale_f32_16x16x128_f8f6f4 v[102:105], v[10:17], v[190:197], v[102:105], v205, v205 op_sel_hi:[0,0,0]
	v_mfma_scale_f32_16x16x128_f8f6f4 v[98:101], v[168:175], v[190:197], v[98:101], v205, v205 op_sel_hi:[0,0,0]
	s_waitcnt lgkmcnt(2)
	v_mfma_scale_f32_16x16x128_f8f6f4 v[78:81], v[10:17], v[218:225], v[78:81], v205, v205 op_sel_hi:[0,0,0]
	v_mfma_scale_f32_16x16x128_f8f6f4 v[70:73], v[168:175], v[218:225], v[70:73], v205, v205 op_sel_hi:[0,0,0]
	s_waitcnt lgkmcnt(0)
	v_mfma_scale_f32_16x16x128_f8f6f4 v[50:53], v[10:17], v[226:233], v[50:53], v205, v205 op_sel_hi:[0,0,0]
	v_mfma_scale_f32_16x16x128_f8f6f4 v[42:45], v[168:175], v[226:233], v[42:45], v205, v205 op_sel_hi:[0,0,0]
	s_barrier
	s_mov_b32 m0, s81
	v_lshl_add_u64 v[6:7], v[6:7], 0, s[30:31]
	ds_read_b128 v[234:237], v167
	ds_read_b128 v[238:241], v167 offset:1024
	ds_read_b128 v[242:245], v167 offset:2048
	ds_read_b128 v[246:249], v167 offset:3072
	global_load_lds_dwordx4 v[6:7], off
	v_lshl_add_u64 v[6:7], v[8:9], 0, s[30:31]
	s_mov_b32 m0, s82
	s_nop 0
	global_load_lds_dwordx4 v[6:7], off
	s_waitcnt vmcnt(10)
	s_barrier
	s_waitcnt lgkmcnt(2)
	v_mfma_scale_f32_16x16x128_f8f6f4 v[140:143], v[234:241], v[182:189], v[140:143], v205, v205 op_sel_hi:[0,0,0]
	s_waitcnt lgkmcnt(0)
	v_mfma_scale_f32_16x16x128_f8f6f4 v[144:147], v[242:249], v[182:189], v[144:147], v205, v205 op_sel_hi:[0,0,0]
	v_mfma_scale_f32_16x16x128_f8f6f4 v[136:139], v[234:241], v[190:197], v[136:139], v205, v205 op_sel_hi:[0,0,0]
	v_mfma_scale_f32_16x16x128_f8f6f4 v[132:135], v[242:249], v[190:197], v[132:135], v205, v205 op_sel_hi:[0,0,0]
	v_mfma_scale_f32_16x16x128_f8f6f4 v[110:113], v[234:241], v[218:225], v[110:113], v205, v205 op_sel_hi:[0,0,0]
	v_mfma_scale_f32_16x16x128_f8f6f4 v[106:109], v[242:249], v[218:225], v[106:109], v205, v205 op_sel_hi:[0,0,0]
	v_mfma_scale_f32_16x16x128_f8f6f4 v[74:77], v[234:241], v[226:233], v[74:77], v205, v205 op_sel_hi:[0,0,0]
	v_mfma_scale_f32_16x16x128_f8f6f4 v[66:69], v[242:249], v[226:233], v[66:69], v205, v205 op_sel_hi:[0,0,0]
	s_mov_b32 m0, s45
	v_lshl_add_u64 v[2:3], v[2:3], 0, s[30:31]
	s_barrier
	ds_read_b128 v[182:185], v161 offset:49152
	ds_read_b128 v[186:189], v161 offset:50176
	ds_read_b128 v[190:193], v161 offset:51200
	ds_read_b128 v[194:197], v161 offset:52224
	ds_read_b128 v[218:221], v161 offset:53248
	ds_read_b128 v[222:225], v161 offset:54272
	ds_read_b128 v[226:229], v161 offset:55296
	ds_read_b128 v[230:233], v161 offset:56320
	global_load_lds_dwordx4 v[2:3], off
	v_lshl_add_u64 v[2:3], v[4:5], 0, s[30:31]
	s_mov_b32 m0, s46
	s_nop 0
	global_load_lds_dwordx4 v[2:3], off
	s_barrier
	s_waitcnt lgkmcnt(6)
	v_mfma_scale_f32_16x16x128_f8f6f4 v[94:97], v[10:17], v[182:189], v[94:97], v205, v205 op_sel_hi:[0,0,0]
	v_mfma_scale_f32_16x16x128_f8f6f4 v[90:93], v[168:175], v[182:189], v[90:93], v205, v205 op_sel_hi:[0,0,0]
	s_waitcnt lgkmcnt(4)
	v_mfma_scale_f32_16x16x128_f8f6f4 v[62:65], v[10:17], v[190:197], v[62:65], v205, v205 op_sel_hi:[0,0,0]
	v_mfma_scale_f32_16x16x128_f8f6f4 v[58:61], v[168:175], v[190:197], v[58:61], v205, v205 op_sel_hi:[0,0,0]
	s_waitcnt lgkmcnt(2)
	v_mfma_scale_f32_16x16x128_f8f6f4 v[38:41], v[10:17], v[218:225], v[38:41], v205, v205 op_sel_hi:[0,0,0]
	v_mfma_scale_f32_16x16x128_f8f6f4 v[34:37], v[168:175], v[218:225], v[34:37], v205, v205 op_sel_hi:[0,0,0]
	s_waitcnt lgkmcnt(0)
	v_mfma_scale_f32_16x16x128_f8f6f4 v[22:25], v[10:17], v[226:233], v[22:25], v205, v205 op_sel_hi:[0,0,0]
	v_mfma_scale_f32_16x16x128_f8f6f4 v[18:21], v[168:175], v[226:233], v[18:21], v205, v205 op_sel_hi:[0,0,0]
	s_barrier
	s_add_u32 s74, s74, 0x2080
	s_addc_u32 s75, s75, 0
	s_mov_b32 m0, s83
	v_lshl_add_u64 v[2:3], s[74:75], 0, v[148:149]
	global_load_lds_dwordx4 v[2:3], off
	v_lshl_add_u64 v[2:3], s[74:75], 0, v[152:153]
	s_mov_b32 m0, s84
	s_nop 0
	global_load_lds_dwordx4 v[2:3], off
	s_waitcnt vmcnt(10)
	s_barrier
	v_mfma_scale_f32_16x16x128_f8f6f4 v[122:125], v[234:241], v[182:189], v[122:125], v205, v205 op_sel_hi:[0,0,0]
	v_mfma_scale_f32_16x16x128_f8f6f4 v[118:121], v[242:249], v[182:189], v[118:121], v205, v205 op_sel_hi:[0,0,0]
	v_mfma_scale_f32_16x16x128_f8f6f4 v[86:89], v[234:241], v[190:197], v[86:89], v205, v205 op_sel_hi:[0,0,0]
	v_mfma_scale_f32_16x16x128_f8f6f4 v[82:85], v[242:249], v[190:197], v[82:85], v205, v205 op_sel_hi:[0,0,0]
	v_mfma_scale_f32_16x16x128_f8f6f4 v[54:57], v[234:241], v[218:225], v[54:57], v205, v205 op_sel_hi:[0,0,0]
	v_mfma_scale_f32_16x16x128_f8f6f4 v[46:49], v[242:249], v[218:225], v[46:49], v205, v205 op_sel_hi:[0,0,0]
	v_mfma_scale_f32_16x16x128_f8f6f4 v[30:33], v[234:241], v[226:233], v[30:33], v205, v205 op_sel_hi:[0,0,0]
	v_mfma_scale_f32_16x16x128_f8f6f4 v[26:29], v[242:249], v[226:233], v[26:29], v205, v205 op_sel_hi:[0,0,0]
	s_add_i32 s87, s87, 2
	s_add_u32 s6, s6, 0x100
	s_addc_u32 s7, s7, 0
	s_add_u32 s85, s85, 0x100
	s_addc_u32 s86, s86, 0
	s_cmp_gt_u32 s87, 5
	s_barrier
	s_cbranch_scc0 .LBB0_457
	s_lshl_b32 s74, s78, 8
	s_cmp_eq_u32 s80, 2
	s_nop 15
	s_nop 15
	s_cselect_b64 s[6:7], -1, 0
	s_and_b64 s[6:7], s[6:7], s[16:17]
	s_andn2_b64 vcc, exec, s[6:7]
	s_mov_b64 s[6:7], -1
	s_cbranch_vccz .LBB0_528
	s_cmp_lt_i32 s80, 2
	s_cselect_b64 s[6:7], -1, 0
	s_and_b64 s[60:61], s[6:7], exec
	v_readlane_b32 s60, v254, 30
	v_readlane_b32 s61, v254, 31
	s_cselect_b32 s59, s9, s11
	s_cselect_b32 s62, s8, s10
	s_lshl_b64 s[60:61], s[60:61], 2
	s_add_u32 s60, s62, s60
	s_addc_u32 s61, s59, s61
	v_lshlrev_b32_e32 v14, 2, v160
	global_load_dwordx4 v[2:5], v14, s[60:61] offset:48
	global_load_dwordx4 v[6:9], v14, s[60:61] offset:32
	global_load_dwordx4 v[10:13], v14, s[60:61] offset:16
	s_nop 0
	global_load_dwordx4 v[14:17], v14, s[60:61]
	s_ashr_i32 s75, s74, 31
	s_cmp_gt_i32 s80, 1
	s_mov_b64 s[76:77], -1
	s_cbranch_scc0 .LBB0_461
	s_lshl_b64 s[60:61], s[74:75], 8
	s_add_u32 s82, s50, s60
	s_addc_u32 s83, s51, s61
	s_mov_b64 s[76:77], 0

.LBB0_530:
	s_waitcnt vmcnt(0)
	s_setprio 0
	v_readlane_b32 s44, v254, 28
	s_cmpk_gt_u32 s35, 0xff
	v_readlane_b32 s45, v254, 29
	s_cbranch_scc1 .LBB0_532
	s_barrier

.LBB0_536:
	s_add_u32 s47, s12, 0x56668000
	s_addc_u32 s50, s13, 0
	s_add_u32 s51, s12, 0x59668000
	s_addc_u32 s53, s13, 0
	s_add_u32 s57, s12, 0x59c68000
	s_addc_u32 s58, s13, 0
	s_add_u32 s59, s12, 0x5bc68000
	v_and_b32_e32 v17, 15, v16
	v_and_b32_e32 v18, 48, v16
	v_lshlrev_b32_e32 v16, 2, v16
	s_addc_u32 s60, s13, 0
	s_and_b32 s5, s7, 3
	v_lshl_or_b32 v144, s6, 6, v17
	s_lshl_b32 s6, s6, 13
	v_lshl_or_b32 v17, v17, 6, v18
	v_and_b32_e32 v16, 32, v16
	s_add_i32 m0, s43, 0x18000
	v_lshl_add_u64 v[8:9], v[8:9], 0, s[30:31]
	v_bitop3_b32 v19, v17, s6, v16 bitop3:0xde
	s_lshl_b32 s6, s5, 12
	s_waitcnt vmcnt(4)
	s_barrier
	v_readfirstlane_b32 s100, v0
	s_cmp_lt_u32 s100, 0x100
	s_cbranch_scc1 .Lmy_sp_g1b
	s_setprio 1
.Lmy_sp_g1b:
	global_load_lds_dwordx4 v[8:9], off
	v_lshl_add_u64 v[6:7], v[6:7], 0, s[30:31]
	s_add_i32 m0, s43, 0x1a000
	s_add_i32 s61, s43, 0x8000
	s_add_i32 s62, s43, 0xa000
	v_bitop3_b32 v145, v17, s6, v16 bitop3:0xde
	global_load_lds_dwordx4 v[6:7], off
	v_lshl_add_u64 v[4:5], v[4:5], 0, s[30:31]
	s_mov_b32 m0, s61
	s_add_u32 s6, s66, 0x4080
	global_load_lds_dwordx4 v[4:5], off
	v_lshl_add_u64 v[2:3], v[2:3], 0, s[30:31]
	s_mov_b32 m0, s62
	s_addc_u32 s7, s67, 0
	global_load_lds_dwordx4 v[2:3], off
	s_add_i32 m0, s43, 0x1c000
	v_lshl_add_u64 v[2:3], s[6:7], 0, v[138:139]
	global_load_lds_dwordx4 v[2:3], off
	v_lshl_add_u64 v[2:3], s[6:7], 0, v[134:135]
	s_add_i32 m0, s43, 0x1e000
	v_lshl_or_b32 v146, s5, 6, v18
	global_load_lds_dwordx4 v[2:3], off
	v_lshlrev_b32_e32 v2, 14, v14
	v_and_b32_e32 v2, 0xffff8000, v2
	v_lshl_add_u32 v2, v13, 11, v2
	v_and_b32_e32 v3, 1, v14
	v_lshl_or_b32 v2, v3, 6, v2
	v_lshl_add_u32 v140, v15, 1, v2
	v_lshlrev_b32_e32 v2, 14, v10
	v_and_b32_e32 v2, 0xffff8000, v2
	s_waitcnt vmcnt(6)
	v_lshl_add_u32 v2, v11, 11, v2
	v_and_b32_e32 v3, 1, v10
	v_lshl_or_b32 v2, v3, 6, v2
	v_mov_b32_e32 v141, v131
	v_lshl_add_u32 v142, v12, 1, v2
	v_mov_b32_e32 v143, v131
	s_mov_b32 s63, 0
	v_add_u32_e32 v147, 0, v19
	s_mov_b64 s[14:15], s[66:67]
	s_mov_b64 s[12:13], s[18:19]
	s_barrier
	s_branch .LBB0_538

.LBB0_541:
	s_add_u32 s17, s18, 0xfffc0080
	s_addc_u32 s22, s19, -1
	s_cmp_eq_u32 s11, 12
	s_cselect_b32 s69, s13, s22
	s_cselect_b32 s68, s12, s17
	s_cselect_b32 s67, s15, s9
	s_cselect_b32 s66, s14, s5
	s_add_i32 s17, 0, 0x10000
	v_add_u32_e32 v130, s17, v145
	ds_read_b128 v[148:151], v130
	ds_read_b128 v[152:155], v130 offset:1024
	ds_read_b128 v[156:159], v130 offset:2048
	ds_read_b128 v[160:163], v130 offset:3072
	v_lshl_add_u64 v[198:199], s[18:19], 0, v[140:141]
	s_add_i32 m0, s43, 0xc000
	ds_read_b128 v[164:167], v147
	ds_read_b128 v[168:171], v147 offset:1024
	ds_read_b128 v[172:175], v147 offset:2048
	ds_read_b128 v[178:181], v147 offset:3072
	ds_read_b128 v[182:185], v147 offset:4096
	ds_read_b128 v[186:189], v147 offset:5120
	ds_read_b128 v[190:193], v147 offset:6144
	ds_read_b128 v[194:197], v147 offset:7168
	global_load_lds_dwordx4 v[198:199], off
	v_lshl_add_u64 v[198:199], s[18:19], 0, v[142:143]
	s_add_i32 m0, s43, 0xe000
	s_nop 0
	global_load_lds_dwordx4 v[198:199], off
	s_waitcnt lgkmcnt(8)
	s_waitcnt vmcnt(10)
	s_barrier
	s_waitcnt lgkmcnt(7)
	v_mfma_f32_16x16x32_bf16 v[126:129], v[148:151], v[164:167], v[126:129]
	s_waitcnt lgkmcnt(5)
	v_mfma_f32_16x16x32_bf16 v[122:125], v[156:159], v[164:167], v[122:125]
	v_mfma_f32_16x16x32_bf16 v[118:121], v[148:151], v[172:175], v[118:121]
	s_waitcnt lgkmcnt(3)
	v_mfma_f32_16x16x32_bf16 v[114:117], v[156:159], v[172:175], v[114:117]
	v_mfma_f32_16x16x32_bf16 v[102:105], v[148:151], v[182:185], v[102:105]
	s_waitcnt lgkmcnt(1)
	v_mfma_f32_16x16x32_bf16 v[98:101], v[156:159], v[182:185], v[98:101]
	v_mfma_f32_16x16x32_bf16 v[86:89], v[148:151], v[190:193], v[86:89]
	v_mfma_f32_16x16x32_bf16 v[82:85], v[156:159], v[190:193], v[82:85]
	v_mfma_f32_16x16x32_bf16 v[126:129], v[152:155], v[168:171], v[126:129]
	v_mfma_f32_16x16x32_bf16 v[122:125], v[160:163], v[168:171], v[122:125]
	v_mfma_f32_16x16x32_bf16 v[118:121], v[152:155], v[178:181], v[118:121]
	v_mfma_f32_16x16x32_bf16 v[114:117], v[160:163], v[178:181], v[114:117]
	v_mfma_f32_16x16x32_bf16 v[102:105], v[152:155], v[186:189], v[102:105]
	s_waitcnt lgkmcnt(0)
	v_mfma_f32_16x16x32_bf16 v[98:101], v[160:163], v[186:189], v[98:101]
	v_mfma_f32_16x16x32_bf16 v[86:89], v[152:155], v[194:197], v[86:89]
	v_mfma_f32_16x16x32_bf16 v[82:85], v[160:163], v[194:197], v[82:85]
	s_barrier
	s_add_i32 s22, 0, 0x14000
	s_add_i32 s17, s17, s38
	v_add_u32_e32 v130, s22, v145
	v_lshl_add_u64 v[230:231], s[66:67], 0, v[138:139]
	s_mov_b32 m0, s17
	ds_read_b128 v[198:201], v130
	ds_read_b128 v[218:221], v130 offset:1024
	ds_read_b128 v[222:225], v130 offset:2048
	ds_read_b128 v[226:229], v130 offset:3072
	global_load_lds_dwordx4 v[230:231], off
	v_lshl_add_u64 v[232:233], s[66:67], 0, v[134:135]
	s_add_i32 m0, s17, 0x2000
	s_nop 0
	global_load_lds_dwordx4 v[232:233], off
	s_waitcnt vmcnt(10)
	s_barrier
	s_waitcnt lgkmcnt(3)
	s_waitcnt lgkmcnt(1)
	v_mfma_f32_16x16x32_bf16 v[110:113], v[198:201], v[164:167], v[110:113]
	v_mfma_f32_16x16x32_bf16 v[106:109], v[222:225], v[164:167], v[106:109]
	v_mfma_f32_16x16x32_bf16 v[94:97], v[198:201], v[172:175], v[94:97]
	v_mfma_f32_16x16x32_bf16 v[90:93], v[222:225], v[172:175], v[90:93]
	v_mfma_f32_16x16x32_bf16 v[78:81], v[198:201], v[182:185], v[78:81]
	v_mfma_f32_16x16x32_bf16 v[74:77], v[222:225], v[182:185], v[74:77]
	v_mfma_f32_16x16x32_bf16 v[70:73], v[198:201], v[190:193], v[70:73]
	v_mfma_f32_16x16x32_bf16 v[58:61], v[222:225], v[190:193], v[58:61]
	s_waitcnt lgkmcnt(0)
	v_mfma_f32_16x16x32_bf16 v[110:113], v[218:221], v[168:171], v[110:113]
	v_mfma_f32_16x16x32_bf16 v[106:109], v[226:229], v[168:171], v[106:109]
	v_mfma_f32_16x16x32_bf16 v[94:97], v[218:221], v[178:181], v[94:97]
	v_mfma_f32_16x16x32_bf16 v[90:93], v[226:229], v[178:181], v[90:93]
	v_mfma_f32_16x16x32_bf16 v[78:81], v[218:221], v[186:189], v[78:81]
	v_mfma_f32_16x16x32_bf16 v[74:77], v[226:229], v[186:189], v[74:77]
	v_mfma_f32_16x16x32_bf16 v[70:73], v[218:221], v[194:197], v[70:73]
	v_mfma_f32_16x16x32_bf16 v[58:61], v[226:229], v[194:197], v[58:61]
	s_mov_b32 m0, s43
	v_lshl_add_u64 v[234:235], s[68:69], 0, v[136:137]
	s_barrier
	ds_read_b128 v[164:167], v147 offset:16384
	ds_read_b128 v[168:171], v147 offset:17408
	ds_read_b128 v[172:175], v147 offset:18432
	ds_read_b128 v[178:181], v147 offset:19456
	ds_read_b128 v[182:185], v147 offset:20480
	ds_read_b128 v[186:189], v147 offset:21504
	ds_read_b128 v[190:193], v147 offset:22528
	ds_read_b128 v[194:197], v147 offset:23552
	global_load_lds_dwordx4 v[234:235], off
	v_lshl_add_u64 v[236:237], s[68:69], 0, v[132:133]
	s_mov_b32 m0, s44
	s_nop 0
	global_load_lds_dwordx4 v[236:237], off
	s_barrier
	s_waitcnt lgkmcnt(7)
	v_mfma_f32_16x16x32_bf16 v[46:49], v[148:151], v[164:167], v[46:49]
	s_waitcnt lgkmcnt(5)
	v_mfma_f32_16x16x32_bf16 v[42:45], v[156:159], v[164:167], v[42:45]
	v_mfma_f32_16x16x32_bf16 v[38:41], v[148:151], v[172:175], v[38:41]
	s_waitcnt lgkmcnt(3)
	v_mfma_f32_16x16x32_bf16 v[34:37], v[156:159], v[172:175], v[34:37]
	v_mfma_f32_16x16x32_bf16 v[22:25], v[148:151], v[182:185], v[22:25]
	s_waitcnt lgkmcnt(1)
	v_mfma_f32_16x16x32_bf16 v[18:21], v[156:159], v[182:185], v[18:21]
	v_mfma_f32_16x16x32_bf16 v[6:9], v[148:151], v[190:193], v[6:9]
	v_mfma_f32_16x16x32_bf16 v[2:5], v[156:159], v[190:193], v[2:5]
	v_mfma_f32_16x16x32_bf16 v[46:49], v[152:155], v[168:171], v[46:49]
	v_mfma_f32_16x16x32_bf16 v[42:45], v[160:163], v[168:171], v[42:45]
	v_mfma_f32_16x16x32_bf16 v[38:41], v[152:155], v[178:181], v[38:41]
	v_mfma_f32_16x16x32_bf16 v[34:37], v[160:163], v[178:181], v[34:37]
	v_mfma_f32_16x16x32_bf16 v[22:25], v[152:155], v[186:189], v[22:25]
	s_waitcnt lgkmcnt(0)
	v_mfma_f32_16x16x32_bf16 v[18:21], v[160:163], v[186:189], v[18:21]
	v_mfma_f32_16x16x32_bf16 v[6:9], v[152:155], v[194:197], v[6:9]
	v_mfma_f32_16x16x32_bf16 v[2:5], v[160:163], v[194:197], v[2:5]
	s_barrier
	s_add_u32 s64, s66, 0x4000
	s_addc_u32 s65, s67, 0
	s_add_i32 s17, s22, s38
	v_lshl_add_u64 v[148:149], s[64:65], 0, v[138:139]
	s_mov_b32 m0, s17
	s_nop 0
	global_load_lds_dwordx4 v[148:149], off
	v_lshl_add_u64 v[148:149], s[64:65], 0, v[134:135]
	s_add_i32 m0, s17, 0x2000
	s_nop 0
	global_load_lds_dwordx4 v[148:149], off
	s_waitcnt vmcnt(10)
	s_barrier
	v_mfma_f32_16x16x32_bf16 v[30:33], v[198:201], v[164:167], v[30:33]
	v_mfma_f32_16x16x32_bf16 v[26:29], v[222:225], v[164:167], v[26:29]
	v_mfma_f32_16x16x32_bf16 v[14:17], v[198:201], v[172:175], v[14:17]
	v_mfma_f32_16x16x32_bf16 v[10:13], v[222:225], v[172:175], v[10:13]
	v_mfma_f32_16x16x32_bf16 v[62:65], v[198:201], v[182:185], v[62:65]
	v_mfma_f32_16x16x32_bf16 v[66:69], v[222:225], v[182:185], v[66:69]
	v_mfma_f32_16x16x32_bf16 v[50:53], v[198:201], v[190:193], v[50:53]
	v_mfma_f32_16x16x32_bf16 v[54:57], v[222:225], v[190:193], v[54:57]
	v_mfma_f32_16x16x32_bf16 v[30:33], v[218:221], v[168:171], v[30:33]
	v_mfma_f32_16x16x32_bf16 v[26:29], v[226:229], v[168:171], v[26:29]
	v_mfma_f32_16x16x32_bf16 v[14:17], v[218:221], v[178:181], v[14:17]
	v_mfma_f32_16x16x32_bf16 v[10:13], v[226:229], v[178:181], v[10:13]
	v_mfma_f32_16x16x32_bf16 v[62:65], v[218:221], v[186:189], v[62:65]
	v_mfma_f32_16x16x32_bf16 v[66:69], v[226:229], v[186:189], v[66:69]
	v_mfma_f32_16x16x32_bf16 v[50:53], v[218:221], v[194:197], v[50:53]
	v_mfma_f32_16x16x32_bf16 v[54:57], v[226:229], v[194:197], v[54:57]
	s_add_i32 s17, 0, 0x18000
	v_add_u32_e32 v130, s17, v145
	s_barrier
	ds_read_b128 v[148:151], v130
	ds_read_b128 v[152:155], v130 offset:1024
	ds_read_b128 v[156:159], v130 offset:2048
	ds_read_b128 v[160:163], v130 offset:3072
	s_add_u32 s64, s68, 0x40000
	s_addc_u32 s65, s69, 0
	s_mov_b32 m0, s45
	v_lshl_add_u64 v[198:199], s[64:65], 0, v[136:137]
	ds_read_b128 v[164:167], v147 offset:32768
	ds_read_b128 v[168:171], v147 offset:33792
	ds_read_b128 v[172:175], v147 offset:34816
	ds_read_b128 v[178:181], v147 offset:35840
	ds_read_b128 v[182:185], v147 offset:36864
	ds_read_b128 v[186:189], v147 offset:37888
	ds_read_b128 v[190:193], v147 offset:38912
	ds_read_b128 v[194:197], v147 offset:39936
	global_load_lds_dwordx4 v[198:199], off
	v_lshl_add_u64 v[198:199], s[64:65], 0, v[132:133]
	s_mov_b32 m0, s46
	s_nop 0
	global_load_lds_dwordx4 v[198:199], off
	s_waitcnt lgkmcnt(8)
	s_waitcnt vmcnt(10)
	s_barrier
	s_waitcnt lgkmcnt(7)
	v_mfma_f32_16x16x32_bf16 v[126:129], v[148:151], v[164:167], v[126:129]
	s_waitcnt lgkmcnt(5)
	v_mfma_f32_16x16x32_bf16 v[122:125], v[156:159], v[164:167], v[122:125]
	v_mfma_f32_16x16x32_bf16 v[118:121], v[148:151], v[172:175], v[118:121]
	s_waitcnt lgkmcnt(3)
	v_mfma_f32_16x16x32_bf16 v[114:117], v[156:159], v[172:175], v[114:117]
	v_mfma_f32_16x16x32_bf16 v[102:105], v[148:151], v[182:185], v[102:105]
	s_waitcnt lgkmcnt(1)
	v_mfma_f32_16x16x32_bf16 v[98:101], v[156:159], v[182:185], v[98:101]
	v_mfma_f32_16x16x32_bf16 v[86:89], v[148:151], v[190:193], v[86:89]
	v_mfma_f32_16x16x32_bf16 v[82:85], v[156:159], v[190:193], v[82:85]
	v_mfma_f32_16x16x32_bf16 v[126:129], v[152:155], v[168:171], v[126:129]
	v_mfma_f32_16x16x32_bf16 v[122:125], v[160:163], v[168:171], v[122:125]
	v_mfma_f32_16x16x32_bf16 v[118:121], v[152:155], v[178:181], v[118:121]
	v_mfma_f32_16x16x32_bf16 v[114:117], v[160:163], v[178:181], v[114:117]
	v_mfma_f32_16x16x32_bf16 v[102:105], v[152:155], v[186:189], v[102:105]
	s_waitcnt lgkmcnt(0)
	v_mfma_f32_16x16x32_bf16 v[98:101], v[160:163], v[186:189], v[98:101]
	v_mfma_f32_16x16x32_bf16 v[86:89], v[152:155], v[194:197], v[86:89]
	v_mfma_f32_16x16x32_bf16 v[82:85], v[160:163], v[194:197], v[82:85]
	s_barrier
	s_add_i32 s22, 0, 0x1c000
	s_add_i32 s17, s17, s38
	v_add_u32_e32 v130, s22, v145
	v_lshl_add_u64 v[230:231], v[230:231], 0, s[30:31]
	s_mov_b32 m0, s17
	ds_read_b128 v[198:201], v130
	ds_read_b128 v[218:221], v130 offset:1024
	ds_read_b128 v[222:225], v130 offset:2048
	ds_read_b128 v[226:229], v130 offset:3072
	global_load_lds_dwordx4 v[230:231], off
	v_lshl_add_u64 v[230:231], v[232:233], 0, s[30:31]
	s_add_i32 m0, s17, 0x2000
	s_nop 0
	global_load_lds_dwordx4 v[230:231], off
	s_waitcnt vmcnt(10)
	s_barrier
	s_waitcnt lgkmcnt(3)
	s_waitcnt lgkmcnt(1)
	v_mfma_f32_16x16x32_bf16 v[110:113], v[198:201], v[164:167], v[110:113]
	v_mfma_f32_16x16x32_bf16 v[106:109], v[222:225], v[164:167], v[106:109]
	v_mfma_f32_16x16x32_bf16 v[94:97], v[198:201], v[172:175], v[94:97]
	v_mfma_f32_16x16x32_bf16 v[90:93], v[222:225], v[172:175], v[90:93]
	v_mfma_f32_16x16x32_bf16 v[78:81], v[198:201], v[182:185], v[78:81]
	v_mfma_f32_16x16x32_bf16 v[74:77], v[222:225], v[182:185], v[74:77]
	v_mfma_f32_16x16x32_bf16 v[70:73], v[198:201], v[190:193], v[70:73]
	v_mfma_f32_16x16x32_bf16 v[58:61], v[222:225], v[190:193], v[58:61]
	s_waitcnt lgkmcnt(0)
	v_mfma_f32_16x16x32_bf16 v[110:113], v[218:221], v[168:171], v[110:113]
	v_mfma_f32_16x16x32_bf16 v[106:109], v[226:229], v[168:171], v[106:109]
	v_mfma_f32_16x16x32_bf16 v[94:97], v[218:221], v[178:181], v[94:97]
	v_mfma_f32_16x16x32_bf16 v[90:93], v[226:229], v[178:181], v[90:93]
	v_mfma_f32_16x16x32_bf16 v[78:81], v[218:221], v[186:189], v[78:81]
	v_mfma_f32_16x16x32_bf16 v[74:77], v[226:229], v[186:189], v[74:77]
	v_mfma_f32_16x16x32_bf16 v[70:73], v[218:221], v[194:197], v[70:73]
	v_mfma_f32_16x16x32_bf16 v[58:61], v[226:229], v[194:197], v[58:61]
	s_mov_b32 m0, s61
	v_lshl_add_u64 v[230:231], v[234:235], 0, s[30:31]
	s_barrier
	ds_read_b128 v[164:167], v147 offset:49152
	ds_read_b128 v[168:171], v147 offset:50176
	ds_read_b128 v[172:175], v147 offset:51200
	ds_read_b128 v[178:181], v147 offset:52224
	ds_read_b128 v[182:185], v147 offset:53248
	ds_read_b128 v[186:189], v147 offset:54272
	ds_read_b128 v[190:193], v147 offset:55296
	ds_read_b128 v[194:197], v147 offset:56320
	global_load_lds_dwordx4 v[230:231], off
	v_lshl_add_u64 v[230:231], v[236:237], 0, s[30:31]
	s_mov_b32 m0, s62
	s_nop 0
	global_load_lds_dwordx4 v[230:231], off
	s_barrier
	s_waitcnt lgkmcnt(7)
	v_mfma_f32_16x16x32_bf16 v[46:49], v[148:151], v[164:167], v[46:49]
	s_waitcnt lgkmcnt(5)
	v_mfma_f32_16x16x32_bf16 v[42:45], v[156:159], v[164:167], v[42:45]
	v_mfma_f32_16x16x32_bf16 v[38:41], v[148:151], v[172:175], v[38:41]
	s_waitcnt lgkmcnt(3)
	v_mfma_f32_16x16x32_bf16 v[34:37], v[156:159], v[172:175], v[34:37]
	v_mfma_f32_16x16x32_bf16 v[22:25], v[148:151], v[182:185], v[22:25]
	s_waitcnt lgkmcnt(1)
	v_mfma_f32_16x16x32_bf16 v[18:21], v[156:159], v[182:185], v[18:21]
	v_mfma_f32_16x16x32_bf16 v[6:9], v[148:151], v[190:193], v[6:9]
	v_mfma_f32_16x16x32_bf16 v[2:5], v[156:159], v[190:193], v[2:5]
	v_mfma_f32_16x16x32_bf16 v[46:49], v[152:155], v[168:171], v[46:49]
	v_mfma_f32_16x16x32_bf16 v[42:45], v[160:163], v[168:171], v[42:45]
	v_mfma_f32_16x16x32_bf16 v[38:41], v[152:155], v[178:181], v[38:41]
	v_mfma_f32_16x16x32_bf16 v[34:37], v[160:163], v[178:181], v[34:37]
	v_mfma_f32_16x16x32_bf16 v[22:25], v[152:155], v[186:189], v[22:25]
	s_waitcnt lgkmcnt(0)
	v_mfma_f32_16x16x32_bf16 v[18:21], v[160:163], v[186:189], v[18:21]
	v_mfma_f32_16x16x32_bf16 v[6:9], v[152:155], v[194:197], v[6:9]
	v_mfma_f32_16x16x32_bf16 v[2:5], v[160:163], v[194:197], v[2:5]
	s_barrier
	s_add_u32 s64, s66, 0x4080
	s_addc_u32 s65, s67, 0
	s_add_i32 s17, s22, s38
	v_lshl_add_u64 v[148:149], s[64:65], 0, v[138:139]
	s_mov_b32 m0, s17
	s_nop 0
	global_load_lds_dwordx4 v[148:149], off
	v_lshl_add_u64 v[148:149], s[64:65], 0, v[134:135]
	s_add_i32 m0, s17, 0x2000
	s_nop 0
	global_load_lds_dwordx4 v[148:149], off
	s_waitcnt vmcnt(10)
	s_barrier
	v_mfma_f32_16x16x32_bf16 v[30:33], v[198:201], v[164:167], v[30:33]
	v_mfma_f32_16x16x32_bf16 v[26:29], v[222:225], v[164:167], v[26:29]
	v_mfma_f32_16x16x32_bf16 v[14:17], v[198:201], v[172:175], v[14:17]
	v_mfma_f32_16x16x32_bf16 v[10:13], v[222:225], v[172:175], v[10:13]
	v_mfma_f32_16x16x32_bf16 v[62:65], v[198:201], v[182:185], v[62:65]
	v_mfma_f32_16x16x32_bf16 v[66:69], v[222:225], v[182:185], v[66:69]
	v_mfma_f32_16x16x32_bf16 v[50:53], v[198:201], v[190:193], v[50:53]
	v_mfma_f32_16x16x32_bf16 v[54:57], v[222:225], v[190:193], v[54:57]
	v_mfma_f32_16x16x32_bf16 v[30:33], v[218:221], v[168:171], v[30:33]
	v_mfma_f32_16x16x32_bf16 v[26:29], v[226:229], v[168:171], v[26:29]
	v_mfma_f32_16x16x32_bf16 v[14:17], v[218:221], v[178:181], v[14:17]
	v_mfma_f32_16x16x32_bf16 v[10:13], v[226:229], v[178:181], v[10:13]
	v_mfma_f32_16x16x32_bf16 v[62:65], v[218:221], v[186:189], v[62:65]
	v_mfma_f32_16x16x32_bf16 v[66:69], v[226:229], v[186:189], v[66:69]
	v_mfma_f32_16x16x32_bf16 v[50:53], v[218:221], v[194:197], v[50:53]
	v_mfma_f32_16x16x32_bf16 v[54:57], v[226:229], v[194:197], v[54:57]
	s_add_i32 s11, s11, 2
	s_add_u32 s18, s18, 0x100
	s_addc_u32 s19, s19, 0
	s_add_u32 s5, s5, 0x100
	s_addc_u32 s9, s9, 0
	s_cmp_gt_u32 s11, 13
	s_barrier
	s_cbranch_scc0 .LBB0_541
	s_mul_hi_i32 s5, s16, 0x38e38e39
	s_lshr_b32 s9, s5, 31
	s_ashr_i32 s5, s5, 1
	s_add_i32 s18, s5, s9
	s_mul_i32 s5, s18, 9
	s_sub_i32 s11, s16, s5
	s_cmp_lg_u32 s11, 8
	s_cselect_b64 s[66:67], -1, 0
	s_ashr_i32 s19, s18, 31
	s_cmp_gt_i32 s4, 2
	s_mov_b64 s[68:69], -1
	s_cbranch_scc0 .LBB0_548
	s_add_i32 s5, s4, -3
	s_and_b64 vcc, exec, s[66:67]
	s_cbranch_vccz .LBB0_545
	s_lshl_b64 s[16:17], s[18:19], 21
	s_add_u32 s9, s57, s16
	s_addc_u32 s16, s58, s17
	s_lshl_b32 s17, s5, 12
	s_add_u32 s9, s9, s17
	s_addc_u32 s22, s16, 0
	s_lshl_b32 s16, s11, 8
	s_ashr_i32 s17, s16, 31
	s_lshl_b64 s[16:17], s[16:17], 1
	s_add_u32 s16, s9, s16
	s_addc_u32 s17, s22, s17
	s_mov_b64 s[68:69], 0

.LBB0_553:
	s_waitcnt vmcnt(0)
	s_setprio 0
	s_cmpk_gt_u32 s29, 0xff
	s_cbranch_scc1 .LBB0_555
	s_barrier

.LBB0_860:
	s_add_u32 s42, s6, 0x45868000
	s_addc_u32 s43, s7, 0
	s_add_u32 s44, s6, 0x63568000
	v_and_b32_e32 v17, 15, v16
	v_and_b32_e32 v18, 48, v16
	v_lshlrev_b32_e32 v16, 2, v16
	s_sext_i32_i8 s17, s8
	s_addc_u32 s45, s7, 0
	s_and_b32 s8, s9, 3
	v_lshl_or_b32 v19, s10, 6, v17
	s_lshl_b32 s6, s10, 13
	v_lshl_or_b32 v17, v17, 6, v18
	v_and_b32_e32 v16, 32, v16
	s_add_i32 m0, s36, 0x18000
	v_lshl_add_u64 v[8:9], v[8:9], 0, s[30:31]
	v_bitop3_b32 v20, v17, s6, v16 bitop3:0xde
	s_lshl_b32 s6, s8, 12
	s_waitcnt vmcnt(4)
	s_barrier
	v_readfirstlane_b32 s100, v0
	s_cmp_lt_u32 s100, 0x100
	s_cbranch_scc1 .Lmy_sp_mrg0
	s_setprio 1
.Lmy_sp_mrg0:
	global_load_lds_dwordx4 v[8:9], off
	v_lshl_add_u64 v[6:7], v[6:7], 0, s[30:31]
	s_add_i32 m0, s36, 0x1a000
	s_add_i32 s46, s36, 0x8000
	s_add_i32 s47, s36, 0xa000
	v_bitop3_b32 v182, v17, s6, v16 bitop3:0xde
	global_load_lds_dwordx4 v[6:7], off
	v_lshl_add_u64 v[4:5], v[4:5], 0, s[30:31]
	s_mov_b32 m0, s46
	s_add_u32 s6, s64, 0x4080
	global_load_lds_dwordx4 v[4:5], off
	v_lshl_add_u64 v[2:3], v[2:3], 0, s[30:31]
	s_mov_b32 m0, s47
	s_addc_u32 s7, s65, 0
	global_load_lds_dwordx4 v[2:3], off
	s_add_i32 m0, s36, 0x1c000
	v_lshl_add_u64 v[2:3], s[6:7], 0, v[164:165]
	global_load_lds_dwordx4 v[2:3], off
	v_lshl_add_u64 v[2:3], s[6:7], 0, v[168:169]
	s_add_i32 m0, s36, 0x1e000
	s_movk_i32 s6, 0x1e00
	global_load_lds_dwordx4 v[2:3], off
	v_mul_lo_u32 v2, v19, s6
	s_lshl_b32 s6, s8, 6
	v_or3_b32 v183, v2, s6, v18
	v_lshlrev_b32_e32 v2, 10, v19
	v_or3_b32 v184, v2, s6, v18
	v_lshlrev_b32_e32 v2, 14, v10
	v_and_b32_e32 v2, 0xffff8000, v2
	v_lshl_add_u32 v2, v11, 11, v2
	v_and_b32_e32 v3, 1, v10
	v_lshl_or_b32 v2, v3, 6, v2
	v_lshl_add_u32 v172, v13, 1, v2
	v_lshlrev_b32_e32 v2, 14, v12
	v_and_b32_e32 v2, 0xffff8000, v2
	s_waitcnt vmcnt(6)
	v_lshl_add_u32 v2, v14, 11, v2
	v_and_b32_e32 v3, 1, v12
	v_lshl_or_b32 v2, v3, 6, v2
	v_mov_b32_e32 v173, v131
	v_lshl_add_u32 v174, v15, 1, v2
	v_mov_b32_e32 v175, v131
	s_mov_b32 s50, 0
	v_add_u32_e32 v185, 0, v20
	s_mov_b64 s[10:11], s[14:15]
	s_mov_b64 s[12:13], s[64:65]
	s_barrier
	s_branch .LBB0_862

.LBB0_869:
	s_add_u32 s58, s14, s64
	s_addc_u32 s59, s15, s65
	s_add_u32 s58, s58, 0x100
	s_addc_u32 s59, s59, 0
	s_add_u32 s60, s9, s64
	s_addc_u32 s61, s53, s65
	s_cmpk_eq_i32 s64, 0x700
	s_cselect_b32 s69, s11, s59
	s_cselect_b32 s68, s10, s58
	s_cselect_b32 s67, s13, s61
	s_cselect_b32 s66, s12, s60
	s_add_i32 s58, 0, 0x10000
	v_add_u32_e32 v130, s58, v182
	ds_read_b128 v[132:135], v130
	ds_read_b128 v[136:139], v130 offset:1024
	ds_read_b128 v[140:143], v130 offset:2048
	ds_read_b128 v[144:147], v130 offset:3072
	v_lshl_add_u64 v[218:219], v[178:179], 0, s[64:65]
	s_add_i32 m0, s36, 0xc000
	ds_read_b128 v[148:151], v185
	ds_read_b128 v[152:155], v185 offset:1024
	ds_read_b128 v[156:159], v185 offset:2048
	ds_read_b128 v[160:163], v185 offset:3072
	ds_read_b128 v[186:189], v185 offset:4096
	ds_read_b128 v[190:193], v185 offset:5120
	ds_read_b128 v[194:197], v185 offset:6144
	ds_read_b128 v[198:201], v185 offset:7168
	global_load_lds_dwordx4 v[218:219], off
	v_lshl_add_u64 v[218:219], v[180:181], 0, s[64:65]
	s_add_i32 m0, s36, 0xe000
	s_nop 0
	global_load_lds_dwordx4 v[218:219], off
	s_waitcnt lgkmcnt(8)
	s_waitcnt vmcnt(10)
	s_barrier
	s_waitcnt lgkmcnt(7)
	v_mfma_f32_16x16x32_bf16 v[126:129], v[132:135], v[148:151], v[126:129]
	s_waitcnt lgkmcnt(5)
	v_mfma_f32_16x16x32_bf16 v[122:125], v[140:143], v[148:151], v[122:125]
	v_mfma_f32_16x16x32_bf16 v[110:113], v[132:135], v[156:159], v[110:113]
	s_waitcnt lgkmcnt(3)
	v_mfma_f32_16x16x32_bf16 v[106:109], v[140:143], v[156:159], v[106:109]
	v_mfma_f32_16x16x32_bf16 v[94:97], v[132:135], v[186:189], v[94:97]
	s_waitcnt lgkmcnt(1)
	v_mfma_f32_16x16x32_bf16 v[90:93], v[140:143], v[186:189], v[90:93]
	v_mfma_f32_16x16x32_bf16 v[78:81], v[132:135], v[194:197], v[78:81]
	v_mfma_f32_16x16x32_bf16 v[74:77], v[140:143], v[194:197], v[74:77]
	v_mfma_f32_16x16x32_bf16 v[126:129], v[136:139], v[152:155], v[126:129]
	v_mfma_f32_16x16x32_bf16 v[122:125], v[144:147], v[152:155], v[122:125]
	v_mfma_f32_16x16x32_bf16 v[110:113], v[136:139], v[160:163], v[110:113]
	v_mfma_f32_16x16x32_bf16 v[106:109], v[144:147], v[160:163], v[106:109]
	v_mfma_f32_16x16x32_bf16 v[94:97], v[136:139], v[190:193], v[94:97]
	s_waitcnt lgkmcnt(0)
	v_mfma_f32_16x16x32_bf16 v[90:93], v[144:147], v[190:193], v[90:93]
	v_mfma_f32_16x16x32_bf16 v[78:81], v[136:139], v[198:201], v[78:81]
	v_mfma_f32_16x16x32_bf16 v[74:77], v[144:147], v[198:201], v[74:77]
	s_barrier
	s_add_i32 s60, 0, 0x14000
	s_add_i32 s58, s58, s35
	v_add_u32_e32 v130, s60, v182
	v_lshl_add_u64 v[234:235], s[66:67], 0, v[164:165]
	s_mov_b32 m0, s58
	ds_read_b128 v[218:221], v130
	ds_read_b128 v[222:225], v130 offset:1024
	ds_read_b128 v[226:229], v130 offset:2048
	ds_read_b128 v[230:233], v130 offset:3072
	global_load_lds_dwordx4 v[234:235], off
	v_lshl_add_u64 v[236:237], s[66:67], 0, v[168:169]
	s_add_i32 m0, s58, 0x2000
	s_nop 0
	global_load_lds_dwordx4 v[236:237], off
	s_waitcnt vmcnt(10)
	s_barrier
	s_waitcnt lgkmcnt(3)
	s_waitcnt lgkmcnt(1)
	v_mfma_f32_16x16x32_bf16 v[118:121], v[218:221], v[148:151], v[118:121]
	v_mfma_f32_16x16x32_bf16 v[114:117], v[226:229], v[148:151], v[114:117]
	v_mfma_f32_16x16x32_bf16 v[102:105], v[218:221], v[156:159], v[102:105]
	v_mfma_f32_16x16x32_bf16 v[98:101], v[226:229], v[156:159], v[98:101]
	v_mfma_f32_16x16x32_bf16 v[86:89], v[218:221], v[186:189], v[86:89]
	v_mfma_f32_16x16x32_bf16 v[82:85], v[226:229], v[186:189], v[82:85]
	v_mfma_f32_16x16x32_bf16 v[70:73], v[218:221], v[194:197], v[70:73]
	v_mfma_f32_16x16x32_bf16 v[66:69], v[226:229], v[194:197], v[66:69]
	s_waitcnt lgkmcnt(0)
	v_mfma_f32_16x16x32_bf16 v[118:121], v[222:225], v[152:155], v[118:121]
	v_mfma_f32_16x16x32_bf16 v[114:117], v[230:233], v[152:155], v[114:117]
	v_mfma_f32_16x16x32_bf16 v[102:105], v[222:225], v[160:163], v[102:105]
	v_mfma_f32_16x16x32_bf16 v[98:101], v[230:233], v[160:163], v[98:101]
	v_mfma_f32_16x16x32_bf16 v[86:89], v[222:225], v[190:193], v[86:89]
	v_mfma_f32_16x16x32_bf16 v[82:85], v[230:233], v[190:193], v[82:85]
	v_mfma_f32_16x16x32_bf16 v[70:73], v[222:225], v[198:201], v[70:73]
	v_mfma_f32_16x16x32_bf16 v[66:69], v[230:233], v[198:201], v[66:69]
	s_mov_b32 m0, s36
	v_lshl_add_u64 v[238:239], s[68:69], 0, v[166:167]
	s_barrier
	ds_read_b128 v[148:151], v185 offset:16384
	ds_read_b128 v[152:155], v185 offset:17408
	ds_read_b128 v[156:159], v185 offset:18432
	ds_read_b128 v[160:163], v185 offset:19456
	ds_read_b128 v[186:189], v185 offset:20480
	ds_read_b128 v[190:193], v185 offset:21504
	ds_read_b128 v[194:197], v185 offset:22528
	ds_read_b128 v[198:201], v185 offset:23552
	global_load_lds_dwordx4 v[238:239], off
	v_lshl_add_u64 v[240:241], s[68:69], 0, v[170:171]
	s_mov_b32 m0, s37
	s_nop 0
	global_load_lds_dwordx4 v[240:241], off
	s_barrier
	s_waitcnt lgkmcnt(7)
	v_mfma_f32_16x16x32_bf16 v[62:65], v[132:135], v[148:151], v[62:65]
	s_waitcnt lgkmcnt(5)
	v_mfma_f32_16x16x32_bf16 v[58:61], v[140:143], v[148:151], v[58:61]
	v_mfma_f32_16x16x32_bf16 v[46:49], v[132:135], v[156:159], v[46:49]
	s_waitcnt lgkmcnt(3)
	v_mfma_f32_16x16x32_bf16 v[42:45], v[140:143], v[156:159], v[42:45]
	v_mfma_f32_16x16x32_bf16 v[30:33], v[132:135], v[186:189], v[30:33]
	s_waitcnt lgkmcnt(1)
	v_mfma_f32_16x16x32_bf16 v[26:29], v[140:143], v[186:189], v[26:29]
	v_mfma_f32_16x16x32_bf16 v[14:17], v[132:135], v[194:197], v[14:17]
	v_mfma_f32_16x16x32_bf16 v[10:13], v[140:143], v[194:197], v[10:13]
	v_mfma_f32_16x16x32_bf16 v[62:65], v[136:139], v[152:155], v[62:65]
	v_mfma_f32_16x16x32_bf16 v[58:61], v[144:147], v[152:155], v[58:61]
	v_mfma_f32_16x16x32_bf16 v[46:49], v[136:139], v[160:163], v[46:49]
	v_mfma_f32_16x16x32_bf16 v[42:45], v[144:147], v[160:163], v[42:45]
	v_mfma_f32_16x16x32_bf16 v[30:33], v[136:139], v[190:193], v[30:33]
	s_waitcnt lgkmcnt(0)
	v_mfma_f32_16x16x32_bf16 v[26:29], v[144:147], v[190:193], v[26:29]
	v_mfma_f32_16x16x32_bf16 v[14:17], v[136:139], v[198:201], v[14:17]
	v_mfma_f32_16x16x32_bf16 v[10:13], v[144:147], v[198:201], v[10:13]
	s_barrier
	s_add_u32 s58, s66, 0x4000
	s_addc_u32 s59, s67, 0
	s_add_i32 s60, s60, s35
	v_lshl_add_u64 v[132:133], s[58:59], 0, v[164:165]
	s_mov_b32 m0, s60
	s_nop 0
	global_load_lds_dwordx4 v[132:133], off
	v_lshl_add_u64 v[132:133], s[58:59], 0, v[168:169]
	s_add_i32 m0, s60, 0x2000
	s_nop 0
	global_load_lds_dwordx4 v[132:133], off
	s_waitcnt vmcnt(10)
	s_barrier
	v_mfma_f32_16x16x32_bf16 v[54:57], v[218:221], v[148:151], v[54:57]
	v_mfma_f32_16x16x32_bf16 v[50:53], v[226:229], v[148:151], v[50:53]
	v_mfma_f32_16x16x32_bf16 v[38:41], v[218:221], v[156:159], v[38:41]
	v_mfma_f32_16x16x32_bf16 v[34:37], v[226:229], v[156:159], v[34:37]
	v_mfma_f32_16x16x32_bf16 v[22:25], v[218:221], v[186:189], v[22:25]
	v_mfma_f32_16x16x32_bf16 v[18:21], v[226:229], v[186:189], v[18:21]
	v_mfma_f32_16x16x32_bf16 v[6:9], v[218:221], v[194:197], v[6:9]
	v_mfma_f32_16x16x32_bf16 v[2:5], v[226:229], v[194:197], v[2:5]
	v_mfma_f32_16x16x32_bf16 v[54:57], v[222:225], v[152:155], v[54:57]
	v_mfma_f32_16x16x32_bf16 v[50:53], v[230:233], v[152:155], v[50:53]
	v_mfma_f32_16x16x32_bf16 v[38:41], v[222:225], v[160:163], v[38:41]
	v_mfma_f32_16x16x32_bf16 v[34:37], v[230:233], v[160:163], v[34:37]
	v_mfma_f32_16x16x32_bf16 v[22:25], v[222:225], v[190:193], v[22:25]
	v_mfma_f32_16x16x32_bf16 v[18:21], v[230:233], v[190:193], v[18:21]
	v_mfma_f32_16x16x32_bf16 v[6:9], v[222:225], v[198:201], v[6:9]
	v_mfma_f32_16x16x32_bf16 v[2:5], v[230:233], v[198:201], v[2:5]
	s_add_i32 s60, 0, 0x18000
	v_add_u32_e32 v130, s60, v182
	s_barrier
	ds_read_b128 v[132:135], v130
	ds_read_b128 v[136:139], v130 offset:1024
	ds_read_b128 v[140:143], v130 offset:2048
	ds_read_b128 v[144:147], v130 offset:3072
	s_add_u32 s58, s68, 0x40000
	s_addc_u32 s59, s69, 0
	s_mov_b32 m0, s38
	v_lshl_add_u64 v[218:219], s[58:59], 0, v[166:167]
	ds_read_b128 v[148:151], v185 offset:32768
	ds_read_b128 v[152:155], v185 offset:33792
	ds_read_b128 v[156:159], v185 offset:34816
	ds_read_b128 v[160:163], v185 offset:35840
	ds_read_b128 v[186:189], v185 offset:36864
	ds_read_b128 v[190:193], v185 offset:37888
	ds_read_b128 v[194:197], v185 offset:38912
	ds_read_b128 v[198:201], v185 offset:39936
	global_load_lds_dwordx4 v[218:219], off
	v_lshl_add_u64 v[218:219], s[58:59], 0, v[170:171]
	s_mov_b32 m0, s39
	s_nop 0
	global_load_lds_dwordx4 v[218:219], off
	s_waitcnt lgkmcnt(8)
	s_waitcnt vmcnt(10)
	s_barrier
	s_waitcnt lgkmcnt(7)
	v_mfma_f32_16x16x32_bf16 v[126:129], v[132:135], v[148:151], v[126:129]
	s_waitcnt lgkmcnt(5)
	v_mfma_f32_16x16x32_bf16 v[122:125], v[140:143], v[148:151], v[122:125]
	v_mfma_f32_16x16x32_bf16 v[110:113], v[132:135], v[156:159], v[110:113]
	s_waitcnt lgkmcnt(3)
	v_mfma_f32_16x16x32_bf16 v[106:109], v[140:143], v[156:159], v[106:109]
	v_mfma_f32_16x16x32_bf16 v[94:97], v[132:135], v[186:189], v[94:97]
	s_waitcnt lgkmcnt(1)
	v_mfma_f32_16x16x32_bf16 v[90:93], v[140:143], v[186:189], v[90:93]
	v_mfma_f32_16x16x32_bf16 v[78:81], v[132:135], v[194:197], v[78:81]
	v_mfma_f32_16x16x32_bf16 v[74:77], v[140:143], v[194:197], v[74:77]
	v_mfma_f32_16x16x32_bf16 v[126:129], v[136:139], v[152:155], v[126:129]
	v_mfma_f32_16x16x32_bf16 v[122:125], v[144:147], v[152:155], v[122:125]
	v_mfma_f32_16x16x32_bf16 v[110:113], v[136:139], v[160:163], v[110:113]
	v_mfma_f32_16x16x32_bf16 v[106:109], v[144:147], v[160:163], v[106:109]
	v_mfma_f32_16x16x32_bf16 v[94:97], v[136:139], v[190:193], v[94:97]
	s_waitcnt lgkmcnt(0)
	v_mfma_f32_16x16x32_bf16 v[90:93], v[144:147], v[190:193], v[90:93]
	v_mfma_f32_16x16x32_bf16 v[78:81], v[136:139], v[198:201], v[78:81]
	v_mfma_f32_16x16x32_bf16 v[74:77], v[144:147], v[198:201], v[74:77]
	s_barrier
	s_add_i32 s61, 0, 0x1c000
	s_add_i32 s58, s60, s35
	v_add_u32_e32 v130, s61, v182
	v_lshl_add_u64 v[234:235], v[234:235], 0, s[30:31]
	s_mov_b32 m0, s58
	ds_read_b128 v[218:221], v130
	ds_read_b128 v[222:225], v130 offset:1024
	ds_read_b128 v[226:229], v130 offset:2048
	ds_read_b128 v[230:233], v130 offset:3072
	global_load_lds_dwordx4 v[234:235], off
	v_lshl_add_u64 v[234:235], v[236:237], 0, s[30:31]
	s_add_i32 m0, s58, 0x2000
	s_nop 0
	global_load_lds_dwordx4 v[234:235], off
	s_waitcnt vmcnt(10)
	s_barrier
	s_waitcnt lgkmcnt(3)
	s_waitcnt lgkmcnt(1)
	v_mfma_f32_16x16x32_bf16 v[118:121], v[218:221], v[148:151], v[118:121]
	v_mfma_f32_16x16x32_bf16 v[114:117], v[226:229], v[148:151], v[114:117]
	v_mfma_f32_16x16x32_bf16 v[102:105], v[218:221], v[156:159], v[102:105]
	v_mfma_f32_16x16x32_bf16 v[98:101], v[226:229], v[156:159], v[98:101]
	v_mfma_f32_16x16x32_bf16 v[86:89], v[218:221], v[186:189], v[86:89]
	v_mfma_f32_16x16x32_bf16 v[82:85], v[226:229], v[186:189], v[82:85]
	v_mfma_f32_16x16x32_bf16 v[70:73], v[218:221], v[194:197], v[70:73]
	v_mfma_f32_16x16x32_bf16 v[66:69], v[226:229], v[194:197], v[66:69]
	s_waitcnt lgkmcnt(0)
	v_mfma_f32_16x16x32_bf16 v[118:121], v[222:225], v[152:155], v[118:121]
	v_mfma_f32_16x16x32_bf16 v[114:117], v[230:233], v[152:155], v[114:117]
	v_mfma_f32_16x16x32_bf16 v[102:105], v[222:225], v[160:163], v[102:105]
	v_mfma_f32_16x16x32_bf16 v[98:101], v[230:233], v[160:163], v[98:101]
	v_mfma_f32_16x16x32_bf16 v[86:89], v[222:225], v[190:193], v[86:89]
	v_mfma_f32_16x16x32_bf16 v[82:85], v[230:233], v[190:193], v[82:85]
	v_mfma_f32_16x16x32_bf16 v[70:73], v[222:225], v[198:201], v[70:73]
	v_mfma_f32_16x16x32_bf16 v[66:69], v[230:233], v[198:201], v[66:69]
	s_mov_b32 m0, s46
	v_lshl_add_u64 v[234:235], v[238:239], 0, s[30:31]
	s_barrier
	ds_read_b128 v[148:151], v185 offset:49152
	ds_read_b128 v[152:155], v185 offset:50176
	ds_read_b128 v[156:159], v185 offset:51200
	ds_read_b128 v[160:163], v185 offset:52224
	ds_read_b128 v[186:189], v185 offset:53248
	ds_read_b128 v[190:193], v185 offset:54272
	ds_read_b128 v[194:197], v185 offset:55296
	ds_read_b128 v[198:201], v185 offset:56320
	global_load_lds_dwordx4 v[234:235], off
	v_lshl_add_u64 v[234:235], v[240:241], 0, s[30:31]
	s_mov_b32 m0, s47
	s_nop 0
	global_load_lds_dwordx4 v[234:235], off
	s_barrier
	s_waitcnt lgkmcnt(7)
	v_mfma_f32_16x16x32_bf16 v[62:65], v[132:135], v[148:151], v[62:65]
	s_waitcnt lgkmcnt(5)
	v_mfma_f32_16x16x32_bf16 v[58:61], v[140:143], v[148:151], v[58:61]
	v_mfma_f32_16x16x32_bf16 v[46:49], v[132:135], v[156:159], v[46:49]
	s_waitcnt lgkmcnt(3)
	v_mfma_f32_16x16x32_bf16 v[42:45], v[140:143], v[156:159], v[42:45]
	v_mfma_f32_16x16x32_bf16 v[30:33], v[132:135], v[186:189], v[30:33]
	s_waitcnt lgkmcnt(1)
	v_mfma_f32_16x16x32_bf16 v[26:29], v[140:143], v[186:189], v[26:29]
	v_mfma_f32_16x16x32_bf16 v[14:17], v[132:135], v[194:197], v[14:17]
	v_mfma_f32_16x16x32_bf16 v[10:13], v[140:143], v[194:197], v[10:13]
	v_mfma_f32_16x16x32_bf16 v[62:65], v[136:139], v[152:155], v[62:65]
	v_mfma_f32_16x16x32_bf16 v[58:61], v[144:147], v[152:155], v[58:61]
	v_mfma_f32_16x16x32_bf16 v[46:49], v[136:139], v[160:163], v[46:49]
	v_mfma_f32_16x16x32_bf16 v[42:45], v[144:147], v[160:163], v[42:45]
	v_mfma_f32_16x16x32_bf16 v[30:33], v[136:139], v[190:193], v[30:33]
	s_waitcnt lgkmcnt(0)
	v_mfma_f32_16x16x32_bf16 v[26:29], v[144:147], v[190:193], v[26:29]
	v_mfma_f32_16x16x32_bf16 v[14:17], v[136:139], v[198:201], v[14:17]
	v_mfma_f32_16x16x32_bf16 v[10:13], v[144:147], v[198:201], v[10:13]
	s_barrier
	s_add_u32 s58, s66, 0x4080
	s_addc_u32 s59, s67, 0
	s_add_i32 s60, s61, s35
	v_lshl_add_u64 v[132:133], s[58:59], 0, v[164:165]
	s_mov_b32 m0, s60
	s_nop 0
	global_load_lds_dwordx4 v[132:133], off
	v_lshl_add_u64 v[132:133], s[58:59], 0, v[168:169]
	s_add_i32 m0, s60, 0x2000
	s_nop 0
	global_load_lds_dwordx4 v[132:133], off
	s_waitcnt vmcnt(10)
	s_barrier
	v_mfma_f32_16x16x32_bf16 v[54:57], v[218:221], v[148:151], v[54:57]
	v_mfma_f32_16x16x32_bf16 v[50:53], v[226:229], v[148:151], v[50:53]
	v_mfma_f32_16x16x32_bf16 v[38:41], v[218:221], v[156:159], v[38:41]
	v_mfma_f32_16x16x32_bf16 v[34:37], v[226:229], v[156:159], v[34:37]
	v_mfma_f32_16x16x32_bf16 v[22:25], v[218:221], v[186:189], v[22:25]
	v_mfma_f32_16x16x32_bf16 v[18:21], v[226:229], v[186:189], v[18:21]
	v_mfma_f32_16x16x32_bf16 v[6:9], v[218:221], v[194:197], v[6:9]
	v_mfma_f32_16x16x32_bf16 v[2:5], v[226:229], v[194:197], v[2:5]
	v_mfma_f32_16x16x32_bf16 v[54:57], v[222:225], v[152:155], v[54:57]
	v_mfma_f32_16x16x32_bf16 v[50:53], v[230:233], v[152:155], v[50:53]
	v_mfma_f32_16x16x32_bf16 v[38:41], v[222:225], v[160:163], v[38:41]
	v_mfma_f32_16x16x32_bf16 v[34:37], v[230:233], v[160:163], v[34:37]
	v_mfma_f32_16x16x32_bf16 v[22:25], v[222:225], v[190:193], v[22:25]
	v_mfma_f32_16x16x32_bf16 v[18:21], v[230:233], v[190:193], v[18:21]
	v_mfma_f32_16x16x32_bf16 v[6:9], v[222:225], v[198:201], v[6:9]
	v_mfma_f32_16x16x32_bf16 v[2:5], v[230:233], v[198:201], v[2:5]
	s_add_u32 s64, s64, 0x100
	s_addc_u32 s65, s65, 0
	s_cmp_gt_u32 s57, 13
	s_barrier
	s_cbranch_scc1 .LBB0_861

.LBB0_872:
	s_waitcnt vmcnt(0)
	s_setprio 0
	s_cmpk_gt_u32 s22, 0xff
	s_cbranch_scc1 .LBB0_874
	s_barrier

.LBB0_952:
	s_add_u32 s39, s8, 0x5ed68000
	v_and_b32_e32 v17, 15, v16
	v_and_b32_e32 v18, 48, v16
	v_lshlrev_b32_e32 v16, 2, v16
	s_sext_i32_i8 s47, s10
	s_addc_u32 s42, s9, 0
	s_and_b32 s10, s12, 3
	v_lshl_or_b32 v19, v17, 6, v18
	s_lshl_b32 s8, s11, 13
	v_and_b32_e32 v16, 32, v16
	s_add_i32 m0, s7, 0x18000
	v_lshl_add_u64 v[8:9], v[8:9], 0, s[30:31]
	v_bitop3_b32 v20, v19, s8, v16 bitop3:0xde
	s_lshl_b32 s8, s10, 12
	s_waitcnt vmcnt(4)
	s_barrier
	v_readfirstlane_b32 s100, v0
	s_cmp_lt_u32 s100, 0x100
	s_cbranch_scc1 .Lmy_sp_wo0
	s_setprio 1
.Lmy_sp_wo0:
	global_load_lds_dwordx4 v[8:9], off
	v_lshl_add_u64 v[6:7], v[6:7], 0, s[30:31]
	s_add_i32 m0, s7, 0x1a000
	s_add_i32 s43, s7, 0x8000
	s_add_i32 s44, s7, 0xa000
	v_bitop3_b32 v144, v19, s8, v16 bitop3:0xde
	global_load_lds_dwordx4 v[6:7], off
	v_lshl_add_u64 v[4:5], v[4:5], 0, s[30:31]
	s_mov_b32 m0, s43
	s_add_u32 s8, s18, 0x4080
	global_load_lds_dwordx4 v[4:5], off
	v_lshl_add_u64 v[2:3], v[2:3], 0, s[30:31]
	s_mov_b32 m0, s44
	s_addc_u32 s9, s19, 0
	global_load_lds_dwordx4 v[2:3], off
	s_add_i32 m0, s7, 0x1c000
	v_lshl_add_u64 v[2:3], s[8:9], 0, v[138:139]
	global_load_lds_dwordx4 v[2:3], off
	v_lshl_add_u64 v[2:3], s[8:9], 0, v[134:135]
	s_add_i32 m0, s7, 0x1e000
	s_lshl_b32 s8, s10, 6
	global_load_lds_dwordx4 v[2:3], off
	v_lshlrev_b32_e32 v2, 10, v17
	v_lshl_or_b32 v2, s11, 16, v2
	v_or3_b32 v145, v2, s8, v18
	v_lshlrev_b32_e32 v2, 14, v13
	v_and_b32_e32 v2, 0xffff8000, v2
	v_lshl_add_u32 v2, v14, 11, v2
	v_and_b32_e32 v3, 1, v13
	v_lshl_or_b32 v2, v3, 6, v2
	v_lshl_add_u32 v140, v15, 1, v2
	v_lshlrev_b32_e32 v2, 14, v10
	v_and_b32_e32 v2, 0xffff8000, v2
	s_waitcnt vmcnt(6)
	v_lshl_add_u32 v2, v11, 11, v2
	v_and_b32_e32 v3, 1, v10
	v_lshl_or_b32 v2, v3, 6, v2
	v_mov_b32_e32 v141, v131
	v_lshl_add_u32 v142, v12, 1, v2
	v_mov_b32_e32 v143, v131
	s_mov_b32 s45, 0
	v_add_u32_e32 v146, 0, v20
	s_mov_b64 s[14:15], s[18:19]
	s_mov_b64 s[10:11], s[16:17]
	s_barrier

.LBB0_956:
	s_add_u32 s18, s16, 0xfffc0080
	s_addc_u32 s19, s17, -1
	s_cmp_eq_u32 s51, 12
	s_cselect_b32 s63, s11, s19
	s_cselect_b32 s62, s10, s18
	s_cselect_b32 s19, s15, s50
	s_cselect_b32 s18, s14, s9
	s_add_i32 s53, 0, 0x10000
	v_add_u32_e32 v130, s53, v144
	ds_read_b128 v[148:151], v130
	ds_read_b128 v[152:155], v130 offset:1024
	ds_read_b128 v[156:159], v130 offset:2048
	ds_read_b128 v[160:163], v130 offset:3072
	v_lshl_add_u64 v[198:199], s[16:17], 0, v[140:141]
	s_add_i32 m0, s7, 0xc000
	ds_read_b128 v[164:167], v146
	ds_read_b128 v[168:171], v146 offset:1024
	ds_read_b128 v[172:175], v146 offset:2048
	ds_read_b128 v[178:181], v146 offset:3072
	ds_read_b128 v[182:185], v146 offset:4096
	ds_read_b128 v[186:189], v146 offset:5120
	ds_read_b128 v[190:193], v146 offset:6144
	ds_read_b128 v[194:197], v146 offset:7168
	global_load_lds_dwordx4 v[198:199], off
	v_lshl_add_u64 v[198:199], s[16:17], 0, v[142:143]
	s_add_i32 m0, s7, 0xe000
	s_nop 0
	global_load_lds_dwordx4 v[198:199], off
	s_waitcnt lgkmcnt(8)
	s_waitcnt vmcnt(10)
	s_barrier
	s_waitcnt lgkmcnt(7)
	v_mfma_f32_16x16x32_bf16 v[126:129], v[148:151], v[164:167], v[126:129]
	s_waitcnt lgkmcnt(5)
	v_mfma_f32_16x16x32_bf16 v[122:125], v[156:159], v[164:167], v[122:125]
	v_mfma_f32_16x16x32_bf16 v[118:121], v[148:151], v[172:175], v[118:121]
	s_waitcnt lgkmcnt(3)
	v_mfma_f32_16x16x32_bf16 v[114:117], v[156:159], v[172:175], v[114:117]
	v_mfma_f32_16x16x32_bf16 v[102:105], v[148:151], v[182:185], v[102:105]
	s_waitcnt lgkmcnt(1)
	v_mfma_f32_16x16x32_bf16 v[98:101], v[156:159], v[182:185], v[98:101]
	v_mfma_f32_16x16x32_bf16 v[86:89], v[148:151], v[190:193], v[86:89]
	v_mfma_f32_16x16x32_bf16 v[82:85], v[156:159], v[190:193], v[82:85]
	v_mfma_f32_16x16x32_bf16 v[126:129], v[152:155], v[168:171], v[126:129]
	v_mfma_f32_16x16x32_bf16 v[122:125], v[160:163], v[168:171], v[122:125]
	v_mfma_f32_16x16x32_bf16 v[118:121], v[152:155], v[178:181], v[118:121]
	v_mfma_f32_16x16x32_bf16 v[114:117], v[160:163], v[178:181], v[114:117]
	v_mfma_f32_16x16x32_bf16 v[102:105], v[152:155], v[186:189], v[102:105]
	s_waitcnt lgkmcnt(0)
	v_mfma_f32_16x16x32_bf16 v[98:101], v[160:163], v[186:189], v[98:101]
	v_mfma_f32_16x16x32_bf16 v[86:89], v[152:155], v[194:197], v[86:89]
	v_mfma_f32_16x16x32_bf16 v[82:85], v[160:163], v[194:197], v[82:85]
	s_barrier
	s_add_i32 s57, 0, 0x14000
	s_add_i32 s53, s53, s35
	v_add_u32_e32 v130, s57, v144
	v_lshl_add_u64 v[230:231], s[18:19], 0, v[138:139]
	s_mov_b32 m0, s53
	ds_read_b128 v[198:201], v130
	ds_read_b128 v[218:221], v130 offset:1024
	ds_read_b128 v[222:225], v130 offset:2048
	ds_read_b128 v[226:229], v130 offset:3072
	global_load_lds_dwordx4 v[230:231], off
	v_lshl_add_u64 v[232:233], s[18:19], 0, v[134:135]
	s_add_i32 m0, s53, 0x2000
	s_nop 0
	global_load_lds_dwordx4 v[232:233], off
	s_waitcnt vmcnt(10)
	s_barrier
	s_waitcnt lgkmcnt(3)
	s_waitcnt lgkmcnt(1)
	v_mfma_f32_16x16x32_bf16 v[110:113], v[198:201], v[164:167], v[110:113]
	v_mfma_f32_16x16x32_bf16 v[106:109], v[222:225], v[164:167], v[106:109]
	v_mfma_f32_16x16x32_bf16 v[94:97], v[198:201], v[172:175], v[94:97]
	v_mfma_f32_16x16x32_bf16 v[90:93], v[222:225], v[172:175], v[90:93]
	v_mfma_f32_16x16x32_bf16 v[78:81], v[198:201], v[182:185], v[78:81]
	v_mfma_f32_16x16x32_bf16 v[74:77], v[222:225], v[182:185], v[74:77]
	v_mfma_f32_16x16x32_bf16 v[70:73], v[198:201], v[190:193], v[70:73]
	v_mfma_f32_16x16x32_bf16 v[66:69], v[222:225], v[190:193], v[66:69]
	s_waitcnt lgkmcnt(0)
	v_mfma_f32_16x16x32_bf16 v[110:113], v[218:221], v[168:171], v[110:113]
	v_mfma_f32_16x16x32_bf16 v[106:109], v[226:229], v[168:171], v[106:109]
	v_mfma_f32_16x16x32_bf16 v[94:97], v[218:221], v[178:181], v[94:97]
	v_mfma_f32_16x16x32_bf16 v[90:93], v[226:229], v[178:181], v[90:93]
	v_mfma_f32_16x16x32_bf16 v[78:81], v[218:221], v[186:189], v[78:81]
	v_mfma_f32_16x16x32_bf16 v[74:77], v[226:229], v[186:189], v[74:77]
	v_mfma_f32_16x16x32_bf16 v[70:73], v[218:221], v[194:197], v[70:73]
	v_mfma_f32_16x16x32_bf16 v[66:69], v[226:229], v[194:197], v[66:69]
	s_mov_b32 m0, s7
	v_lshl_add_u64 v[234:235], s[62:63], 0, v[136:137]
	s_barrier
	ds_read_b128 v[164:167], v146 offset:16384
	ds_read_b128 v[168:171], v146 offset:17408
	ds_read_b128 v[172:175], v146 offset:18432
	ds_read_b128 v[178:181], v146 offset:19456
	ds_read_b128 v[182:185], v146 offset:20480
	ds_read_b128 v[186:189], v146 offset:21504
	ds_read_b128 v[190:193], v146 offset:22528
	ds_read_b128 v[194:197], v146 offset:23552
	global_load_lds_dwordx4 v[234:235], off
	v_lshl_add_u64 v[236:237], s[62:63], 0, v[132:133]
	s_mov_b32 m0, s36
	s_nop 0
	global_load_lds_dwordx4 v[236:237], off
	s_barrier
	s_waitcnt lgkmcnt(7)
	v_mfma_f32_16x16x32_bf16 v[54:57], v[148:151], v[164:167], v[54:57]
	s_waitcnt lgkmcnt(5)
	v_mfma_f32_16x16x32_bf16 v[50:53], v[156:159], v[164:167], v[50:53]
	v_mfma_f32_16x16x32_bf16 v[38:41], v[148:151], v[172:175], v[38:41]
	s_waitcnt lgkmcnt(3)
	v_mfma_f32_16x16x32_bf16 v[34:37], v[156:159], v[172:175], v[34:37]
	v_mfma_f32_16x16x32_bf16 v[22:25], v[148:151], v[182:185], v[22:25]
	s_waitcnt lgkmcnt(1)
	v_mfma_f32_16x16x32_bf16 v[18:21], v[156:159], v[182:185], v[18:21]
	v_mfma_f32_16x16x32_bf16 v[6:9], v[148:151], v[190:193], v[6:9]
	v_mfma_f32_16x16x32_bf16 v[2:5], v[156:159], v[190:193], v[2:5]
	v_mfma_f32_16x16x32_bf16 v[54:57], v[152:155], v[168:171], v[54:57]
	v_mfma_f32_16x16x32_bf16 v[50:53], v[160:163], v[168:171], v[50:53]
	v_mfma_f32_16x16x32_bf16 v[38:41], v[152:155], v[178:181], v[38:41]
	v_mfma_f32_16x16x32_bf16 v[34:37], v[160:163], v[178:181], v[34:37]
	v_mfma_f32_16x16x32_bf16 v[22:25], v[152:155], v[186:189], v[22:25]
	s_waitcnt lgkmcnt(0)
	v_mfma_f32_16x16x32_bf16 v[18:21], v[160:163], v[186:189], v[18:21]
	v_mfma_f32_16x16x32_bf16 v[6:9], v[152:155], v[194:197], v[6:9]
	v_mfma_f32_16x16x32_bf16 v[2:5], v[160:163], v[194:197], v[2:5]
	s_barrier
	s_add_u32 s58, s18, 0x4000
	s_addc_u32 s59, s19, 0
	s_add_i32 s53, s57, s35
	v_lshl_add_u64 v[148:149], s[58:59], 0, v[138:139]
	s_mov_b32 m0, s53
	s_nop 0
	global_load_lds_dwordx4 v[148:149], off
	v_lshl_add_u64 v[148:149], s[58:59], 0, v[134:135]
	s_add_i32 m0, s53, 0x2000
	s_nop 0
	global_load_lds_dwordx4 v[148:149], off
	s_waitcnt vmcnt(10)
	s_barrier
	v_mfma_f32_16x16x32_bf16 v[30:33], v[198:201], v[164:167], v[30:33]
	v_mfma_f32_16x16x32_bf16 v[26:29], v[222:225], v[164:167], v[26:29]
	v_mfma_f32_16x16x32_bf16 v[14:17], v[198:201], v[172:175], v[14:17]
	v_mfma_f32_16x16x32_bf16 v[10:13], v[222:225], v[172:175], v[10:13]
	v_mfma_f32_16x16x32_bf16 v[58:61], v[198:201], v[182:185], v[58:61]
	v_mfma_f32_16x16x32_bf16 v[62:65], v[222:225], v[182:185], v[62:65]
	v_mfma_f32_16x16x32_bf16 v[42:45], v[198:201], v[190:193], v[42:45]
	v_mfma_f32_16x16x32_bf16 v[46:49], v[222:225], v[190:193], v[46:49]
	v_mfma_f32_16x16x32_bf16 v[30:33], v[218:221], v[168:171], v[30:33]
	v_mfma_f32_16x16x32_bf16 v[26:29], v[226:229], v[168:171], v[26:29]
	v_mfma_f32_16x16x32_bf16 v[14:17], v[218:221], v[178:181], v[14:17]
	v_mfma_f32_16x16x32_bf16 v[10:13], v[226:229], v[178:181], v[10:13]
	v_mfma_f32_16x16x32_bf16 v[58:61], v[218:221], v[186:189], v[58:61]
	v_mfma_f32_16x16x32_bf16 v[62:65], v[226:229], v[186:189], v[62:65]
	v_mfma_f32_16x16x32_bf16 v[42:45], v[218:221], v[194:197], v[42:45]
	v_mfma_f32_16x16x32_bf16 v[46:49], v[226:229], v[194:197], v[46:49]
	s_add_i32 s53, 0, 0x18000
	v_add_u32_e32 v130, s53, v144
	s_barrier
	ds_read_b128 v[148:151], v130
	ds_read_b128 v[152:155], v130 offset:1024
	ds_read_b128 v[156:159], v130 offset:2048
	ds_read_b128 v[160:163], v130 offset:3072
	s_add_u32 s58, s62, 0x40000
	s_addc_u32 s59, s63, 0
	s_mov_b32 m0, s37
	v_lshl_add_u64 v[198:199], s[58:59], 0, v[136:137]
	ds_read_b128 v[164:167], v146 offset:32768
	ds_read_b128 v[168:171], v146 offset:33792
	ds_read_b128 v[172:175], v146 offset:34816
	ds_read_b128 v[178:181], v146 offset:35840
	ds_read_b128 v[182:185], v146 offset:36864
	ds_read_b128 v[186:189], v146 offset:37888
	ds_read_b128 v[190:193], v146 offset:38912
	ds_read_b128 v[194:197], v146 offset:39936
	global_load_lds_dwordx4 v[198:199], off
	v_lshl_add_u64 v[198:199], s[58:59], 0, v[132:133]
	s_mov_b32 m0, s38
	s_nop 0
	global_load_lds_dwordx4 v[198:199], off
	s_waitcnt lgkmcnt(8)
	s_waitcnt vmcnt(10)
	s_barrier
	s_waitcnt lgkmcnt(7)
	v_mfma_f32_16x16x32_bf16 v[126:129], v[148:151], v[164:167], v[126:129]
	s_waitcnt lgkmcnt(5)
	v_mfma_f32_16x16x32_bf16 v[122:125], v[156:159], v[164:167], v[122:125]
	v_mfma_f32_16x16x32_bf16 v[118:121], v[148:151], v[172:175], v[118:121]
	s_waitcnt lgkmcnt(3)
	v_mfma_f32_16x16x32_bf16 v[114:117], v[156:159], v[172:175], v[114:117]
	v_mfma_f32_16x16x32_bf16 v[102:105], v[148:151], v[182:185], v[102:105]
	s_waitcnt lgkmcnt(1)
	v_mfma_f32_16x16x32_bf16 v[98:101], v[156:159], v[182:185], v[98:101]
	v_mfma_f32_16x16x32_bf16 v[86:89], v[148:151], v[190:193], v[86:89]
	v_mfma_f32_16x16x32_bf16 v[82:85], v[156:159], v[190:193], v[82:85]
	v_mfma_f32_16x16x32_bf16 v[126:129], v[152:155], v[168:171], v[126:129]
	v_mfma_f32_16x16x32_bf16 v[122:125], v[160:163], v[168:171], v[122:125]
	v_mfma_f32_16x16x32_bf16 v[118:121], v[152:155], v[178:181], v[118:121]
	v_mfma_f32_16x16x32_bf16 v[114:117], v[160:163], v[178:181], v[114:117]
	v_mfma_f32_16x16x32_bf16 v[102:105], v[152:155], v[186:189], v[102:105]
	s_waitcnt lgkmcnt(0)
	v_mfma_f32_16x16x32_bf16 v[98:101], v[160:163], v[186:189], v[98:101]
	v_mfma_f32_16x16x32_bf16 v[86:89], v[152:155], v[194:197], v[86:89]
	v_mfma_f32_16x16x32_bf16 v[82:85], v[160:163], v[194:197], v[82:85]
	s_barrier
	s_add_i32 s57, 0, 0x1c000
	s_add_i32 s53, s53, s35
	v_add_u32_e32 v130, s57, v144
	v_lshl_add_u64 v[230:231], v[230:231], 0, s[30:31]
	s_mov_b32 m0, s53
	ds_read_b128 v[198:201], v130
	ds_read_b128 v[218:221], v130 offset:1024
	ds_read_b128 v[222:225], v130 offset:2048
	ds_read_b128 v[226:229], v130 offset:3072
	global_load_lds_dwordx4 v[230:231], off
	v_lshl_add_u64 v[230:231], v[232:233], 0, s[30:31]
	s_add_i32 m0, s53, 0x2000
	s_nop 0
	global_load_lds_dwordx4 v[230:231], off
	s_waitcnt vmcnt(10)
	s_barrier
	s_waitcnt lgkmcnt(3)
	s_waitcnt lgkmcnt(1)
	v_mfma_f32_16x16x32_bf16 v[110:113], v[198:201], v[164:167], v[110:113]
	v_mfma_f32_16x16x32_bf16 v[106:109], v[222:225], v[164:167], v[106:109]
	v_mfma_f32_16x16x32_bf16 v[94:97], v[198:201], v[172:175], v[94:97]
	v_mfma_f32_16x16x32_bf16 v[90:93], v[222:225], v[172:175], v[90:93]
	v_mfma_f32_16x16x32_bf16 v[78:81], v[198:201], v[182:185], v[78:81]
	v_mfma_f32_16x16x32_bf16 v[74:77], v[222:225], v[182:185], v[74:77]
	v_mfma_f32_16x16x32_bf16 v[70:73], v[198:201], v[190:193], v[70:73]
	v_mfma_f32_16x16x32_bf16 v[66:69], v[222:225], v[190:193], v[66:69]
	s_waitcnt lgkmcnt(0)
	v_mfma_f32_16x16x32_bf16 v[110:113], v[218:221], v[168:171], v[110:113]
	v_mfma_f32_16x16x32_bf16 v[106:109], v[226:229], v[168:171], v[106:109]
	v_mfma_f32_16x16x32_bf16 v[94:97], v[218:221], v[178:181], v[94:97]
	v_mfma_f32_16x16x32_bf16 v[90:93], v[226:229], v[178:181], v[90:93]
	v_mfma_f32_16x16x32_bf16 v[78:81], v[218:221], v[186:189], v[78:81]
	v_mfma_f32_16x16x32_bf16 v[74:77], v[226:229], v[186:189], v[74:77]
	v_mfma_f32_16x16x32_bf16 v[70:73], v[218:221], v[194:197], v[70:73]
	v_mfma_f32_16x16x32_bf16 v[66:69], v[226:229], v[194:197], v[66:69]
	s_mov_b32 m0, s43
	v_lshl_add_u64 v[230:231], v[234:235], 0, s[30:31]
	s_barrier
	ds_read_b128 v[164:167], v146 offset:49152
	ds_read_b128 v[168:171], v146 offset:50176
	ds_read_b128 v[172:175], v146 offset:51200
	ds_read_b128 v[178:181], v146 offset:52224
	ds_read_b128 v[182:185], v146 offset:53248
	ds_read_b128 v[186:189], v146 offset:54272
	ds_read_b128 v[190:193], v146 offset:55296
	ds_read_b128 v[194:197], v146 offset:56320
	global_load_lds_dwordx4 v[230:231], off
	v_lshl_add_u64 v[230:231], v[236:237], 0, s[30:31]
	s_mov_b32 m0, s44
	s_nop 0
	global_load_lds_dwordx4 v[230:231], off
	s_barrier
	s_waitcnt lgkmcnt(7)
	v_mfma_f32_16x16x32_bf16 v[54:57], v[148:151], v[164:167], v[54:57]
	s_waitcnt lgkmcnt(5)
	v_mfma_f32_16x16x32_bf16 v[50:53], v[156:159], v[164:167], v[50:53]
	v_mfma_f32_16x16x32_bf16 v[38:41], v[148:151], v[172:175], v[38:41]
	s_waitcnt lgkmcnt(3)
	v_mfma_f32_16x16x32_bf16 v[34:37], v[156:159], v[172:175], v[34:37]
	v_mfma_f32_16x16x32_bf16 v[22:25], v[148:151], v[182:185], v[22:25]
	s_waitcnt lgkmcnt(1)
	v_mfma_f32_16x16x32_bf16 v[18:21], v[156:159], v[182:185], v[18:21]
	v_mfma_f32_16x16x32_bf16 v[6:9], v[148:151], v[190:193], v[6:9]
	v_mfma_f32_16x16x32_bf16 v[2:5], v[156:159], v[190:193], v[2:5]
	v_mfma_f32_16x16x32_bf16 v[54:57], v[152:155], v[168:171], v[54:57]
	v_mfma_f32_16x16x32_bf16 v[50:53], v[160:163], v[168:171], v[50:53]
	v_mfma_f32_16x16x32_bf16 v[38:41], v[152:155], v[178:181], v[38:41]
	v_mfma_f32_16x16x32_bf16 v[34:37], v[160:163], v[178:181], v[34:37]
	v_mfma_f32_16x16x32_bf16 v[22:25], v[152:155], v[186:189], v[22:25]
	s_waitcnt lgkmcnt(0)
	v_mfma_f32_16x16x32_bf16 v[18:21], v[160:163], v[186:189], v[18:21]
	v_mfma_f32_16x16x32_bf16 v[6:9], v[152:155], v[194:197], v[6:9]
	v_mfma_f32_16x16x32_bf16 v[2:5], v[160:163], v[194:197], v[2:5]
	s_barrier
	s_add_u32 s18, s18, 0x4080
	s_addc_u32 s19, s19, 0
	s_add_i32 s53, s57, s35
	v_lshl_add_u64 v[148:149], s[18:19], 0, v[138:139]
	s_mov_b32 m0, s53
	s_nop 0
	global_load_lds_dwordx4 v[148:149], off
	v_lshl_add_u64 v[148:149], s[18:19], 0, v[134:135]
	s_add_i32 m0, s53, 0x2000
	s_nop 0
	global_load_lds_dwordx4 v[148:149], off
	s_waitcnt vmcnt(10)
	s_barrier
	v_mfma_f32_16x16x32_bf16 v[30:33], v[198:201], v[164:167], v[30:33]
	v_mfma_f32_16x16x32_bf16 v[26:29], v[222:225], v[164:167], v[26:29]
	v_mfma_f32_16x16x32_bf16 v[14:17], v[198:201], v[172:175], v[14:17]
	v_mfma_f32_16x16x32_bf16 v[10:13], v[222:225], v[172:175], v[10:13]
	v_mfma_f32_16x16x32_bf16 v[58:61], v[198:201], v[182:185], v[58:61]
	v_mfma_f32_16x16x32_bf16 v[62:65], v[222:225], v[182:185], v[62:65]
	v_mfma_f32_16x16x32_bf16 v[42:45], v[198:201], v[190:193], v[42:45]
	v_mfma_f32_16x16x32_bf16 v[46:49], v[222:225], v[190:193], v[46:49]
	v_mfma_f32_16x16x32_bf16 v[30:33], v[218:221], v[168:171], v[30:33]
	v_mfma_f32_16x16x32_bf16 v[26:29], v[226:229], v[168:171], v[26:29]
	v_mfma_f32_16x16x32_bf16 v[14:17], v[218:221], v[178:181], v[14:17]
	v_mfma_f32_16x16x32_bf16 v[10:13], v[226:229], v[178:181], v[10:13]
	v_mfma_f32_16x16x32_bf16 v[58:61], v[218:221], v[186:189], v[58:61]
	v_mfma_f32_16x16x32_bf16 v[62:65], v[226:229], v[186:189], v[62:65]
	v_mfma_f32_16x16x32_bf16 v[42:45], v[218:221], v[194:197], v[42:45]
	v_mfma_f32_16x16x32_bf16 v[46:49], v[226:229], v[194:197], v[46:49]
	s_add_i32 s51, s51, 2
	s_add_u32 s16, s16, 0x100
	s_addc_u32 s17, s17, 0
	s_add_u32 s9, s9, 0x100
	s_addc_u32 s50, s50, 0
	s_cmp_gt_u32 s51, 13
	s_barrier
	s_cbranch_scc0 .LBB0_956
	s_lshl_b32 s16, s6, 8
	s_ashr_i32 s17, s16, 31
	s_lshl_b64 s[16:17], s[16:17], 11
	s_add_u32 s6, s39, s16
	s_addc_u32 s9, s42, s17
	s_lshl_b32 s16, s47, 8
	s_ashr_i32 s17, s16, 31
	s_lshl_b64 s[16:17], s[16:17], 1
	s_add_u32 s16, s6, s16
	s_addc_u32 s17, s9, s17
	v_mov_b32_e32 v130, v145
	v_cvt_pk_bf16_f32 v110, v110, v111
	v_lshl_add_u64 v[148:149], v[130:131], 1, s[16:17]
	v_cvt_pk_bf16_f32 v111, v112, v113
	v_cvt_pk_bf16_f32 v112, v106, v107
	v_cvt_pk_bf16_f32 v113, v108, v109
	s_mov_b32 s6, 0x8000
	global_store_dwordx4 v[148:149], v[110:113], off offset:16
	v_cvt_pk_bf16_f32 v94, v94, v95
	v_cvt_pk_bf16_f32 v95, v96, v97
	v_add_co_u32_e32 v110, vcc, s6, v148
	v_cvt_pk_bf16_f32 v96, v90, v91
	s_nop 0
	v_addc_co_u32_e32 v111, vcc, 0, v149, vcc
	v_cvt_pk_bf16_f32 v97, v92, v93
	s_mov_b32 s6, 0x10000
	global_store_dwordx4 v[110:111], v[94:97], off offset:16
	v_cvt_pk_bf16_f32 v78, v78, v79
	v_cvt_pk_bf16_f32 v79, v80, v81
	v_add_co_u32_e32 v94, vcc, s6, v148
	v_cvt_pk_bf16_f32 v80, v74, v75
	s_nop 0
	v_addc_co_u32_e32 v95, vcc, 0, v149, vcc
	v_cvt_pk_bf16_f32 v81, v76, v77
	s_mov_b32 s6, 0x18000
	global_store_dwordx4 v[94:95], v[78:81], off offset:16
	v_cvt_pk_bf16_f32 v54, v54, v55
	v_cvt_pk_bf16_f32 v55, v56, v57
	v_add_co_u32_e32 v78, vcc, s6, v148
	s_mov_b32 s6, 0x40000
	s_nop 0
	v_addc_co_u32_e32 v79, vcc, 0, v149, vcc
	v_cvt_pk_bf16_f32 v56, v50, v51
	v_add_co_u32_e32 v50, vcc, s6, v148
	v_cvt_pk_bf16_f32 v30, v30, v31
	s_nop 0
	v_addc_co_u32_e32 v51, vcc, 0, v149, vcc
	v_cvt_pk_bf16_f32 v31, v32, v33
	v_cvt_pk_bf16_f32 v32, v26, v27
	v_cvt_pk_bf16_f32 v33, v28, v29
	s_mov_b32 s6, 0x48000
	global_store_dwordx4 v[50:51], v[30:33], off offset:16
	v_cvt_pk_bf16_f32 v14, v14, v15
	v_cvt_pk_bf16_f32 v15, v16, v17
	v_add_co_u32_e32 v30, vcc, s6, v148
	v_cvt_pk_bf16_f32 v16, v10, v11
	s_nop 0
	v_addc_co_u32_e32 v31, vcc, 0, v149, vcc
	v_cvt_pk_bf16_f32 v17, v12, v13
	s_mov_b32 s6, 0x50000
	global_store_dwordx4 v[30:31], v[14:17], off offset:16
	v_cvt_pk_bf16_f32 v10, v22, v23
	v_cvt_pk_bf16_f32 v11, v24, v25
	v_add_co_u32_e32 v14, vcc, s6, v148
	v_cvt_pk_bf16_f32 v12, v18, v19
	v_cvt_pk_bf16_f32 v13, v20, v21
	v_addc_co_u32_e32 v15, vcc, 0, v149, vcc
	global_store_dwordx4 v[14:15], v[10:13], off
	s_mov_b32 s6, 0x58000
	v_cvt_pk_bf16_f32 v126, v126, v127
	v_cvt_pk_bf16_f32 v10, v58, v59
	v_cvt_pk_bf16_f32 v11, v60, v61
	v_cvt_pk_bf16_f32 v12, v62, v63
	v_cvt_pk_bf16_f32 v13, v64, v65
	global_store_dwordx4 v[14:15], v[10:13], off offset:16
	v_cvt_pk_bf16_f32 v127, v128, v129
	v_cvt_pk_bf16_f32 v128, v122, v123
	v_add_co_u32_e32 v10, vcc, s6, v148
	v_cvt_pk_bf16_f32 v129, v124, v125
	s_nop 0
	v_addc_co_u32_e32 v11, vcc, 0, v149, vcc
	v_cvt_pk_bf16_f32 v106, v118, v119
	v_cvt_pk_bf16_f32 v107, v120, v121
	v_cvt_pk_bf16_f32 v108, v114, v115
	v_cvt_pk_bf16_f32 v109, v116, v117
	v_cvt_pk_bf16_f32 v90, v102, v103
	v_cvt_pk_bf16_f32 v91, v104, v105
	v_cvt_pk_bf16_f32 v92, v98, v99
	v_cvt_pk_bf16_f32 v93, v100, v101
	v_cvt_pk_bf16_f32 v74, v86, v87
	v_cvt_pk_bf16_f32 v75, v88, v89
	v_cvt_pk_bf16_f32 v76, v82, v83
	v_cvt_pk_bf16_f32 v77, v84, v85
	v_cvt_pk_bf16_f32 v70, v70, v71
	v_cvt_pk_bf16_f32 v71, v72, v73
	v_cvt_pk_bf16_f32 v72, v66, v67
	v_cvt_pk_bf16_f32 v73, v68, v69
	v_cvt_pk_bf16_f32 v57, v52, v53
	v_cvt_pk_bf16_f32 v26, v38, v39
	v_cvt_pk_bf16_f32 v27, v40, v41
	v_cvt_pk_bf16_f32 v28, v34, v35
	v_cvt_pk_bf16_f32 v29, v36, v37
	v_cvt_pk_bf16_f32 v6, v6, v7
	v_cvt_pk_bf16_f32 v7, v8, v9
	v_cvt_pk_bf16_f32 v8, v2, v3
	v_cvt_pk_bf16_f32 v9, v4, v5
	v_cvt_pk_bf16_f32 v2, v42, v43
	v_cvt_pk_bf16_f32 v3, v44, v45
	v_cvt_pk_bf16_f32 v4, v46, v47
	v_cvt_pk_bf16_f32 v5, v48, v49
	s_and_b64 vcc, exec, s[12:13]
	s_mov_b32 s6, s8
	s_mov_b32 s47, s46
	s_mov_b64 s[18:19], s[14:15]
	s_mov_b64 s[16:17], s[10:11]
	global_store_dwordx4 v[148:149], v[126:129], off
	global_store_dwordx4 v[110:111], v[106:109], off
	global_store_dwordx4 v[94:95], v[90:93], off
	global_store_dwordx4 v[78:79], v[74:77], off
	global_store_dwordx4 v[78:79], v[70:73], off offset:16
	global_store_dwordx4 v[50:51], v[54:57], off
	global_store_dwordx4 v[30:31], v[26:29], off
	global_store_dwordx4 v[10:11], v[6:9], off
	global_store_dwordx4 v[10:11], v[2:5], off offset:16
	s_cbranch_vccz .LBB0_953
	s_waitcnt vmcnt(0)
	s_setprio 0
	v_readlane_b32 s44, v254, 28
	s_cmpk_gt_u32 s2, 0xff
	s_movk_i32 s47, 0x900
	s_mov_b64 s[42:43], 0x4000
	v_readlane_b32 s45, v254, 29
	s_cbranch_scc1 .LBB0_960
	s_barrier

.LBB0_1020:
	s_add_u32 s39, s6, 0x5ed68000
	v_and_b32_e32 v17, 15, v16
	v_and_b32_e32 v18, 48, v16
	v_lshlrev_b32_e32 v16, 2, v16
	s_sext_i32_i8 s47, s8
	s_addc_u32 s42, s7, 0
	s_and_b32 s8, s10, 3
	v_lshl_or_b32 v19, v17, 6, v18
	s_lshl_b32 s6, s9, 13
	v_and_b32_e32 v16, 32, v16
	s_add_i32 m0, s5, 0x18000
	v_lshl_add_u64 v[8:9], v[8:9], 0, s[30:31]
	v_bitop3_b32 v20, v19, s6, v16 bitop3:0xde
	s_lshl_b32 s6, s8, 12
	s_waitcnt vmcnt(4)
	s_barrier
	v_readfirstlane_b32 s100, v0
	s_cmp_lt_u32 s100, 0x100
	s_cbranch_scc1 .Lmy_sp_wo1
	s_setprio 1
.Lmy_sp_wo1:
	global_load_lds_dwordx4 v[8:9], off
	v_lshl_add_u64 v[6:7], v[6:7], 0, s[30:31]
	s_add_i32 m0, s5, 0x1a000
	s_add_i32 s43, s5, 0x8000
	s_add_i32 s44, s5, 0xa000
	v_bitop3_b32 v144, v19, s6, v16 bitop3:0xde
	global_load_lds_dwordx4 v[6:7], off
	v_lshl_add_u64 v[4:5], v[4:5], 0, s[30:31]
	s_mov_b32 m0, s43
	s_add_u32 s6, s16, 0x4080
	global_load_lds_dwordx4 v[4:5], off
	v_lshl_add_u64 v[2:3], v[2:3], 0, s[30:31]
	s_mov_b32 m0, s44
	s_addc_u32 s7, s17, 0
	global_load_lds_dwordx4 v[2:3], off
	s_add_i32 m0, s5, 0x1c000
	v_lshl_add_u64 v[2:3], s[6:7], 0, v[132:133]
	global_load_lds_dwordx4 v[2:3], off
	v_lshl_add_u64 v[2:3], s[6:7], 0, v[136:137]
	s_add_i32 m0, s5, 0x1e000
	s_lshl_b32 s6, s8, 6
	global_load_lds_dwordx4 v[2:3], off
	v_lshlrev_b32_e32 v2, 10, v17
	v_lshl_or_b32 v2, s9, 16, v2
	v_or3_b32 v145, v2, s6, v18
	v_lshlrev_b32_e32 v2, 14, v10
	v_and_b32_e32 v2, 0xffff8000, v2
	v_lshl_add_u32 v2, v11, 11, v2
	v_and_b32_e32 v3, 1, v10
	v_lshl_or_b32 v2, v3, 6, v2
	v_lshl_add_u32 v140, v13, 1, v2
	v_lshlrev_b32_e32 v2, 14, v12
	v_and_b32_e32 v2, 0xffff8000, v2
	s_waitcnt vmcnt(6)
	v_lshl_add_u32 v2, v14, 11, v2
	v_and_b32_e32 v3, 1, v12
	v_lshl_or_b32 v2, v3, 6, v2
	v_mov_b32_e32 v141, v131
	v_lshl_add_u32 v142, v15, 1, v2
	v_mov_b32_e32 v143, v131
	s_mov_b32 s45, 0
	v_add_u32_e32 v146, 0, v20
	s_mov_b64 s[10:11], s[14:15]
	s_mov_b64 s[12:13], s[16:17]
	s_barrier

.LBB0_1028:
	s_add_u32 s16, s14, 0xfffc0080
	s_addc_u32 s17, s15, -1
	s_cmp_eq_u32 s51, 12
	s_cselect_b32 s19, s11, s17
	s_cselect_b32 s18, s10, s16
	s_cselect_b32 s17, s13, s50
	s_cselect_b32 s16, s12, s9
	s_add_i32 s53, 0, 0x10000
	v_add_u32_e32 v130, s53, v144
	ds_read_b128 v[148:151], v130
	ds_read_b128 v[152:155], v130 offset:1024
	ds_read_b128 v[156:159], v130 offset:2048
	ds_read_b128 v[160:163], v130 offset:3072
	v_lshl_add_u64 v[198:199], s[14:15], 0, v[140:141]
	s_add_i32 m0, s5, 0xc000
	ds_read_b128 v[164:167], v146
	ds_read_b128 v[168:171], v146 offset:1024
	ds_read_b128 v[172:175], v146 offset:2048
	ds_read_b128 v[178:181], v146 offset:3072
	ds_read_b128 v[182:185], v146 offset:4096
	ds_read_b128 v[186:189], v146 offset:5120
	ds_read_b128 v[190:193], v146 offset:6144
	ds_read_b128 v[194:197], v146 offset:7168
	global_load_lds_dwordx4 v[198:199], off
	v_lshl_add_u64 v[198:199], s[14:15], 0, v[142:143]
	s_add_i32 m0, s5, 0xe000
	s_nop 0
	global_load_lds_dwordx4 v[198:199], off
	s_waitcnt lgkmcnt(8)
	s_waitcnt vmcnt(10)
	s_barrier
	s_waitcnt lgkmcnt(7)
	v_mfma_f32_16x16x32_bf16 v[126:129], v[148:151], v[164:167], v[126:129]
	s_waitcnt lgkmcnt(5)
	v_mfma_f32_16x16x32_bf16 v[122:125], v[156:159], v[164:167], v[122:125]
	v_mfma_f32_16x16x32_bf16 v[118:121], v[148:151], v[172:175], v[118:121]
	s_waitcnt lgkmcnt(3)
	v_mfma_f32_16x16x32_bf16 v[114:117], v[156:159], v[172:175], v[114:117]
	v_mfma_f32_16x16x32_bf16 v[102:105], v[148:151], v[182:185], v[102:105]
	s_waitcnt lgkmcnt(1)
	v_mfma_f32_16x16x32_bf16 v[98:101], v[156:159], v[182:185], v[98:101]
	v_mfma_f32_16x16x32_bf16 v[86:89], v[148:151], v[190:193], v[86:89]
	v_mfma_f32_16x16x32_bf16 v[82:85], v[156:159], v[190:193], v[82:85]
	v_mfma_f32_16x16x32_bf16 v[126:129], v[152:155], v[168:171], v[126:129]
	v_mfma_f32_16x16x32_bf16 v[122:125], v[160:163], v[168:171], v[122:125]
	v_mfma_f32_16x16x32_bf16 v[118:121], v[152:155], v[178:181], v[118:121]
	v_mfma_f32_16x16x32_bf16 v[114:117], v[160:163], v[178:181], v[114:117]
	v_mfma_f32_16x16x32_bf16 v[102:105], v[152:155], v[186:189], v[102:105]
	s_waitcnt lgkmcnt(0)
	v_mfma_f32_16x16x32_bf16 v[98:101], v[160:163], v[186:189], v[98:101]
	v_mfma_f32_16x16x32_bf16 v[86:89], v[152:155], v[194:197], v[86:89]
	v_mfma_f32_16x16x32_bf16 v[82:85], v[160:163], v[194:197], v[82:85]
	s_barrier
	s_add_i32 s57, 0, 0x14000
	s_add_i32 s53, s53, s35
	v_add_u32_e32 v130, s57, v144
	v_lshl_add_u64 v[230:231], s[16:17], 0, v[132:133]
	s_mov_b32 m0, s53
	ds_read_b128 v[198:201], v130
	ds_read_b128 v[218:221], v130 offset:1024
	ds_read_b128 v[222:225], v130 offset:2048
	ds_read_b128 v[226:229], v130 offset:3072
	global_load_lds_dwordx4 v[230:231], off
	v_lshl_add_u64 v[232:233], s[16:17], 0, v[136:137]
	s_add_i32 m0, s53, 0x2000
	s_nop 0
	global_load_lds_dwordx4 v[232:233], off
	s_waitcnt vmcnt(10)
	s_barrier
	s_waitcnt lgkmcnt(3)
	s_waitcnt lgkmcnt(1)
	v_mfma_f32_16x16x32_bf16 v[110:113], v[198:201], v[164:167], v[110:113]
	v_mfma_f32_16x16x32_bf16 v[106:109], v[222:225], v[164:167], v[106:109]
	v_mfma_f32_16x16x32_bf16 v[94:97], v[198:201], v[172:175], v[94:97]
	v_mfma_f32_16x16x32_bf16 v[90:93], v[222:225], v[172:175], v[90:93]
	v_mfma_f32_16x16x32_bf16 v[78:81], v[198:201], v[182:185], v[78:81]
	v_mfma_f32_16x16x32_bf16 v[74:77], v[222:225], v[182:185], v[74:77]
	v_mfma_f32_16x16x32_bf16 v[70:73], v[198:201], v[190:193], v[70:73]
	v_mfma_f32_16x16x32_bf16 v[66:69], v[222:225], v[190:193], v[66:69]
	s_waitcnt lgkmcnt(0)
	v_mfma_f32_16x16x32_bf16 v[110:113], v[218:221], v[168:171], v[110:113]
	v_mfma_f32_16x16x32_bf16 v[106:109], v[226:229], v[168:171], v[106:109]
	v_mfma_f32_16x16x32_bf16 v[94:97], v[218:221], v[178:181], v[94:97]
	v_mfma_f32_16x16x32_bf16 v[90:93], v[226:229], v[178:181], v[90:93]
	v_mfma_f32_16x16x32_bf16 v[78:81], v[218:221], v[186:189], v[78:81]
	v_mfma_f32_16x16x32_bf16 v[74:77], v[226:229], v[186:189], v[74:77]
	v_mfma_f32_16x16x32_bf16 v[70:73], v[218:221], v[194:197], v[70:73]
	v_mfma_f32_16x16x32_bf16 v[66:69], v[226:229], v[194:197], v[66:69]
	s_mov_b32 m0, s5
	v_lshl_add_u64 v[234:235], s[18:19], 0, v[134:135]
	s_barrier
	ds_read_b128 v[164:167], v146 offset:16384
	ds_read_b128 v[168:171], v146 offset:17408
	ds_read_b128 v[172:175], v146 offset:18432
	ds_read_b128 v[178:181], v146 offset:19456
	ds_read_b128 v[182:185], v146 offset:20480
	ds_read_b128 v[186:189], v146 offset:21504
	ds_read_b128 v[190:193], v146 offset:22528
	ds_read_b128 v[194:197], v146 offset:23552
	global_load_lds_dwordx4 v[234:235], off
	v_lshl_add_u64 v[236:237], s[18:19], 0, v[138:139]
	s_mov_b32 m0, s36
	s_nop 0
	global_load_lds_dwordx4 v[236:237], off
	s_barrier
	s_waitcnt lgkmcnt(7)
	v_mfma_f32_16x16x32_bf16 v[54:57], v[148:151], v[164:167], v[54:57]
	s_waitcnt lgkmcnt(5)
	v_mfma_f32_16x16x32_bf16 v[50:53], v[156:159], v[164:167], v[50:53]
	v_mfma_f32_16x16x32_bf16 v[38:41], v[148:151], v[172:175], v[38:41]
	s_waitcnt lgkmcnt(3)
	v_mfma_f32_16x16x32_bf16 v[34:37], v[156:159], v[172:175], v[34:37]
	v_mfma_f32_16x16x32_bf16 v[22:25], v[148:151], v[182:185], v[22:25]
	s_waitcnt lgkmcnt(1)
	v_mfma_f32_16x16x32_bf16 v[18:21], v[156:159], v[182:185], v[18:21]
	v_mfma_f32_16x16x32_bf16 v[6:9], v[148:151], v[190:193], v[6:9]
	v_mfma_f32_16x16x32_bf16 v[2:5], v[156:159], v[190:193], v[2:5]
	v_mfma_f32_16x16x32_bf16 v[54:57], v[152:155], v[168:171], v[54:57]
	v_mfma_f32_16x16x32_bf16 v[50:53], v[160:163], v[168:171], v[50:53]
	v_mfma_f32_16x16x32_bf16 v[38:41], v[152:155], v[178:181], v[38:41]
	v_mfma_f32_16x16x32_bf16 v[34:37], v[160:163], v[178:181], v[34:37]
	v_mfma_f32_16x16x32_bf16 v[22:25], v[152:155], v[186:189], v[22:25]
	s_waitcnt lgkmcnt(0)
	v_mfma_f32_16x16x32_bf16 v[18:21], v[160:163], v[186:189], v[18:21]
	v_mfma_f32_16x16x32_bf16 v[6:9], v[152:155], v[194:197], v[6:9]
	v_mfma_f32_16x16x32_bf16 v[2:5], v[160:163], v[194:197], v[2:5]
	s_barrier
	s_add_u32 s58, s16, 0x4000
	s_addc_u32 s59, s17, 0
	s_add_i32 s53, s57, s35
	v_lshl_add_u64 v[148:149], s[58:59], 0, v[132:133]
	s_mov_b32 m0, s53
	s_nop 0
	global_load_lds_dwordx4 v[148:149], off
	v_lshl_add_u64 v[148:149], s[58:59], 0, v[136:137]
	s_add_i32 m0, s53, 0x2000
	s_nop 0
	global_load_lds_dwordx4 v[148:149], off
	s_waitcnt vmcnt(10)
	s_barrier
	v_mfma_f32_16x16x32_bf16 v[30:33], v[198:201], v[164:167], v[30:33]
	v_mfma_f32_16x16x32_bf16 v[26:29], v[222:225], v[164:167], v[26:29]
	v_mfma_f32_16x16x32_bf16 v[14:17], v[198:201], v[172:175], v[14:17]
	v_mfma_f32_16x16x32_bf16 v[10:13], v[222:225], v[172:175], v[10:13]
	v_mfma_f32_16x16x32_bf16 v[58:61], v[198:201], v[182:185], v[58:61]
	v_mfma_f32_16x16x32_bf16 v[62:65], v[222:225], v[182:185], v[62:65]
	v_mfma_f32_16x16x32_bf16 v[42:45], v[198:201], v[190:193], v[42:45]
	v_mfma_f32_16x16x32_bf16 v[46:49], v[222:225], v[190:193], v[46:49]
	v_mfma_f32_16x16x32_bf16 v[30:33], v[218:221], v[168:171], v[30:33]
	v_mfma_f32_16x16x32_bf16 v[26:29], v[226:229], v[168:171], v[26:29]
	v_mfma_f32_16x16x32_bf16 v[14:17], v[218:221], v[178:181], v[14:17]
	v_mfma_f32_16x16x32_bf16 v[10:13], v[226:229], v[178:181], v[10:13]
	v_mfma_f32_16x16x32_bf16 v[58:61], v[218:221], v[186:189], v[58:61]
	v_mfma_f32_16x16x32_bf16 v[62:65], v[226:229], v[186:189], v[62:65]
	v_mfma_f32_16x16x32_bf16 v[42:45], v[218:221], v[194:197], v[42:45]
	v_mfma_f32_16x16x32_bf16 v[46:49], v[226:229], v[194:197], v[46:49]
	s_add_i32 s53, 0, 0x18000
	v_add_u32_e32 v130, s53, v144
	s_barrier
	ds_read_b128 v[148:151], v130
	ds_read_b128 v[152:155], v130 offset:1024
	ds_read_b128 v[156:159], v130 offset:2048
	ds_read_b128 v[160:163], v130 offset:3072
	s_add_u32 s18, s18, 0x40000
	s_addc_u32 s19, s19, 0
	s_mov_b32 m0, s37
	v_lshl_add_u64 v[198:199], s[18:19], 0, v[134:135]
	ds_read_b128 v[164:167], v146 offset:32768
	ds_read_b128 v[168:171], v146 offset:33792
	ds_read_b128 v[172:175], v146 offset:34816
	ds_read_b128 v[178:181], v146 offset:35840
	ds_read_b128 v[182:185], v146 offset:36864
	ds_read_b128 v[186:189], v146 offset:37888
	ds_read_b128 v[190:193], v146 offset:38912
	ds_read_b128 v[194:197], v146 offset:39936
	global_load_lds_dwordx4 v[198:199], off
	v_lshl_add_u64 v[198:199], s[18:19], 0, v[138:139]
	s_mov_b32 m0, s38
	s_nop 0
	global_load_lds_dwordx4 v[198:199], off
	s_waitcnt lgkmcnt(8)
	s_waitcnt vmcnt(10)
	s_barrier
	s_waitcnt lgkmcnt(7)
	v_mfma_f32_16x16x32_bf16 v[126:129], v[148:151], v[164:167], v[126:129]
	s_waitcnt lgkmcnt(5)
	v_mfma_f32_16x16x32_bf16 v[122:125], v[156:159], v[164:167], v[122:125]
	v_mfma_f32_16x16x32_bf16 v[118:121], v[148:151], v[172:175], v[118:121]
	s_waitcnt lgkmcnt(3)
	v_mfma_f32_16x16x32_bf16 v[114:117], v[156:159], v[172:175], v[114:117]
	v_mfma_f32_16x16x32_bf16 v[102:105], v[148:151], v[182:185], v[102:105]
	s_waitcnt lgkmcnt(1)
	v_mfma_f32_16x16x32_bf16 v[98:101], v[156:159], v[182:185], v[98:101]
	v_mfma_f32_16x16x32_bf16 v[86:89], v[148:151], v[190:193], v[86:89]
	v_mfma_f32_16x16x32_bf16 v[82:85], v[156:159], v[190:193], v[82:85]
	v_mfma_f32_16x16x32_bf16 v[126:129], v[152:155], v[168:171], v[126:129]
	v_mfma_f32_16x16x32_bf16 v[122:125], v[160:163], v[168:171], v[122:125]
	v_mfma_f32_16x16x32_bf16 v[118:121], v[152:155], v[178:181], v[118:121]
	v_mfma_f32_16x16x32_bf16 v[114:117], v[160:163], v[178:181], v[114:117]
	v_mfma_f32_16x16x32_bf16 v[102:105], v[152:155], v[186:189], v[102:105]
	s_waitcnt lgkmcnt(0)
	v_mfma_f32_16x16x32_bf16 v[98:101], v[160:163], v[186:189], v[98:101]
	v_mfma_f32_16x16x32_bf16 v[86:89], v[152:155], v[194:197], v[86:89]
	v_mfma_f32_16x16x32_bf16 v[82:85], v[160:163], v[194:197], v[82:85]
	s_barrier
	s_add_i32 s18, 0, 0x1c000
	s_add_i32 s19, s53, s35
	v_add_u32_e32 v130, s18, v144
	v_lshl_add_u64 v[230:231], v[230:231], 0, s[30:31]
	s_mov_b32 m0, s19
	ds_read_b128 v[198:201], v130
	ds_read_b128 v[218:221], v130 offset:1024
	ds_read_b128 v[222:225], v130 offset:2048
	ds_read_b128 v[226:229], v130 offset:3072
	global_load_lds_dwordx4 v[230:231], off
	v_lshl_add_u64 v[230:231], v[232:233], 0, s[30:31]
	s_add_i32 m0, s19, 0x2000
	s_nop 0
	global_load_lds_dwordx4 v[230:231], off
	s_waitcnt vmcnt(10)
	s_barrier
	s_waitcnt lgkmcnt(3)
	s_waitcnt lgkmcnt(1)
	v_mfma_f32_16x16x32_bf16 v[110:113], v[198:201], v[164:167], v[110:113]
	v_mfma_f32_16x16x32_bf16 v[106:109], v[222:225], v[164:167], v[106:109]
	v_mfma_f32_16x16x32_bf16 v[94:97], v[198:201], v[172:175], v[94:97]
	v_mfma_f32_16x16x32_bf16 v[90:93], v[222:225], v[172:175], v[90:93]
	v_mfma_f32_16x16x32_bf16 v[78:81], v[198:201], v[182:185], v[78:81]
	v_mfma_f32_16x16x32_bf16 v[74:77], v[222:225], v[182:185], v[74:77]
	v_mfma_f32_16x16x32_bf16 v[70:73], v[198:201], v[190:193], v[70:73]
	v_mfma_f32_16x16x32_bf16 v[66:69], v[222:225], v[190:193], v[66:69]
	s_waitcnt lgkmcnt(0)
	v_mfma_f32_16x16x32_bf16 v[110:113], v[218:221], v[168:171], v[110:113]
	v_mfma_f32_16x16x32_bf16 v[106:109], v[226:229], v[168:171], v[106:109]
	v_mfma_f32_16x16x32_bf16 v[94:97], v[218:221], v[178:181], v[94:97]
	v_mfma_f32_16x16x32_bf16 v[90:93], v[226:229], v[178:181], v[90:93]
	v_mfma_f32_16x16x32_bf16 v[78:81], v[218:221], v[186:189], v[78:81]
	v_mfma_f32_16x16x32_bf16 v[74:77], v[226:229], v[186:189], v[74:77]
	v_mfma_f32_16x16x32_bf16 v[70:73], v[218:221], v[194:197], v[70:73]
	v_mfma_f32_16x16x32_bf16 v[66:69], v[226:229], v[194:197], v[66:69]
	s_mov_b32 m0, s43
	v_lshl_add_u64 v[230:231], v[234:235], 0, s[30:31]
	s_barrier
	ds_read_b128 v[164:167], v146 offset:49152
	ds_read_b128 v[168:171], v146 offset:50176
	ds_read_b128 v[172:175], v146 offset:51200
	ds_read_b128 v[178:181], v146 offset:52224
	ds_read_b128 v[182:185], v146 offset:53248
	ds_read_b128 v[186:189], v146 offset:54272
	ds_read_b128 v[190:193], v146 offset:55296
	ds_read_b128 v[194:197], v146 offset:56320
	global_load_lds_dwordx4 v[230:231], off
	v_lshl_add_u64 v[230:231], v[236:237], 0, s[30:31]
	s_mov_b32 m0, s44
	s_nop 0
	global_load_lds_dwordx4 v[230:231], off
	s_barrier
	s_waitcnt lgkmcnt(7)
	v_mfma_f32_16x16x32_bf16 v[54:57], v[148:151], v[164:167], v[54:57]
	s_waitcnt lgkmcnt(5)
	v_mfma_f32_16x16x32_bf16 v[50:53], v[156:159], v[164:167], v[50:53]
	v_mfma_f32_16x16x32_bf16 v[38:41], v[148:151], v[172:175], v[38:41]
	s_waitcnt lgkmcnt(3)
	v_mfma_f32_16x16x32_bf16 v[34:37], v[156:159], v[172:175], v[34:37]
	v_mfma_f32_16x16x32_bf16 v[22:25], v[148:151], v[182:185], v[22:25]
	s_waitcnt lgkmcnt(1)
	v_mfma_f32_16x16x32_bf16 v[18:21], v[156:159], v[182:185], v[18:21]
	v_mfma_f32_16x16x32_bf16 v[6:9], v[148:151], v[190:193], v[6:9]
	v_mfma_f32_16x16x32_bf16 v[2:5], v[156:159], v[190:193], v[2:5]
	v_mfma_f32_16x16x32_bf16 v[54:57], v[152:155], v[168:171], v[54:57]
	v_mfma_f32_16x16x32_bf16 v[50:53], v[160:163], v[168:171], v[50:53]
	v_mfma_f32_16x16x32_bf16 v[38:41], v[152:155], v[178:181], v[38:41]
	v_mfma_f32_16x16x32_bf16 v[34:37], v[160:163], v[178:181], v[34:37]
	v_mfma_f32_16x16x32_bf16 v[22:25], v[152:155], v[186:189], v[22:25]
	s_waitcnt lgkmcnt(0)
	v_mfma_f32_16x16x32_bf16 v[18:21], v[160:163], v[186:189], v[18:21]
	v_mfma_f32_16x16x32_bf16 v[6:9], v[152:155], v[194:197], v[6:9]
	v_mfma_f32_16x16x32_bf16 v[2:5], v[160:163], v[194:197], v[2:5]
	s_barrier
	s_add_u32 s16, s16, 0x4080
	s_addc_u32 s17, s17, 0
	s_add_i32 s18, s18, s35
	v_lshl_add_u64 v[148:149], s[16:17], 0, v[132:133]
	s_mov_b32 m0, s18
	s_nop 0
	global_load_lds_dwordx4 v[148:149], off
	v_lshl_add_u64 v[148:149], s[16:17], 0, v[136:137]
	s_add_i32 m0, s18, 0x2000
	s_nop 0
	global_load_lds_dwordx4 v[148:149], off
	s_waitcnt vmcnt(10)
	s_barrier
	v_mfma_f32_16x16x32_bf16 v[30:33], v[198:201], v[164:167], v[30:33]
	v_mfma_f32_16x16x32_bf16 v[26:29], v[222:225], v[164:167], v[26:29]
	v_mfma_f32_16x16x32_bf16 v[14:17], v[198:201], v[172:175], v[14:17]
	v_mfma_f32_16x16x32_bf16 v[10:13], v[222:225], v[172:175], v[10:13]
	v_mfma_f32_16x16x32_bf16 v[58:61], v[198:201], v[182:185], v[58:61]
	v_mfma_f32_16x16x32_bf16 v[62:65], v[222:225], v[182:185], v[62:65]
	v_mfma_f32_16x16x32_bf16 v[42:45], v[198:201], v[190:193], v[42:45]
	v_mfma_f32_16x16x32_bf16 v[46:49], v[222:225], v[190:193], v[46:49]
	v_mfma_f32_16x16x32_bf16 v[30:33], v[218:221], v[168:171], v[30:33]
	v_mfma_f32_16x16x32_bf16 v[26:29], v[226:229], v[168:171], v[26:29]
	v_mfma_f32_16x16x32_bf16 v[14:17], v[218:221], v[178:181], v[14:17]
	v_mfma_f32_16x16x32_bf16 v[10:13], v[226:229], v[178:181], v[10:13]
	v_mfma_f32_16x16x32_bf16 v[58:61], v[218:221], v[186:189], v[58:61]
	v_mfma_f32_16x16x32_bf16 v[62:65], v[226:229], v[186:189], v[62:65]
	v_mfma_f32_16x16x32_bf16 v[42:45], v[218:221], v[194:197], v[42:45]
	v_mfma_f32_16x16x32_bf16 v[46:49], v[226:229], v[194:197], v[46:49]
	s_add_i32 s51, s51, 2
	s_add_u32 s14, s14, 0x100
	s_addc_u32 s15, s15, 0
	s_add_u32 s9, s9, 0x100
	s_addc_u32 s50, s50, 0
	s_cmp_gt_u32 s51, 13
	s_barrier
	s_cbranch_scc0 .LBB0_1028
	s_lshl_b32 s14, s4, 8
	s_ashr_i32 s15, s14, 31
	s_lshl_b64 s[14:15], s[14:15], 11
	s_add_u32 s4, s39, s14
	s_addc_u32 s9, s42, s15
	s_lshl_b32 s14, s47, 8
	s_ashr_i32 s15, s14, 31
	s_lshl_b64 s[14:15], s[14:15], 1
	s_add_u32 s14, s4, s14
	s_addc_u32 s15, s9, s15
	v_mov_b32_e32 v130, v145
	v_cvt_pk_bf16_f32 v110, v110, v111
	v_lshl_add_u64 v[148:149], v[130:131], 1, s[14:15]
	v_cvt_pk_bf16_f32 v111, v112, v113
	v_cvt_pk_bf16_f32 v112, v106, v107
	v_cvt_pk_bf16_f32 v113, v108, v109
	s_mov_b32 s4, 0x8000
	global_store_dwordx4 v[148:149], v[110:113], off offset:16
	v_cvt_pk_bf16_f32 v94, v94, v95
	v_cvt_pk_bf16_f32 v95, v96, v97
	v_add_co_u32_e32 v110, vcc, s4, v148
	v_cvt_pk_bf16_f32 v96, v90, v91
	s_nop 0
	v_addc_co_u32_e32 v111, vcc, 0, v149, vcc
	v_cvt_pk_bf16_f32 v97, v92, v93
	s_mov_b32 s4, 0x10000
	global_store_dwordx4 v[110:111], v[94:97], off offset:16
	v_cvt_pk_bf16_f32 v78, v78, v79
	v_cvt_pk_bf16_f32 v79, v80, v81
	v_add_co_u32_e32 v94, vcc, s4, v148
	v_cvt_pk_bf16_f32 v80, v74, v75
	s_nop 0
	v_addc_co_u32_e32 v95, vcc, 0, v149, vcc
	v_cvt_pk_bf16_f32 v81, v76, v77
	s_mov_b32 s4, 0x18000
	global_store_dwordx4 v[94:95], v[78:81], off offset:16
	v_cvt_pk_bf16_f32 v54, v54, v55
	v_cvt_pk_bf16_f32 v55, v56, v57
	v_add_co_u32_e32 v78, vcc, s4, v148
	s_mov_b32 s4, 0x40000
	s_nop 0
	v_addc_co_u32_e32 v79, vcc, 0, v149, vcc
	v_cvt_pk_bf16_f32 v56, v50, v51
	v_add_co_u32_e32 v50, vcc, s4, v148
	v_cvt_pk_bf16_f32 v30, v30, v31
	s_nop 0
	v_addc_co_u32_e32 v51, vcc, 0, v149, vcc
	v_cvt_pk_bf16_f32 v31, v32, v33
	v_cvt_pk_bf16_f32 v32, v26, v27
	v_cvt_pk_bf16_f32 v33, v28, v29
	s_mov_b32 s4, 0x48000
	global_store_dwordx4 v[50:51], v[30:33], off offset:16
	v_cvt_pk_bf16_f32 v14, v14, v15
	v_cvt_pk_bf16_f32 v15, v16, v17
	v_add_co_u32_e32 v30, vcc, s4, v148
	v_cvt_pk_bf16_f32 v16, v10, v11
	s_nop 0
	v_addc_co_u32_e32 v31, vcc, 0, v149, vcc
	v_cvt_pk_bf16_f32 v17, v12, v13
	s_mov_b32 s4, 0x50000
	global_store_dwordx4 v[30:31], v[14:17], off offset:16
	v_cvt_pk_bf16_f32 v10, v22, v23
	v_cvt_pk_bf16_f32 v11, v24, v25
	v_add_co_u32_e32 v14, vcc, s4, v148
	v_cvt_pk_bf16_f32 v12, v18, v19
	v_cvt_pk_bf16_f32 v13, v20, v21
	v_addc_co_u32_e32 v15, vcc, 0, v149, vcc
	global_store_dwordx4 v[14:15], v[10:13], off
	s_mov_b32 s4, 0x58000
	v_cvt_pk_bf16_f32 v126, v126, v127
	v_cvt_pk_bf16_f32 v10, v58, v59
	v_cvt_pk_bf16_f32 v11, v60, v61
	v_cvt_pk_bf16_f32 v12, v62, v63
	v_cvt_pk_bf16_f32 v13, v64, v65
	global_store_dwordx4 v[14:15], v[10:13], off offset:16
	v_cvt_pk_bf16_f32 v127, v128, v129
	v_cvt_pk_bf16_f32 v128, v122, v123
	v_add_co_u32_e32 v10, vcc, s4, v148
	v_cvt_pk_bf16_f32 v129, v124, v125
	s_nop 0
	v_addc_co_u32_e32 v11, vcc, 0, v149, vcc
	v_cvt_pk_bf16_f32 v106, v118, v119
	v_cvt_pk_bf16_f32 v107, v120, v121
	v_cvt_pk_bf16_f32 v108, v114, v115
	v_cvt_pk_bf16_f32 v109, v116, v117
	v_cvt_pk_bf16_f32 v90, v102, v103
	v_cvt_pk_bf16_f32 v91, v104, v105
	v_cvt_pk_bf16_f32 v92, v98, v99
	v_cvt_pk_bf16_f32 v93, v100, v101
	v_cvt_pk_bf16_f32 v74, v86, v87
	v_cvt_pk_bf16_f32 v75, v88, v89
	v_cvt_pk_bf16_f32 v76, v82, v83
	v_cvt_pk_bf16_f32 v77, v84, v85
	v_cvt_pk_bf16_f32 v70, v70, v71
	v_cvt_pk_bf16_f32 v71, v72, v73
	v_cvt_pk_bf16_f32 v72, v66, v67
	v_cvt_pk_bf16_f32 v73, v68, v69
	v_cvt_pk_bf16_f32 v57, v52, v53
	v_cvt_pk_bf16_f32 v26, v38, v39
	v_cvt_pk_bf16_f32 v27, v40, v41
	v_cvt_pk_bf16_f32 v28, v34, v35
	v_cvt_pk_bf16_f32 v29, v36, v37
	v_cvt_pk_bf16_f32 v6, v6, v7
	v_cvt_pk_bf16_f32 v7, v8, v9
	v_cvt_pk_bf16_f32 v8, v2, v3
	v_cvt_pk_bf16_f32 v9, v4, v5
	v_cvt_pk_bf16_f32 v2, v42, v43
	v_cvt_pk_bf16_f32 v3, v44, v45
	v_cvt_pk_bf16_f32 v4, v46, v47
	v_cvt_pk_bf16_f32 v5, v48, v49
	s_and_b64 vcc, exec, s[6:7]
	s_mov_b32 s4, s8
	s_mov_b32 s47, s46
	s_mov_b64 s[16:17], s[12:13]
	s_mov_b64 s[14:15], s[10:11]
	s_mov_b32 s53, 0x42b17218
	global_store_dwordx4 v[148:149], v[126:129], off
	global_store_dwordx4 v[110:111], v[106:109], off
	global_store_dwordx4 v[94:95], v[90:93], off
	global_store_dwordx4 v[78:79], v[74:77], off
	global_store_dwordx4 v[78:79], v[70:73], off offset:16
	global_store_dwordx4 v[50:51], v[54:57], off
	global_store_dwordx4 v[30:31], v[26:29], off
	global_store_dwordx4 v[10:11], v[6:9], off
	global_store_dwordx4 v[10:11], v[2:5], off offset:16
	s_cbranch_vccz .LBB0_1021
	s_waitcnt vmcnt(0)
	s_setprio 0
	s_cmpk_gt_u32 s22, 0xff
	s_cbranch_scc1 .LBB0_1032
	s_barrier

.LBB0_1094:
	s_add_u32 s42, s4, 0x45868000
	s_addc_u32 s43, s5, 0
	s_add_u32 s44, s4, 0x63568000
	v_and_b32_e32 v17, 15, v16
	v_and_b32_e32 v18, 48, v16
	v_lshlrev_b32_e32 v16, 2, v16
	s_sext_i32_i8 s15, s6
	s_addc_u32 s45, s5, 0
	s_and_b32 s6, s7, 3
	v_lshl_or_b32 v19, s8, 6, v17
	s_lshl_b32 s4, s8, 13
	v_lshl_or_b32 v17, v17, 6, v18
	v_and_b32_e32 v16, 32, v16
	s_add_i32 m0, s36, 0x18000
	v_lshl_add_u64 v[8:9], v[8:9], 0, s[30:31]
	v_bitop3_b32 v20, v17, s4, v16 bitop3:0xde
	s_lshl_b32 s4, s6, 12
	s_waitcnt vmcnt(4)
	s_barrier
	v_readfirstlane_b32 s100, v0
	s_cmp_lt_u32 s100, 0x100
	s_cbranch_scc1 .Lmy_sp_mrgL
	s_setprio 1
.Lmy_sp_mrgL:
	global_load_lds_dwordx4 v[8:9], off
	v_lshl_add_u64 v[6:7], v[6:7], 0, s[30:31]
	s_add_i32 m0, s36, 0x1a000
	s_add_i32 s46, s36, 0x8000
	s_add_i32 s47, s36, 0xa000
	v_bitop3_b32 v182, v17, s4, v16 bitop3:0xde
	global_load_lds_dwordx4 v[6:7], off
	v_lshl_add_u64 v[4:5], v[4:5], 0, s[30:31]
	s_mov_b32 m0, s46
	s_add_u32 s4, s62, 0x4080
	global_load_lds_dwordx4 v[4:5], off
	v_lshl_add_u64 v[2:3], v[2:3], 0, s[30:31]
	s_mov_b32 m0, s47
	s_addc_u32 s5, s63, 0
	global_load_lds_dwordx4 v[2:3], off
	s_add_i32 m0, s36, 0x1c000
	v_lshl_add_u64 v[2:3], s[4:5], 0, v[164:165]
	global_load_lds_dwordx4 v[2:3], off
	v_lshl_add_u64 v[2:3], s[4:5], 0, v[168:169]
	s_add_i32 m0, s36, 0x1e000
	s_movk_i32 s4, 0x1e00
	global_load_lds_dwordx4 v[2:3], off
	v_mul_lo_u32 v2, v19, s4
	s_lshl_b32 s4, s6, 6
	v_or3_b32 v183, v2, s4, v18
	v_lshlrev_b32_e32 v2, 10, v19
	v_or3_b32 v184, v2, s4, v18
	v_lshlrev_b32_e32 v2, 14, v10
	v_and_b32_e32 v2, 0xffff8000, v2
	v_lshl_add_u32 v2, v11, 11, v2
	v_and_b32_e32 v3, 1, v10
	v_lshl_or_b32 v2, v3, 6, v2
	v_lshl_add_u32 v172, v13, 1, v2
	v_lshlrev_b32_e32 v2, 14, v12
	v_and_b32_e32 v2, 0xffff8000, v2
	s_waitcnt vmcnt(6)
	v_lshl_add_u32 v2, v14, 11, v2
	v_and_b32_e32 v3, 1, v12
	v_lshl_or_b32 v2, v3, 6, v2
	v_mov_b32_e32 v173, v131
	v_lshl_add_u32 v174, v15, 1, v2
	v_mov_b32_e32 v175, v131
	s_mov_b32 s50, 0
	v_add_u32_e32 v185, 0, v20
	s_mov_b64 s[8:9], s[12:13]
	s_mov_b64 s[10:11], s[62:63]
	s_barrier
	s_branch .LBB0_1096

.LBB0_1103:
	s_add_u32 s58, s12, s62
	s_addc_u32 s59, s13, s63
	s_add_u32 s58, s58, 0x100
	s_addc_u32 s59, s59, 0
	s_add_u32 s60, s7, s62
	s_addc_u32 s61, s53, s63
	s_cmpk_eq_i32 s62, 0x700
	s_cselect_b32 s67, s9, s59
	s_cselect_b32 s66, s8, s58
	s_cselect_b32 s65, s11, s61
	s_cselect_b32 s64, s10, s60
	s_add_i32 s58, 0, 0x10000
	v_add_u32_e32 v130, s58, v182
	ds_read_b128 v[132:135], v130
	ds_read_b128 v[136:139], v130 offset:1024
	ds_read_b128 v[140:143], v130 offset:2048
	ds_read_b128 v[144:147], v130 offset:3072
	v_lshl_add_u64 v[218:219], v[178:179], 0, s[62:63]
	s_add_i32 m0, s36, 0xc000
	ds_read_b128 v[148:151], v185
	ds_read_b128 v[152:155], v185 offset:1024
	ds_read_b128 v[156:159], v185 offset:2048
	ds_read_b128 v[160:163], v185 offset:3072
	ds_read_b128 v[186:189], v185 offset:4096
	ds_read_b128 v[190:193], v185 offset:5120
	ds_read_b128 v[194:197], v185 offset:6144
	ds_read_b128 v[198:201], v185 offset:7168
	global_load_lds_dwordx4 v[218:219], off
	v_lshl_add_u64 v[218:219], v[180:181], 0, s[62:63]
	s_add_i32 m0, s36, 0xe000
	s_nop 0
	global_load_lds_dwordx4 v[218:219], off
	s_waitcnt lgkmcnt(8)
	s_waitcnt vmcnt(10)
	s_barrier
	s_waitcnt lgkmcnt(7)
	v_mfma_f32_16x16x32_bf16 v[126:129], v[132:135], v[148:151], v[126:129]
	s_waitcnt lgkmcnt(5)
	v_mfma_f32_16x16x32_bf16 v[122:125], v[140:143], v[148:151], v[122:125]
	v_mfma_f32_16x16x32_bf16 v[110:113], v[132:135], v[156:159], v[110:113]
	s_waitcnt lgkmcnt(3)
	v_mfma_f32_16x16x32_bf16 v[106:109], v[140:143], v[156:159], v[106:109]
	v_mfma_f32_16x16x32_bf16 v[94:97], v[132:135], v[186:189], v[94:97]
	s_waitcnt lgkmcnt(1)
	v_mfma_f32_16x16x32_bf16 v[90:93], v[140:143], v[186:189], v[90:93]
	v_mfma_f32_16x16x32_bf16 v[78:81], v[132:135], v[194:197], v[78:81]
	v_mfma_f32_16x16x32_bf16 v[74:77], v[140:143], v[194:197], v[74:77]
	v_mfma_f32_16x16x32_bf16 v[126:129], v[136:139], v[152:155], v[126:129]
	v_mfma_f32_16x16x32_bf16 v[122:125], v[144:147], v[152:155], v[122:125]
	v_mfma_f32_16x16x32_bf16 v[110:113], v[136:139], v[160:163], v[110:113]
	v_mfma_f32_16x16x32_bf16 v[106:109], v[144:147], v[160:163], v[106:109]
	v_mfma_f32_16x16x32_bf16 v[94:97], v[136:139], v[190:193], v[94:97]
	s_waitcnt lgkmcnt(0)
	v_mfma_f32_16x16x32_bf16 v[90:93], v[144:147], v[190:193], v[90:93]
	v_mfma_f32_16x16x32_bf16 v[78:81], v[136:139], v[198:201], v[78:81]
	v_mfma_f32_16x16x32_bf16 v[74:77], v[144:147], v[198:201], v[74:77]
	s_barrier
	s_add_i32 s60, 0, 0x14000
	s_add_i32 s58, s58, s35
	v_add_u32_e32 v130, s60, v182
	v_lshl_add_u64 v[234:235], s[64:65], 0, v[164:165]
	s_mov_b32 m0, s58
	ds_read_b128 v[218:221], v130
	ds_read_b128 v[222:225], v130 offset:1024
	ds_read_b128 v[226:229], v130 offset:2048
	ds_read_b128 v[230:233], v130 offset:3072
	global_load_lds_dwordx4 v[234:235], off
	v_lshl_add_u64 v[236:237], s[64:65], 0, v[168:169]
	s_add_i32 m0, s58, 0x2000
	s_nop 0
	global_load_lds_dwordx4 v[236:237], off
	s_waitcnt vmcnt(10)
	s_barrier
	s_waitcnt lgkmcnt(3)
	s_waitcnt lgkmcnt(1)
	v_mfma_f32_16x16x32_bf16 v[118:121], v[218:221], v[148:151], v[118:121]
	v_mfma_f32_16x16x32_bf16 v[114:117], v[226:229], v[148:151], v[114:117]
	v_mfma_f32_16x16x32_bf16 v[102:105], v[218:221], v[156:159], v[102:105]
	v_mfma_f32_16x16x32_bf16 v[98:101], v[226:229], v[156:159], v[98:101]
	v_mfma_f32_16x16x32_bf16 v[86:89], v[218:221], v[186:189], v[86:89]
	v_mfma_f32_16x16x32_bf16 v[82:85], v[226:229], v[186:189], v[82:85]
	v_mfma_f32_16x16x32_bf16 v[70:73], v[218:221], v[194:197], v[70:73]
	v_mfma_f32_16x16x32_bf16 v[66:69], v[226:229], v[194:197], v[66:69]
	s_waitcnt lgkmcnt(0)
	v_mfma_f32_16x16x32_bf16 v[118:121], v[222:225], v[152:155], v[118:121]
	v_mfma_f32_16x16x32_bf16 v[114:117], v[230:233], v[152:155], v[114:117]
	v_mfma_f32_16x16x32_bf16 v[102:105], v[222:225], v[160:163], v[102:105]
	v_mfma_f32_16x16x32_bf16 v[98:101], v[230:233], v[160:163], v[98:101]
	v_mfma_f32_16x16x32_bf16 v[86:89], v[222:225], v[190:193], v[86:89]
	v_mfma_f32_16x16x32_bf16 v[82:85], v[230:233], v[190:193], v[82:85]
	v_mfma_f32_16x16x32_bf16 v[70:73], v[222:225], v[198:201], v[70:73]
	v_mfma_f32_16x16x32_bf16 v[66:69], v[230:233], v[198:201], v[66:69]
	s_mov_b32 m0, s36
	v_lshl_add_u64 v[238:239], s[66:67], 0, v[166:167]
	s_barrier
	ds_read_b128 v[148:151], v185 offset:16384
	ds_read_b128 v[152:155], v185 offset:17408
	ds_read_b128 v[156:159], v185 offset:18432
	ds_read_b128 v[160:163], v185 offset:19456
	ds_read_b128 v[186:189], v185 offset:20480
	ds_read_b128 v[190:193], v185 offset:21504
	ds_read_b128 v[194:197], v185 offset:22528
	ds_read_b128 v[198:201], v185 offset:23552
	global_load_lds_dwordx4 v[238:239], off
	v_lshl_add_u64 v[240:241], s[66:67], 0, v[170:171]
	s_mov_b32 m0, s37
	s_nop 0
	global_load_lds_dwordx4 v[240:241], off
	s_barrier
	s_waitcnt lgkmcnt(7)
	v_mfma_f32_16x16x32_bf16 v[62:65], v[132:135], v[148:151], v[62:65]
	s_waitcnt lgkmcnt(5)
	v_mfma_f32_16x16x32_bf16 v[58:61], v[140:143], v[148:151], v[58:61]
	v_mfma_f32_16x16x32_bf16 v[46:49], v[132:135], v[156:159], v[46:49]
	s_waitcnt lgkmcnt(3)
	v_mfma_f32_16x16x32_bf16 v[42:45], v[140:143], v[156:159], v[42:45]
	v_mfma_f32_16x16x32_bf16 v[30:33], v[132:135], v[186:189], v[30:33]
	s_waitcnt lgkmcnt(1)
	v_mfma_f32_16x16x32_bf16 v[26:29], v[140:143], v[186:189], v[26:29]
	v_mfma_f32_16x16x32_bf16 v[14:17], v[132:135], v[194:197], v[14:17]
	v_mfma_f32_16x16x32_bf16 v[10:13], v[140:143], v[194:197], v[10:13]
	v_mfma_f32_16x16x32_bf16 v[62:65], v[136:139], v[152:155], v[62:65]
	v_mfma_f32_16x16x32_bf16 v[58:61], v[144:147], v[152:155], v[58:61]
	v_mfma_f32_16x16x32_bf16 v[46:49], v[136:139], v[160:163], v[46:49]
	v_mfma_f32_16x16x32_bf16 v[42:45], v[144:147], v[160:163], v[42:45]
	v_mfma_f32_16x16x32_bf16 v[30:33], v[136:139], v[190:193], v[30:33]
	s_waitcnt lgkmcnt(0)
	v_mfma_f32_16x16x32_bf16 v[26:29], v[144:147], v[190:193], v[26:29]
	v_mfma_f32_16x16x32_bf16 v[14:17], v[136:139], v[198:201], v[14:17]
	v_mfma_f32_16x16x32_bf16 v[10:13], v[144:147], v[198:201], v[10:13]
	s_barrier
	s_add_u32 s58, s64, 0x4000
	s_addc_u32 s59, s65, 0
	s_add_i32 s60, s60, s35
	v_lshl_add_u64 v[132:133], s[58:59], 0, v[164:165]
	s_mov_b32 m0, s60
	s_nop 0
	global_load_lds_dwordx4 v[132:133], off
	v_lshl_add_u64 v[132:133], s[58:59], 0, v[168:169]
	s_add_i32 m0, s60, 0x2000
	s_nop 0
	global_load_lds_dwordx4 v[132:133], off
	s_waitcnt vmcnt(10)
	s_barrier
	v_mfma_f32_16x16x32_bf16 v[54:57], v[218:221], v[148:151], v[54:57]
	v_mfma_f32_16x16x32_bf16 v[50:53], v[226:229], v[148:151], v[50:53]
	v_mfma_f32_16x16x32_bf16 v[38:41], v[218:221], v[156:159], v[38:41]
	v_mfma_f32_16x16x32_bf16 v[34:37], v[226:229], v[156:159], v[34:37]
	v_mfma_f32_16x16x32_bf16 v[22:25], v[218:221], v[186:189], v[22:25]
	v_mfma_f32_16x16x32_bf16 v[18:21], v[226:229], v[186:189], v[18:21]
	v_mfma_f32_16x16x32_bf16 v[6:9], v[218:221], v[194:197], v[6:9]
	v_mfma_f32_16x16x32_bf16 v[2:5], v[226:229], v[194:197], v[2:5]
	v_mfma_f32_16x16x32_bf16 v[54:57], v[222:225], v[152:155], v[54:57]
	v_mfma_f32_16x16x32_bf16 v[50:53], v[230:233], v[152:155], v[50:53]
	v_mfma_f32_16x16x32_bf16 v[38:41], v[222:225], v[160:163], v[38:41]
	v_mfma_f32_16x16x32_bf16 v[34:37], v[230:233], v[160:163], v[34:37]
	v_mfma_f32_16x16x32_bf16 v[22:25], v[222:225], v[190:193], v[22:25]
	v_mfma_f32_16x16x32_bf16 v[18:21], v[230:233], v[190:193], v[18:21]
	v_mfma_f32_16x16x32_bf16 v[6:9], v[222:225], v[198:201], v[6:9]
	v_mfma_f32_16x16x32_bf16 v[2:5], v[230:233], v[198:201], v[2:5]
	s_add_i32 s60, 0, 0x18000
	v_add_u32_e32 v130, s60, v182
	s_barrier
	ds_read_b128 v[132:135], v130
	ds_read_b128 v[136:139], v130 offset:1024
	ds_read_b128 v[140:143], v130 offset:2048
	ds_read_b128 v[144:147], v130 offset:3072
	s_add_u32 s58, s66, 0x40000
	s_addc_u32 s59, s67, 0
	s_mov_b32 m0, s38
	v_lshl_add_u64 v[218:219], s[58:59], 0, v[166:167]
	ds_read_b128 v[148:151], v185 offset:32768
	ds_read_b128 v[152:155], v185 offset:33792
	ds_read_b128 v[156:159], v185 offset:34816
	ds_read_b128 v[160:163], v185 offset:35840
	ds_read_b128 v[186:189], v185 offset:36864
	ds_read_b128 v[190:193], v185 offset:37888
	ds_read_b128 v[194:197], v185 offset:38912
	ds_read_b128 v[198:201], v185 offset:39936
	global_load_lds_dwordx4 v[218:219], off
	v_lshl_add_u64 v[218:219], s[58:59], 0, v[170:171]
	s_mov_b32 m0, s39
	s_nop 0
	global_load_lds_dwordx4 v[218:219], off
	s_waitcnt lgkmcnt(8)
	s_waitcnt vmcnt(10)
	s_barrier
	s_waitcnt lgkmcnt(7)
	v_mfma_f32_16x16x32_bf16 v[126:129], v[132:135], v[148:151], v[126:129]
	s_waitcnt lgkmcnt(5)
	v_mfma_f32_16x16x32_bf16 v[122:125], v[140:143], v[148:151], v[122:125]
	v_mfma_f32_16x16x32_bf16 v[110:113], v[132:135], v[156:159], v[110:113]
	s_waitcnt lgkmcnt(3)
	v_mfma_f32_16x16x32_bf16 v[106:109], v[140:143], v[156:159], v[106:109]
	v_mfma_f32_16x16x32_bf16 v[94:97], v[132:135], v[186:189], v[94:97]
	s_waitcnt lgkmcnt(1)
	v_mfma_f32_16x16x32_bf16 v[90:93], v[140:143], v[186:189], v[90:93]
	v_mfma_f32_16x16x32_bf16 v[78:81], v[132:135], v[194:197], v[78:81]
	v_mfma_f32_16x16x32_bf16 v[74:77], v[140:143], v[194:197], v[74:77]
	v_mfma_f32_16x16x32_bf16 v[126:129], v[136:139], v[152:155], v[126:129]
	v_mfma_f32_16x16x32_bf16 v[122:125], v[144:147], v[152:155], v[122:125]
	v_mfma_f32_16x16x32_bf16 v[110:113], v[136:139], v[160:163], v[110:113]
	v_mfma_f32_16x16x32_bf16 v[106:109], v[144:147], v[160:163], v[106:109]
	v_mfma_f32_16x16x32_bf16 v[94:97], v[136:139], v[190:193], v[94:97]
	s_waitcnt lgkmcnt(0)
	v_mfma_f32_16x16x32_bf16 v[90:93], v[144:147], v[190:193], v[90:93]
	v_mfma_f32_16x16x32_bf16 v[78:81], v[136:139], v[198:201], v[78:81]
	v_mfma_f32_16x16x32_bf16 v[74:77], v[144:147], v[198:201], v[74:77]
	s_barrier
	s_add_i32 s61, 0, 0x1c000
	s_add_i32 s58, s60, s35
	v_add_u32_e32 v130, s61, v182
	v_lshl_add_u64 v[234:235], v[234:235], 0, s[30:31]
	s_mov_b32 m0, s58
	ds_read_b128 v[218:221], v130
	ds_read_b128 v[222:225], v130 offset:1024
	ds_read_b128 v[226:229], v130 offset:2048
	ds_read_b128 v[230:233], v130 offset:3072
	global_load_lds_dwordx4 v[234:235], off
	v_lshl_add_u64 v[234:235], v[236:237], 0, s[30:31]
	s_add_i32 m0, s58, 0x2000
	s_nop 0
	global_load_lds_dwordx4 v[234:235], off
	s_waitcnt vmcnt(10)
	s_barrier
	s_waitcnt lgkmcnt(3)
	s_waitcnt lgkmcnt(1)
	v_mfma_f32_16x16x32_bf16 v[118:121], v[218:221], v[148:151], v[118:121]
	v_mfma_f32_16x16x32_bf16 v[114:117], v[226:229], v[148:151], v[114:117]
	v_mfma_f32_16x16x32_bf16 v[102:105], v[218:221], v[156:159], v[102:105]
	v_mfma_f32_16x16x32_bf16 v[98:101], v[226:229], v[156:159], v[98:101]
	v_mfma_f32_16x16x32_bf16 v[86:89], v[218:221], v[186:189], v[86:89]
	v_mfma_f32_16x16x32_bf16 v[82:85], v[226:229], v[186:189], v[82:85]
	v_mfma_f32_16x16x32_bf16 v[70:73], v[218:221], v[194:197], v[70:73]
	v_mfma_f32_16x16x32_bf16 v[66:69], v[226:229], v[194:197], v[66:69]
	s_waitcnt lgkmcnt(0)
	v_mfma_f32_16x16x32_bf16 v[118:121], v[222:225], v[152:155], v[118:121]
	v_mfma_f32_16x16x32_bf16 v[114:117], v[230:233], v[152:155], v[114:117]
	v_mfma_f32_16x16x32_bf16 v[102:105], v[222:225], v[160:163], v[102:105]
	v_mfma_f32_16x16x32_bf16 v[98:101], v[230:233], v[160:163], v[98:101]
	v_mfma_f32_16x16x32_bf16 v[86:89], v[222:225], v[190:193], v[86:89]
	v_mfma_f32_16x16x32_bf16 v[82:85], v[230:233], v[190:193], v[82:85]
	v_mfma_f32_16x16x32_bf16 v[70:73], v[222:225], v[198:201], v[70:73]
	v_mfma_f32_16x16x32_bf16 v[66:69], v[230:233], v[198:201], v[66:69]
	s_mov_b32 m0, s46
	v_lshl_add_u64 v[234:235], v[238:239], 0, s[30:31]
	s_barrier
	ds_read_b128 v[148:151], v185 offset:49152
	ds_read_b128 v[152:155], v185 offset:50176
	ds_read_b128 v[156:159], v185 offset:51200
	ds_read_b128 v[160:163], v185 offset:52224
	ds_read_b128 v[186:189], v185 offset:53248
	ds_read_b128 v[190:193], v185 offset:54272
	ds_read_b128 v[194:197], v185 offset:55296
	ds_read_b128 v[198:201], v185 offset:56320
	global_load_lds_dwordx4 v[234:235], off
	v_lshl_add_u64 v[234:235], v[240:241], 0, s[30:31]
	s_mov_b32 m0, s47
	s_nop 0
	global_load_lds_dwordx4 v[234:235], off
	s_barrier
	s_waitcnt lgkmcnt(7)
	v_mfma_f32_16x16x32_bf16 v[62:65], v[132:135], v[148:151], v[62:65]
	s_waitcnt lgkmcnt(5)
	v_mfma_f32_16x16x32_bf16 v[58:61], v[140:143], v[148:151], v[58:61]
	v_mfma_f32_16x16x32_bf16 v[46:49], v[132:135], v[156:159], v[46:49]
	s_waitcnt lgkmcnt(3)
	v_mfma_f32_16x16x32_bf16 v[42:45], v[140:143], v[156:159], v[42:45]
	v_mfma_f32_16x16x32_bf16 v[30:33], v[132:135], v[186:189], v[30:33]
	s_waitcnt lgkmcnt(1)
	v_mfma_f32_16x16x32_bf16 v[26:29], v[140:143], v[186:189], v[26:29]
	v_mfma_f32_16x16x32_bf16 v[14:17], v[132:135], v[194:197], v[14:17]
	v_mfma_f32_16x16x32_bf16 v[10:13], v[140:143], v[194:197], v[10:13]
	v_mfma_f32_16x16x32_bf16 v[62:65], v[136:139], v[152:155], v[62:65]
	v_mfma_f32_16x16x32_bf16 v[58:61], v[144:147], v[152:155], v[58:61]
	v_mfma_f32_16x16x32_bf16 v[46:49], v[136:139], v[160:163], v[46:49]
	v_mfma_f32_16x16x32_bf16 v[42:45], v[144:147], v[160:163], v[42:45]
	v_mfma_f32_16x16x32_bf16 v[30:33], v[136:139], v[190:193], v[30:33]
	s_waitcnt lgkmcnt(0)
	v_mfma_f32_16x16x32_bf16 v[26:29], v[144:147], v[190:193], v[26:29]
	v_mfma_f32_16x16x32_bf16 v[14:17], v[136:139], v[198:201], v[14:17]
	v_mfma_f32_16x16x32_bf16 v[10:13], v[144:147], v[198:201], v[10:13]
	s_barrier
	s_add_u32 s58, s64, 0x4080
	s_addc_u32 s59, s65, 0
	s_add_i32 s60, s61, s35
	v_lshl_add_u64 v[132:133], s[58:59], 0, v[164:165]
	s_mov_b32 m0, s60
	s_nop 0
	global_load_lds_dwordx4 v[132:133], off
	v_lshl_add_u64 v[132:133], s[58:59], 0, v[168:169]
	s_add_i32 m0, s60, 0x2000
	s_nop 0
	global_load_lds_dwordx4 v[132:133], off
	s_waitcnt vmcnt(10)
	s_barrier
	v_mfma_f32_16x16x32_bf16 v[54:57], v[218:221], v[148:151], v[54:57]
	v_mfma_f32_16x16x32_bf16 v[50:53], v[226:229], v[148:151], v[50:53]
	v_mfma_f32_16x16x32_bf16 v[38:41], v[218:221], v[156:159], v[38:41]
	v_mfma_f32_16x16x32_bf16 v[34:37], v[226:229], v[156:159], v[34:37]
	v_mfma_f32_16x16x32_bf16 v[22:25], v[218:221], v[186:189], v[22:25]
	v_mfma_f32_16x16x32_bf16 v[18:21], v[226:229], v[186:189], v[18:21]
	v_mfma_f32_16x16x32_bf16 v[6:9], v[218:221], v[194:197], v[6:9]
	v_mfma_f32_16x16x32_bf16 v[2:5], v[226:229], v[194:197], v[2:5]
	v_mfma_f32_16x16x32_bf16 v[54:57], v[222:225], v[152:155], v[54:57]
	v_mfma_f32_16x16x32_bf16 v[50:53], v[230:233], v[152:155], v[50:53]
	v_mfma_f32_16x16x32_bf16 v[38:41], v[222:225], v[160:163], v[38:41]
	v_mfma_f32_16x16x32_bf16 v[34:37], v[230:233], v[160:163], v[34:37]
	v_mfma_f32_16x16x32_bf16 v[22:25], v[222:225], v[190:193], v[22:25]
	v_mfma_f32_16x16x32_bf16 v[18:21], v[230:233], v[190:193], v[18:21]
	v_mfma_f32_16x16x32_bf16 v[6:9], v[222:225], v[198:201], v[6:9]
	v_mfma_f32_16x16x32_bf16 v[2:5], v[230:233], v[198:201], v[2:5]
	s_add_u32 s62, s62, 0x100
	s_addc_u32 s63, s63, 0
	s_cmp_gt_u32 s57, 13
	s_barrier
	s_cbranch_scc1 .LBB0_1095

.LBB0_1415:
	s_lshl_b32 s59, s8, 7
	v_and_b32_e32 v17, 15, v16
	v_lshrrev_b32_e32 v18, 1, v16
	s_add_u32 s47, s4, 0x45868000
	v_and_b32_e32 v18, 24, v18
	v_lshlrev_b32_e32 v19, 6, v17
	v_lshlrev_b32_e32 v16, 2, v16
	s_addc_u32 s50, s5, 0
	v_lshl_or_b32 v19, v18, 1, v19
	s_lshl_b32 s4, s6, 13
	v_and_b32_e32 v16, 32, v16
	v_bitop3_b32 v20, v19, s4, v16 bitop3:0xde
	s_lshl_b32 s4, s7, 5
	s_and_b32 s7, s4, 0x60
	s_add_i32 m0, s43, 0x18000
	v_lshl_add_u64 v[8:9], v[8:9], 0, s[30:31]
	s_lshl_b32 s4, s7, 7
	s_waitcnt vmcnt(4)
	s_barrier
	v_readfirstlane_b32 s100, v0
	s_cmp_lt_u32 s100, 0x100
	s_cbranch_scc1 .Lmy_sp_up
	s_setprio 1
.Lmy_sp_up:
	global_load_lds_dwordx4 v[8:9], off
	v_lshl_add_u64 v[6:7], v[6:7], 0, s[30:31]
	s_add_i32 m0, s43, 0x1a000
	s_add_i32 s51, s43, 0x8000
	s_add_i32 s53, s43, 0xa000
	v_bitop3_b32 v168, v19, s4, v16 bitop3:0xde
	global_load_lds_dwordx4 v[6:7], off
	v_lshl_add_u64 v[4:5], v[4:5], 0, s[30:31]
	s_mov_b32 m0, s51
	s_add_u32 s4, s60, 0x2080
	global_load_lds_dwordx4 v[4:5], off
	v_lshl_add_u64 v[2:3], v[2:3], 0, s[30:31]
	s_mov_b32 m0, s53
	s_addc_u32 s5, s61, 0
	global_load_lds_dwordx4 v[2:3], off
	s_add_i32 m0, s43, 0x1c000
	v_lshl_add_u64 v[2:3], s[4:5], 0, v[154:155]
	global_load_lds_dwordx4 v[2:3], off
	v_lshl_add_u64 v[2:3], s[4:5], 0, v[150:151]
	s_add_i32 m0, s43, 0x1e000
	s_sub_i32 s4, 0, s1
	global_load_lds_dwordx4 v[2:3], off
	v_lshlrev_b32_e32 v2, 11, v17
	v_lshl_or_b32 v2, s6, 17, v2
	v_or3_b32 v169, s7, v2, v18
	v_cvt_f32_ubyte0_e32 v2, s1
	v_rcp_iflag_f32_e32 v2, v2
	v_and_b32_e32 v3, 1, v14
	s_waitcnt vmcnt(6)
	s_mov_b32 s57, 0
	v_mul_f32_e32 v2, 0x4f7ffffe, v2
	v_cvt_u32_f32_e32 v2, v2
	v_mov_b32_e32 v157, v131
	v_mov_b32_e32 v159, v131
	v_add_u32_e32 v170, 0, v20
	v_readfirstlane_b32 s5, v2
	v_lshlrev_b32_e32 v2, 13, v14
	v_and_b32_e32 v2, 0xffffc000, v2
	v_lshl_add_u32 v2, v13, 10, v2
	v_lshl_or_b32 v2, v3, 6, v2
	v_lshl_add_u32 v156, v15, 1, v2
	v_lshlrev_b32_e32 v2, 13, v10
	v_and_b32_e32 v2, 0xffffc000, v2
	s_mul_i32 s4, s4, s5
	v_lshl_add_u32 v2, v11, 10, v2
	v_and_b32_e32 v3, 1, v10
	s_mul_hi_u32 s4, s5, s4
	v_lshl_or_b32 v2, v3, 6, v2
	s_add_i32 s58, s5, s4
	v_lshl_add_u32 v158, v12, 1, v2
	s_barrier
	s_waitcnt vmcnt(0)

.LBB0_1418:
	s_add_i32 s65, 0, 0x10000
	v_add_u32_e32 v130, s65, v168
	ds_read_b128 v[2:5], v130
	ds_read_b128 v[6:9], v130 offset:1024
	ds_read_b128 v[10:13], v130 offset:2048
	ds_read_b128 v[14:17], v130 offset:3072
	s_add_u32 s62, s18, 0x20080
	s_addc_u32 s63, s19, 0
	s_add_i32 s13, s43, 0xc000
	v_lshl_add_u64 v[50:51], s[62:63], 0, v[152:153]
	s_mov_b32 m0, s13
	s_add_i32 s64, s43, 0xe000
	ds_read_b128 v[18:21], v170
	ds_read_b128 v[22:25], v170 offset:1024
	ds_read_b128 v[26:29], v170 offset:2048
	ds_read_b128 v[30:33], v170 offset:3072
	ds_read_b128 v[34:37], v170 offset:4096
	ds_read_b128 v[38:41], v170 offset:5120
	ds_read_b128 v[42:45], v170 offset:6144
	ds_read_b128 v[46:49], v170 offset:7168
	global_load_lds_dwordx4 v[50:51], off
	v_lshl_add_u64 v[50:51], s[62:63], 0, v[148:149]
	s_mov_b32 m0, s64
	s_nop 0
	global_load_lds_dwordx4 v[50:51], off
	s_waitcnt lgkmcnt(8)
	s_waitcnt vmcnt(10)
	s_barrier
	s_waitcnt lgkmcnt(6)
	v_mfma_scale_f32_16x16x128_f8f6f4 v[140:143], v[2:9], v[18:25], 0, v205, v205 op_sel_hi:[0,0,0]
	v_mfma_scale_f32_16x16x128_f8f6f4 v[132:135], v[10:17], v[18:25], 0, v205, v205 op_sel_hi:[0,0,0]
	s_waitcnt lgkmcnt(4)
	v_mfma_scale_f32_16x16x128_f8f6f4 v[122:125], v[2:9], v[26:33], 0, v205, v205 op_sel_hi:[0,0,0]
	v_mfma_scale_f32_16x16x128_f8f6f4 v[114:117], v[10:17], v[26:33], 0, v205, v205 op_sel_hi:[0,0,0]
	s_waitcnt lgkmcnt(2)
	v_mfma_scale_f32_16x16x128_f8f6f4 v[106:109], v[2:9], v[34:41], 0, v205, v205 op_sel_hi:[0,0,0]
	v_mfma_scale_f32_16x16x128_f8f6f4 v[98:101], v[10:17], v[34:41], 0, v205, v205 op_sel_hi:[0,0,0]
	s_waitcnt lgkmcnt(0)
	v_mfma_scale_f32_16x16x128_f8f6f4 v[90:93], v[2:9], v[42:49], 0, v205, v205 op_sel_hi:[0,0,0]
	v_mfma_scale_f32_16x16x128_f8f6f4 v[78:81], v[10:17], v[42:49], 0, v205, v205 op_sel_hi:[0,0,0]
	s_barrier
	s_add_i32 s67, 0, 0x14000
	v_lshl_add_u64 v[164:165], s[60:61], 0, v[154:155]
	s_mov_b64 s[62:63], 0x100
	s_add_i32 s65, s65, s38
	v_add_u32_e32 v171, s67, v168
	v_lshl_add_u64 v[50:51], v[164:165], 0, s[62:63]
	s_mov_b32 m0, s65
	v_lshl_add_u64 v[166:167], s[60:61], 0, v[150:151]
	s_add_i32 s66, s65, 0x2000
	ds_read_b128 v[178:181], v171
	ds_read_b128 v[182:185], v171 offset:1024
	ds_read_b128 v[186:189], v171 offset:2048
	ds_read_b128 v[190:193], v171 offset:3072
	global_load_lds_dwordx4 v[50:51], off
	v_lshl_add_u64 v[50:51], v[166:167], 0, s[62:63]
	s_mov_b32 m0, s66
	s_nop 0
	global_load_lds_dwordx4 v[50:51], off
	s_waitcnt vmcnt(10)
	s_barrier
	s_waitcnt lgkmcnt(2)
	v_mfma_scale_f32_16x16x128_f8f6f4 v[144:147], v[178:185], v[18:25], 0, v205, v205 op_sel_hi:[0,0,0]
	s_waitcnt lgkmcnt(0)
	v_mfma_scale_f32_16x16x128_f8f6f4 v[136:139], v[186:193], v[18:25], 0, v205, v205 op_sel_hi:[0,0,0]
	v_mfma_scale_f32_16x16x128_f8f6f4 v[126:129], v[178:185], v[26:33], 0, v205, v205 op_sel_hi:[0,0,0]
	v_mfma_scale_f32_16x16x128_f8f6f4 v[118:121], v[186:193], v[26:33], 0, v205, v205 op_sel_hi:[0,0,0]
	v_mfma_scale_f32_16x16x128_f8f6f4 v[110:113], v[178:185], v[34:41], 0, v205, v205 op_sel_hi:[0,0,0]
	v_mfma_scale_f32_16x16x128_f8f6f4 v[102:105], v[186:193], v[34:41], 0, v205, v205 op_sel_hi:[0,0,0]
	v_mfma_scale_f32_16x16x128_f8f6f4 v[94:97], v[178:185], v[42:49], 0, v205, v205 op_sel_hi:[0,0,0]
	v_mfma_scale_f32_16x16x128_f8f6f4 v[86:89], v[186:193], v[42:49], 0, v205, v205 op_sel_hi:[0,0,0]
	v_lshl_add_u64 v[160:161], s[18:19], 0, v[152:153]
	s_mov_b32 m0, s43
	v_lshl_add_u64 v[18:19], v[160:161], 0, s[62:63]
	v_lshl_add_u64 v[162:163], s[18:19], 0, v[148:149]
	s_barrier
	ds_read_b128 v[194:197], v170 offset:16384
	ds_read_b128 v[198:201], v170 offset:17408
	ds_read_b128 v[218:221], v170 offset:18432
	ds_read_b128 v[222:225], v170 offset:19456
	ds_read_b128 v[226:229], v170 offset:20480
	ds_read_b128 v[230:233], v170 offset:21504
	ds_read_b128 v[234:237], v170 offset:22528
	ds_read_b128 v[238:241], v170 offset:23552
	global_load_lds_dwordx4 v[18:19], off
	v_lshl_add_u64 v[18:19], v[162:163], 0, s[62:63]
	s_mov_b32 m0, s44
	s_nop 0
	global_load_lds_dwordx4 v[18:19], off
	s_barrier
	s_waitcnt lgkmcnt(6)
	v_mfma_scale_f32_16x16x128_f8f6f4 v[74:77], v[2:9], v[194:201], 0, v205, v205 op_sel_hi:[0,0,0]
	v_mfma_scale_f32_16x16x128_f8f6f4 v[66:69], v[10:17], v[194:201], 0, v205, v205 op_sel_hi:[0,0,0]
	s_waitcnt lgkmcnt(4)
	v_mfma_scale_f32_16x16x128_f8f6f4 v[58:61], v[2:9], v[218:225], 0, v205, v205 op_sel_hi:[0,0,0]
	v_mfma_scale_f32_16x16x128_f8f6f4 v[50:53], v[10:17], v[218:225], 0, v205, v205 op_sel_hi:[0,0,0]
	s_waitcnt lgkmcnt(2)
	v_mfma_scale_f32_16x16x128_f8f6f4 v[42:45], v[2:9], v[226:233], 0, v205, v205 op_sel_hi:[0,0,0]
	v_mfma_scale_f32_16x16x128_f8f6f4 v[34:37], v[10:17], v[226:233], 0, v205, v205 op_sel_hi:[0,0,0]
	s_waitcnt lgkmcnt(0)
	v_mfma_scale_f32_16x16x128_f8f6f4 v[26:29], v[2:9], v[234:241], 0, v205, v205 op_sel_hi:[0,0,0]
	v_mfma_scale_f32_16x16x128_f8f6f4 v[18:21], v[10:17], v[234:241], 0, v205, v205 op_sel_hi:[0,0,0]
	s_barrier
	s_add_u32 s62, s60, 0x2100
	s_addc_u32 s63, s61, 0
	s_add_i32 s67, s67, s38
	v_lshl_add_u64 v[2:3], s[62:63], 0, v[154:155]
	s_mov_b32 m0, s67
	s_add_i32 s68, s67, 0x2000
	global_load_lds_dwordx4 v[2:3], off
	v_lshl_add_u64 v[2:3], s[62:63], 0, v[150:151]
	s_mov_b32 m0, s68
	s_nop 0
	global_load_lds_dwordx4 v[2:3], off
	s_waitcnt vmcnt(10)
	s_barrier
	v_mfma_scale_f32_16x16x128_f8f6f4 v[82:85], v[178:185], v[194:201], 0, v205, v205 op_sel_hi:[0,0,0]
	v_mfma_scale_f32_16x16x128_f8f6f4 v[70:73], v[186:193], v[194:201], 0, v205, v205 op_sel_hi:[0,0,0]
	v_mfma_scale_f32_16x16x128_f8f6f4 v[62:65], v[178:185], v[218:225], 0, v205, v205 op_sel_hi:[0,0,0]
	v_mfma_scale_f32_16x16x128_f8f6f4 v[54:57], v[186:193], v[218:225], 0, v205, v205 op_sel_hi:[0,0,0]
	v_mfma_scale_f32_16x16x128_f8f6f4 v[46:49], v[178:185], v[226:233], 0, v205, v205 op_sel_hi:[0,0,0]
	v_mfma_scale_f32_16x16x128_f8f6f4 v[38:41], v[186:193], v[226:233], 0, v205, v205 op_sel_hi:[0,0,0]
	v_mfma_scale_f32_16x16x128_f8f6f4 v[30:33], v[178:185], v[234:241], 0, v205, v205 op_sel_hi:[0,0,0]
	v_mfma_scale_f32_16x16x128_f8f6f4 v[22:25], v[186:193], v[234:241], 0, v205, v205 op_sel_hi:[0,0,0]
	s_add_i32 s69, 0, 0x18000
	v_add_u32_e32 v172, s69, v168
	s_barrier
	ds_read_b128 v[10:13], v172
	ds_read_b128 v[14:17], v172 offset:1024
	ds_read_b128 v[2:5], v172 offset:2048
	ds_read_b128 v[6:9], v172 offset:3072
	s_add_u32 s62, s18, 0x20100
	s_addc_u32 s63, s19, 0
	s_mov_b32 m0, s45
	v_lshl_add_u64 v[174:175], s[62:63], 0, v[152:153]
	ds_read_b128 v[178:181], v170 offset:32768
	ds_read_b128 v[182:185], v170 offset:33792
	ds_read_b128 v[186:189], v170 offset:34816
	ds_read_b128 v[190:193], v170 offset:35840
	ds_read_b128 v[194:197], v170 offset:36864
	ds_read_b128 v[198:201], v170 offset:37888
	ds_read_b128 v[218:221], v170 offset:38912
	ds_read_b128 v[222:225], v170 offset:39936
	global_load_lds_dwordx4 v[174:175], off
	v_lshl_add_u64 v[174:175], s[62:63], 0, v[148:149]
	s_mov_b32 m0, s46
	s_nop 0
	global_load_lds_dwordx4 v[174:175], off
	s_waitcnt lgkmcnt(8)
	s_waitcnt vmcnt(10)
	s_barrier
	s_waitcnt lgkmcnt(6)
	v_mfma_scale_f32_16x16x128_f8f6f4 v[140:143], v[10:17], v[178:185], v[140:143], v205, v205 op_sel_hi:[0,0,0]
	v_mfma_scale_f32_16x16x128_f8f6f4 v[132:135], v[2:9], v[178:185], v[132:135], v205, v205 op_sel_hi:[0,0,0]
	s_waitcnt lgkmcnt(4)
	v_mfma_scale_f32_16x16x128_f8f6f4 v[122:125], v[10:17], v[186:193], v[122:125], v205, v205 op_sel_hi:[0,0,0]
	v_mfma_scale_f32_16x16x128_f8f6f4 v[114:117], v[2:9], v[186:193], v[114:117], v205, v205 op_sel_hi:[0,0,0]
	s_waitcnt lgkmcnt(2)
	v_mfma_scale_f32_16x16x128_f8f6f4 v[106:109], v[10:17], v[194:201], v[106:109], v205, v205 op_sel_hi:[0,0,0]
	v_mfma_scale_f32_16x16x128_f8f6f4 v[98:101], v[2:9], v[194:201], v[98:101], v205, v205 op_sel_hi:[0,0,0]
	s_waitcnt lgkmcnt(0)
	v_mfma_scale_f32_16x16x128_f8f6f4 v[90:93], v[10:17], v[218:225], v[90:93], v205, v205 op_sel_hi:[0,0,0]
	v_mfma_scale_f32_16x16x128_f8f6f4 v[78:81], v[2:9], v[218:225], v[78:81], v205, v205 op_sel_hi:[0,0,0]
	s_barrier
	s_add_i32 s71, 0, 0x1c000
	s_mov_b64 s[62:63], 0x180
	s_add_i32 s69, s69, s38
	v_add_u32_e32 v173, s71, v168
	v_lshl_add_u64 v[164:165], v[164:165], 0, s[62:63]
	s_mov_b32 m0, s69
	s_add_i32 s70, s69, 0x2000
	ds_read_b128 v[226:229], v173
	ds_read_b128 v[230:233], v173 offset:1024
	ds_read_b128 v[234:237], v173 offset:2048
	ds_read_b128 v[238:241], v173 offset:3072
	global_load_lds_dwordx4 v[164:165], off
	v_lshl_add_u64 v[164:165], v[166:167], 0, s[62:63]
	s_mov_b32 m0, s70
	s_nop 0
	global_load_lds_dwordx4 v[164:165], off
	s_waitcnt vmcnt(10)
	s_barrier
	s_waitcnt lgkmcnt(2)
	v_mfma_scale_f32_16x16x128_f8f6f4 v[144:147], v[226:233], v[178:185], v[144:147], v205, v205 op_sel_hi:[0,0,0]
	s_waitcnt lgkmcnt(0)
	v_mfma_scale_f32_16x16x128_f8f6f4 v[136:139], v[234:241], v[178:185], v[136:139], v205, v205 op_sel_hi:[0,0,0]
	v_mfma_scale_f32_16x16x128_f8f6f4 v[126:129], v[226:233], v[186:193], v[126:129], v205, v205 op_sel_hi:[0,0,0]
	v_mfma_scale_f32_16x16x128_f8f6f4 v[118:121], v[234:241], v[186:193], v[118:121], v205, v205 op_sel_hi:[0,0,0]
	v_mfma_scale_f32_16x16x128_f8f6f4 v[110:113], v[226:233], v[194:201], v[110:113], v205, v205 op_sel_hi:[0,0,0]
	v_mfma_scale_f32_16x16x128_f8f6f4 v[102:105], v[234:241], v[194:201], v[102:105], v205, v205 op_sel_hi:[0,0,0]
	v_mfma_scale_f32_16x16x128_f8f6f4 v[94:97], v[226:233], v[218:225], v[94:97], v205, v205 op_sel_hi:[0,0,0]
	v_mfma_scale_f32_16x16x128_f8f6f4 v[86:89], v[234:241], v[218:225], v[86:89], v205, v205 op_sel_hi:[0,0,0]
	s_mov_b32 m0, s51
	v_lshl_add_u64 v[160:161], v[160:161], 0, s[62:63]
	s_barrier
	ds_read_b128 v[178:181], v170 offset:49152
	ds_read_b128 v[182:185], v170 offset:50176
	ds_read_b128 v[186:189], v170 offset:51200
	ds_read_b128 v[190:193], v170 offset:52224
	ds_read_b128 v[194:197], v170 offset:53248
	ds_read_b128 v[198:201], v170 offset:54272
	ds_read_b128 v[218:221], v170 offset:55296
	ds_read_b128 v[222:225], v170 offset:56320
	global_load_lds_dwordx4 v[160:161], off
	v_lshl_add_u64 v[160:161], v[162:163], 0, s[62:63]
	s_mov_b32 m0, s53
	s_nop 0
	global_load_lds_dwordx4 v[160:161], off
	s_barrier
	s_waitcnt lgkmcnt(6)
	v_mfma_scale_f32_16x16x128_f8f6f4 v[74:77], v[10:17], v[178:185], v[74:77], v205, v205 op_sel_hi:[0,0,0]
	v_mfma_scale_f32_16x16x128_f8f6f4 v[66:69], v[2:9], v[178:185], v[66:69], v205, v205 op_sel_hi:[0,0,0]
	s_waitcnt lgkmcnt(4)
	v_mfma_scale_f32_16x16x128_f8f6f4 v[58:61], v[10:17], v[186:193], v[58:61], v205, v205 op_sel_hi:[0,0,0]
	v_mfma_scale_f32_16x16x128_f8f6f4 v[50:53], v[2:9], v[186:193], v[50:53], v205, v205 op_sel_hi:[0,0,0]
	s_waitcnt lgkmcnt(2)
	v_mfma_scale_f32_16x16x128_f8f6f4 v[42:45], v[10:17], v[194:201], v[42:45], v205, v205 op_sel_hi:[0,0,0]
	v_mfma_scale_f32_16x16x128_f8f6f4 v[34:37], v[2:9], v[194:201], v[34:37], v205, v205 op_sel_hi:[0,0,0]
	s_waitcnt lgkmcnt(0)
	v_mfma_scale_f32_16x16x128_f8f6f4 v[26:29], v[10:17], v[218:225], v[26:29], v205, v205 op_sel_hi:[0,0,0]
	v_mfma_scale_f32_16x16x128_f8f6f4 v[18:21], v[2:9], v[218:225], v[18:21], v205, v205 op_sel_hi:[0,0,0]
	s_barrier
	s_add_u32 s62, s60, 0x2180
	s_addc_u32 s63, s61, 0
	s_add_i32 s71, s71, s38
	v_lshl_add_u64 v[2:3], s[62:63], 0, v[154:155]
	s_mov_b32 m0, s71
	s_add_i32 s72, s71, 0x2000
	global_load_lds_dwordx4 v[2:3], off
	v_lshl_add_u64 v[2:3], s[62:63], 0, v[150:151]
	s_mov_b32 m0, s72
	s_nop 0
	global_load_lds_dwordx4 v[2:3], off
	s_waitcnt vmcnt(10)
	s_barrier
	v_mfma_scale_f32_16x16x128_f8f6f4 v[82:85], v[226:233], v[178:185], v[82:85], v205, v205 op_sel_hi:[0,0,0]
	v_mfma_scale_f32_16x16x128_f8f6f4 v[70:73], v[234:241], v[178:185], v[70:73], v205, v205 op_sel_hi:[0,0,0]
	v_mfma_scale_f32_16x16x128_f8f6f4 v[62:65], v[226:233], v[186:193], v[62:65], v205, v205 op_sel_hi:[0,0,0]
	v_mfma_scale_f32_16x16x128_f8f6f4 v[54:57], v[234:241], v[186:193], v[54:57], v205, v205 op_sel_hi:[0,0,0]
	v_mfma_scale_f32_16x16x128_f8f6f4 v[46:49], v[226:233], v[194:201], v[46:49], v205, v205 op_sel_hi:[0,0,0]
	v_mfma_scale_f32_16x16x128_f8f6f4 v[38:41], v[234:241], v[194:201], v[38:41], v205, v205 op_sel_hi:[0,0,0]
	v_mfma_scale_f32_16x16x128_f8f6f4 v[30:33], v[226:233], v[218:225], v[30:33], v205, v205 op_sel_hi:[0,0,0]
	v_mfma_scale_f32_16x16x128_f8f6f4 v[22:25], v[234:241], v[218:225], v[22:25], v205, v205 op_sel_hi:[0,0,0]
	s_add_u32 s18, s18, 0x20180
	s_addc_u32 s19, s19, 0
	s_add_u32 s73, s60, 0x200
	s_addc_u32 s74, s61, 0
	s_mov_b32 s75, 0
	s_barrier
.LBB0_1419:
	ds_read_b128 v[10:13], v130
	ds_read_b128 v[14:17], v130 offset:1024
	ds_read_b128 v[160:163], v130 offset:2048
	ds_read_b128 v[164:167], v130 offset:3072
	s_add_u32 s60, s18, 0xfffe0080
	s_addc_u32 s61, s19, -1
	s_cmp_eq_u32 s75, 4
	s_cselect_b32 s63, s15, s61
	s_cselect_b32 s62, s14, s60
	s_cselect_b32 s61, s17, s74
	s_cselect_b32 s60, s16, s73
	s_mov_b32 m0, s13
	v_lshl_add_u64 v[2:3], s[18:19], 0, v[156:157]
	ds_read_b128 v[178:181], v170
	ds_read_b128 v[182:185], v170 offset:1024
	ds_read_b128 v[186:189], v170 offset:2048
	ds_read_b128 v[190:193], v170 offset:3072
	ds_read_b128 v[194:197], v170 offset:4096
	ds_read_b128 v[198:201], v170 offset:5120
	ds_read_b128 v[218:221], v170 offset:6144
	ds_read_b128 v[222:225], v170 offset:7168
	global_load_lds_dwordx4 v[2:3], off
	v_lshl_add_u64 v[2:3], s[18:19], 0, v[158:159]
	s_mov_b32 m0, s64
	s_nop 0
	global_load_lds_dwordx4 v[2:3], off
	s_waitcnt lgkmcnt(8)
	s_waitcnt vmcnt(10)
	s_barrier
	s_waitcnt lgkmcnt(6)
	v_mfma_scale_f32_16x16x128_f8f6f4 v[140:143], v[10:17], v[178:185], v[140:143], v205, v205 op_sel_hi:[0,0,0]
	v_mfma_scale_f32_16x16x128_f8f6f4 v[132:135], v[160:167], v[178:185], v[132:135], v205, v205 op_sel_hi:[0,0,0]
	s_waitcnt lgkmcnt(4)
	v_mfma_scale_f32_16x16x128_f8f6f4 v[122:125], v[10:17], v[186:193], v[122:125], v205, v205 op_sel_hi:[0,0,0]
	v_mfma_scale_f32_16x16x128_f8f6f4 v[114:117], v[160:167], v[186:193], v[114:117], v205, v205 op_sel_hi:[0,0,0]
	s_waitcnt lgkmcnt(2)
	v_mfma_scale_f32_16x16x128_f8f6f4 v[106:109], v[10:17], v[194:201], v[106:109], v205, v205 op_sel_hi:[0,0,0]
	v_mfma_scale_f32_16x16x128_f8f6f4 v[98:101], v[160:167], v[194:201], v[98:101], v205, v205 op_sel_hi:[0,0,0]
	s_waitcnt lgkmcnt(0)
	v_mfma_scale_f32_16x16x128_f8f6f4 v[90:93], v[10:17], v[218:225], v[90:93], v205, v205 op_sel_hi:[0,0,0]
	v_mfma_scale_f32_16x16x128_f8f6f4 v[78:81], v[160:167], v[218:225], v[78:81], v205, v205 op_sel_hi:[0,0,0]
	s_barrier
	s_mov_b32 m0, s65
	v_lshl_add_u64 v[6:7], s[60:61], 0, v[154:155]
	ds_read_b128 v[226:229], v171
	ds_read_b128 v[230:233], v171 offset:1024
	ds_read_b128 v[234:237], v171 offset:2048
	ds_read_b128 v[238:241], v171 offset:3072
	global_load_lds_dwordx4 v[6:7], off
	v_lshl_add_u64 v[8:9], s[60:61], 0, v[150:151]
	s_mov_b32 m0, s66
	s_nop 0
	global_load_lds_dwordx4 v[8:9], off
	s_waitcnt vmcnt(10)
	s_barrier
	s_waitcnt lgkmcnt(2)
	v_mfma_scale_f32_16x16x128_f8f6f4 v[144:147], v[226:233], v[178:185], v[144:147], v205, v205 op_sel_hi:[0,0,0]
	s_waitcnt lgkmcnt(0)
	v_mfma_scale_f32_16x16x128_f8f6f4 v[136:139], v[234:241], v[178:185], v[136:139], v205, v205 op_sel_hi:[0,0,0]
	v_mfma_scale_f32_16x16x128_f8f6f4 v[126:129], v[226:233], v[186:193], v[126:129], v205, v205 op_sel_hi:[0,0,0]
	v_mfma_scale_f32_16x16x128_f8f6f4 v[118:121], v[234:241], v[186:193], v[118:121], v205, v205 op_sel_hi:[0,0,0]
	v_mfma_scale_f32_16x16x128_f8f6f4 v[110:113], v[226:233], v[194:201], v[110:113], v205, v205 op_sel_hi:[0,0,0]
	v_mfma_scale_f32_16x16x128_f8f6f4 v[102:105], v[234:241], v[194:201], v[102:105], v205, v205 op_sel_hi:[0,0,0]
	v_mfma_scale_f32_16x16x128_f8f6f4 v[94:97], v[226:233], v[218:225], v[94:97], v205, v205 op_sel_hi:[0,0,0]
	v_mfma_scale_f32_16x16x128_f8f6f4 v[86:89], v[234:241], v[218:225], v[86:89], v205, v205 op_sel_hi:[0,0,0]
	s_mov_b32 m0, s43
	v_lshl_add_u64 v[2:3], s[62:63], 0, v[152:153]
	s_barrier
	ds_read_b128 v[178:181], v170 offset:16384
	ds_read_b128 v[182:185], v170 offset:17408
	ds_read_b128 v[186:189], v170 offset:18432
	ds_read_b128 v[190:193], v170 offset:19456
	ds_read_b128 v[194:197], v170 offset:20480
	ds_read_b128 v[198:201], v170 offset:21504
	ds_read_b128 v[218:221], v170 offset:22528
	ds_read_b128 v[222:225], v170 offset:23552
	global_load_lds_dwordx4 v[2:3], off
	v_lshl_add_u64 v[4:5], s[62:63], 0, v[148:149]
	s_mov_b32 m0, s44
	s_nop 0
	global_load_lds_dwordx4 v[4:5], off
	s_barrier
	s_waitcnt lgkmcnt(6)
	v_mfma_scale_f32_16x16x128_f8f6f4 v[74:77], v[10:17], v[178:185], v[74:77], v205, v205 op_sel_hi:[0,0,0]
	v_mfma_scale_f32_16x16x128_f8f6f4 v[66:69], v[160:167], v[178:185], v[66:69], v205, v205 op_sel_hi:[0,0,0]
	s_waitcnt lgkmcnt(4)
	v_mfma_scale_f32_16x16x128_f8f6f4 v[58:61], v[10:17], v[186:193], v[58:61], v205, v205 op_sel_hi:[0,0,0]
	v_mfma_scale_f32_16x16x128_f8f6f4 v[50:53], v[160:167], v[186:193], v[50:53], v205, v205 op_sel_hi:[0,0,0]
	s_waitcnt lgkmcnt(2)
	v_mfma_scale_f32_16x16x128_f8f6f4 v[42:45], v[10:17], v[194:201], v[42:45], v205, v205 op_sel_hi:[0,0,0]
	v_mfma_scale_f32_16x16x128_f8f6f4 v[34:37], v[160:167], v[194:201], v[34:37], v205, v205 op_sel_hi:[0,0,0]
	s_waitcnt lgkmcnt(0)
	v_mfma_scale_f32_16x16x128_f8f6f4 v[26:29], v[10:17], v[218:225], v[26:29], v205, v205 op_sel_hi:[0,0,0]
	v_mfma_scale_f32_16x16x128_f8f6f4 v[18:21], v[160:167], v[218:225], v[18:21], v205, v205 op_sel_hi:[0,0,0]
	s_barrier
	s_add_u32 s76, s60, 0x2000
	s_addc_u32 s77, s61, 0
	s_mov_b32 m0, s67
	v_lshl_add_u64 v[10:11], s[76:77], 0, v[154:155]
	global_load_lds_dwordx4 v[10:11], off
	v_lshl_add_u64 v[10:11], s[76:77], 0, v[150:151]
	s_mov_b32 m0, s68
	s_nop 0
	global_load_lds_dwordx4 v[10:11], off
	s_waitcnt vmcnt(10)
	s_barrier
	v_mfma_scale_f32_16x16x128_f8f6f4 v[82:85], v[226:233], v[178:185], v[82:85], v205, v205 op_sel_hi:[0,0,0]
	v_mfma_scale_f32_16x16x128_f8f6f4 v[70:73], v[234:241], v[178:185], v[70:73], v205, v205 op_sel_hi:[0,0,0]
	v_mfma_scale_f32_16x16x128_f8f6f4 v[62:65], v[226:233], v[186:193], v[62:65], v205, v205 op_sel_hi:[0,0,0]
	v_mfma_scale_f32_16x16x128_f8f6f4 v[54:57], v[234:241], v[186:193], v[54:57], v205, v205 op_sel_hi:[0,0,0]
	v_mfma_scale_f32_16x16x128_f8f6f4 v[46:49], v[226:233], v[194:201], v[46:49], v205, v205 op_sel_hi:[0,0,0]
	v_mfma_scale_f32_16x16x128_f8f6f4 v[38:41], v[234:241], v[194:201], v[38:41], v205, v205 op_sel_hi:[0,0,0]
	v_mfma_scale_f32_16x16x128_f8f6f4 v[30:33], v[226:233], v[218:225], v[30:33], v205, v205 op_sel_hi:[0,0,0]
	v_mfma_scale_f32_16x16x128_f8f6f4 v[22:25], v[234:241], v[218:225], v[22:25], v205, v205 op_sel_hi:[0,0,0]
	s_barrier
	ds_read_b128 v[10:13], v172
	ds_read_b128 v[14:17], v172 offset:1024
	ds_read_b128 v[160:163], v172 offset:2048
	ds_read_b128 v[164:167], v172 offset:3072
	s_add_u32 s62, s62, 0x20000
	s_addc_u32 s63, s63, 0
	s_mov_b32 m0, s45
	v_lshl_add_u64 v[174:175], s[62:63], 0, v[152:153]
	ds_read_b128 v[178:181], v170 offset:32768
	ds_read_b128 v[182:185], v170 offset:33792
	ds_read_b128 v[186:189], v170 offset:34816
	ds_read_b128 v[190:193], v170 offset:35840
	ds_read_b128 v[194:197], v170 offset:36864
	ds_read_b128 v[198:201], v170 offset:37888
	ds_read_b128 v[218:221], v170 offset:38912
	ds_read_b128 v[222:225], v170 offset:39936
	global_load_lds_dwordx4 v[174:175], off
	v_lshl_add_u64 v[174:175], s[62:63], 0, v[148:149]
	s_mov_b32 m0, s46
	s_nop 0
	global_load_lds_dwordx4 v[174:175], off
	s_waitcnt lgkmcnt(8)
	s_waitcnt vmcnt(10)
	s_barrier
	s_waitcnt lgkmcnt(6)
	v_mfma_scale_f32_16x16x128_f8f6f4 v[140:143], v[10:17], v[178:185], v[140:143], v205, v205 op_sel_hi:[0,0,0]
	v_mfma_scale_f32_16x16x128_f8f6f4 v[132:135], v[160:167], v[178:185], v[132:135], v205, v205 op_sel_hi:[0,0,0]
	s_waitcnt lgkmcnt(4)
	v_mfma_scale_f32_16x16x128_f8f6f4 v[122:125], v[10:17], v[186:193], v[122:125], v205, v205 op_sel_hi:[0,0,0]
	v_mfma_scale_f32_16x16x128_f8f6f4 v[114:117], v[160:167], v[186:193], v[114:117], v205, v205 op_sel_hi:[0,0,0]
	s_waitcnt lgkmcnt(2)
	v_mfma_scale_f32_16x16x128_f8f6f4 v[106:109], v[10:17], v[194:201], v[106:109], v205, v205 op_sel_hi:[0,0,0]
	v_mfma_scale_f32_16x16x128_f8f6f4 v[98:101], v[160:167], v[194:201], v[98:101], v205, v205 op_sel_hi:[0,0,0]
	s_waitcnt lgkmcnt(0)
	v_mfma_scale_f32_16x16x128_f8f6f4 v[90:93], v[10:17], v[218:225], v[90:93], v205, v205 op_sel_hi:[0,0,0]
	v_mfma_scale_f32_16x16x128_f8f6f4 v[78:81], v[160:167], v[218:225], v[78:81], v205, v205 op_sel_hi:[0,0,0]
	s_barrier
	s_mov_b32 m0, s69
	v_lshl_add_u64 v[6:7], v[6:7], 0, s[30:31]
	ds_read_b128 v[226:229], v173
	ds_read_b128 v[230:233], v173 offset:1024
	ds_read_b128 v[234:237], v173 offset:2048
	ds_read_b128 v[238:241], v173 offset:3072
	global_load_lds_dwordx4 v[6:7], off
	v_lshl_add_u64 v[6:7], v[8:9], 0, s[30:31]
	s_mov_b32 m0, s70
	s_nop 0
	global_load_lds_dwordx4 v[6:7], off
	s_waitcnt vmcnt(10)
	s_barrier
	s_waitcnt lgkmcnt(2)
	v_mfma_scale_f32_16x16x128_f8f6f4 v[144:147], v[226:233], v[178:185], v[144:147], v205, v205 op_sel_hi:[0,0,0]
	s_waitcnt lgkmcnt(0)
	v_mfma_scale_f32_16x16x128_f8f6f4 v[136:139], v[234:241], v[178:185], v[136:139], v205, v205 op_sel_hi:[0,0,0]
	v_mfma_scale_f32_16x16x128_f8f6f4 v[126:129], v[226:233], v[186:193], v[126:129], v205, v205 op_sel_hi:[0,0,0]
	v_mfma_scale_f32_16x16x128_f8f6f4 v[118:121], v[234:241], v[186:193], v[118:121], v205, v205 op_sel_hi:[0,0,0]
	v_mfma_scale_f32_16x16x128_f8f6f4 v[110:113], v[226:233], v[194:201], v[110:113], v205, v205 op_sel_hi:[0,0,0]
	v_mfma_scale_f32_16x16x128_f8f6f4 v[102:105], v[234:241], v[194:201], v[102:105], v205, v205 op_sel_hi:[0,0,0]
	v_mfma_scale_f32_16x16x128_f8f6f4 v[94:97], v[226:233], v[218:225], v[94:97], v205, v205 op_sel_hi:[0,0,0]
	v_mfma_scale_f32_16x16x128_f8f6f4 v[86:89], v[234:241], v[218:225], v[86:89], v205, v205 op_sel_hi:[0,0,0]
	s_mov_b32 m0, s51
	v_lshl_add_u64 v[2:3], v[2:3], 0, s[30:31]
	s_barrier
	ds_read_b128 v[178:181], v170 offset:49152
	ds_read_b128 v[182:185], v170 offset:50176
	ds_read_b128 v[186:189], v170 offset:51200
	ds_read_b128 v[190:193], v170 offset:52224
	ds_read_b128 v[194:197], v170 offset:53248
	ds_read_b128 v[198:201], v170 offset:54272
	ds_read_b128 v[218:221], v170 offset:55296
	ds_read_b128 v[222:225], v170 offset:56320
	global_load_lds_dwordx4 v[2:3], off
	v_lshl_add_u64 v[2:3], v[4:5], 0, s[30:31]
	s_mov_b32 m0, s53
	s_nop 0
	global_load_lds_dwordx4 v[2:3], off
	s_barrier
	s_waitcnt lgkmcnt(6)
	v_mfma_scale_f32_16x16x128_f8f6f4 v[74:77], v[10:17], v[178:185], v[74:77], v205, v205 op_sel_hi:[0,0,0]
	v_mfma_scale_f32_16x16x128_f8f6f4 v[66:69], v[160:167], v[178:185], v[66:69], v205, v205 op_sel_hi:[0,0,0]
	s_waitcnt lgkmcnt(4)
	v_mfma_scale_f32_16x16x128_f8f6f4 v[58:61], v[10:17], v[186:193], v[58:61], v205, v205 op_sel_hi:[0,0,0]
	v_mfma_scale_f32_16x16x128_f8f6f4 v[50:53], v[160:167], v[186:193], v[50:53], v205, v205 op_sel_hi:[0,0,0]
	s_waitcnt lgkmcnt(2)
	v_mfma_scale_f32_16x16x128_f8f6f4 v[42:45], v[10:17], v[194:201], v[42:45], v205, v205 op_sel_hi:[0,0,0]
	v_mfma_scale_f32_16x16x128_f8f6f4 v[34:37], v[160:167], v[194:201], v[34:37], v205, v205 op_sel_hi:[0,0,0]
	s_waitcnt lgkmcnt(0)
	v_mfma_scale_f32_16x16x128_f8f6f4 v[26:29], v[10:17], v[218:225], v[26:29], v205, v205 op_sel_hi:[0,0,0]
	v_mfma_scale_f32_16x16x128_f8f6f4 v[18:21], v[160:167], v[218:225], v[18:21], v205, v205 op_sel_hi:[0,0,0]
	s_barrier
	s_add_u32 s60, s60, 0x2080
	s_addc_u32 s61, s61, 0
	s_mov_b32 m0, s71
	v_lshl_add_u64 v[2:3], s[60:61], 0, v[154:155]
	global_load_lds_dwordx4 v[2:3], off
	v_lshl_add_u64 v[2:3], s[60:61], 0, v[150:151]
	s_mov_b32 m0, s72
	s_nop 0
	global_load_lds_dwordx4 v[2:3], off
	s_waitcnt vmcnt(10)
	s_barrier
	v_mfma_scale_f32_16x16x128_f8f6f4 v[82:85], v[226:233], v[178:185], v[82:85], v205, v205 op_sel_hi:[0,0,0]
	v_mfma_scale_f32_16x16x128_f8f6f4 v[70:73], v[234:241], v[178:185], v[70:73], v205, v205 op_sel_hi:[0,0,0]
	v_mfma_scale_f32_16x16x128_f8f6f4 v[62:65], v[226:233], v[186:193], v[62:65], v205, v205 op_sel_hi:[0,0,0]
	v_mfma_scale_f32_16x16x128_f8f6f4 v[54:57], v[234:241], v[186:193], v[54:57], v205, v205 op_sel_hi:[0,0,0]
	v_mfma_scale_f32_16x16x128_f8f6f4 v[46:49], v[226:233], v[194:201], v[46:49], v205, v205 op_sel_hi:[0,0,0]
	v_mfma_scale_f32_16x16x128_f8f6f4 v[38:41], v[234:241], v[194:201], v[38:41], v205, v205 op_sel_hi:[0,0,0]
	v_mfma_scale_f32_16x16x128_f8f6f4 v[30:33], v[226:233], v[218:225], v[30:33], v205, v205 op_sel_hi:[0,0,0]
	v_mfma_scale_f32_16x16x128_f8f6f4 v[22:25], v[234:241], v[218:225], v[22:25], v205, v205 op_sel_hi:[0,0,0]
	s_add_i32 s75, s75, 2
	s_add_u32 s18, s18, 0x100
	s_addc_u32 s19, s19, 0
	s_add_u32 s73, s73, 0x100
	s_addc_u32 s74, s74, 0
	s_cmp_gt_u32 s75, 5
	s_barrier
	s_cbranch_scc0 .LBB0_1419
	v_mov_b32_e32 v234, 0xbcb8aa3b
	v_mov_b32_e32 v235, 0xbcb8aa3b
	v_mov_b32_e32 v236, 1.0
	v_mov_b32_e32 v237, 1.0
	v_mov_b32_e32 v238, 0x3b000000
	v_mov_b32_e32 v239, 0x3b000000
	v_pk_mul_f32 v[218:219], v[140:141], v[234:235]
	v_pk_mul_f32 v[220:221], v[142:143], v[234:235]
	v_pk_mul_f32 v[226:227], v[132:133], v[234:235]
	v_pk_mul_f32 v[228:229], v[134:135], v[234:235]
	v_exp_f32_e32 v218, v218
	v_exp_f32_e32 v219, v219
	v_exp_f32_e32 v220, v220
	v_exp_f32_e32 v221, v221
	v_exp_f32_e32 v226, v226
	v_exp_f32_e32 v227, v227
	v_exp_f32_e32 v228, v228
	v_exp_f32_e32 v229, v229
	v_pk_mul_f32 v[222:223], v[140:141], v[144:145]
	v_pk_mul_f32 v[224:225], v[142:143], v[146:147]
	v_pk_mul_f32 v[230:231], v[132:133], v[136:137]
	v_pk_mul_f32 v[232:233], v[134:135], v[138:139]
	v_pk_add_f32 v[218:219], v[236:237], v[218:219]
	v_pk_add_f32 v[220:221], v[236:237], v[220:221]
	v_pk_add_f32 v[226:227], v[236:237], v[226:227]
	v_pk_add_f32 v[228:229], v[236:237], v[228:229]
	v_rcp_f32_e32 v218, v218
	v_rcp_f32_e32 v219, v219
	v_rcp_f32_e32 v220, v220
	v_rcp_f32_e32 v221, v221
	v_rcp_f32_e32 v226, v226
	v_rcp_f32_e32 v227, v227
	v_rcp_f32_e32 v228, v228
	v_rcp_f32_e32 v229, v229
	v_pk_mul_f32 v[222:223], v[238:239], v[222:223]
	v_pk_mul_f32 v[224:225], v[238:239], v[224:225]
	v_pk_mul_f32 v[230:231], v[238:239], v[230:231]
	v_pk_mul_f32 v[232:233], v[238:239], v[232:233]
	v_pk_mul_f32 v[222:223], v[218:219], v[222:223]
	v_pk_mul_f32 v[224:225], v[220:221], v[224:225]
	v_pk_mul_f32 v[230:231], v[226:227], v[230:231]
	v_pk_mul_f32 v[232:233], v[228:229], v[232:233]
	v_med3_f32 v222, v222, s26, v209
	v_med3_f32 v223, v223, s26, v209
	v_med3_f32 v224, v224, s26, v209
	v_med3_f32 v225, v225, s26, v209
	v_med3_f32 v230, v230, s26, v209
	v_med3_f32 v231, v231, s26, v209
	v_med3_f32 v232, v232, s26, v209
	v_med3_f32 v233, v233, s26, v209
	v_cvt_pk_fp8_f32 v4, v222, v223
	v_cvt_pk_fp8_f32 v4, v224, v225 op_sel:[0,0,1]
	v_cvt_pk_fp8_f32 v5, v230, v231
	v_cvt_pk_fp8_f32 v5, v232, v233 op_sel:[0,0,1]
	s_ashr_i32 s13, s12, 31
	s_lshl_b64 s[12:13], s[12:13], 11
	s_add_u32 s12, s47, s12
	s_addc_u32 s13, s50, s13
	s_ashr_i32 s14, s59, 31
	s_add_u32 s12, s12, s59
	s_addc_u32 s13, s13, s14
	v_mov_b32_e32 v130, v169
	s_nop 15
	s_nop 15
	global_store_dwordx2 v130, v[4:5], s[12:13]
	v_pk_mul_f32 v[218:219], v[122:123], v[234:235]
	v_pk_mul_f32 v[220:221], v[124:125], v[234:235]
	v_pk_mul_f32 v[226:227], v[114:115], v[234:235]
	v_pk_mul_f32 v[228:229], v[116:117], v[234:235]
	v_exp_f32_e32 v218, v218
	v_exp_f32_e32 v219, v219
	v_exp_f32_e32 v220, v220
	v_exp_f32_e32 v221, v221
	v_exp_f32_e32 v226, v226
	v_exp_f32_e32 v227, v227
	v_exp_f32_e32 v228, v228
	v_exp_f32_e32 v229, v229
	v_pk_mul_f32 v[222:223], v[122:123], v[126:127]
	v_pk_mul_f32 v[224:225], v[124:125], v[128:129]
	v_pk_mul_f32 v[230:231], v[114:115], v[118:119]
	v_pk_mul_f32 v[232:233], v[116:117], v[120:121]
	v_pk_add_f32 v[218:219], v[236:237], v[218:219]
	v_pk_add_f32 v[220:221], v[236:237], v[220:221]
	v_pk_add_f32 v[226:227], v[236:237], v[226:227]
	v_pk_add_f32 v[228:229], v[236:237], v[228:229]
	v_rcp_f32_e32 v218, v218
	v_rcp_f32_e32 v219, v219
	v_rcp_f32_e32 v220, v220
	v_rcp_f32_e32 v221, v221
	v_rcp_f32_e32 v226, v226
	v_rcp_f32_e32 v227, v227
	v_rcp_f32_e32 v228, v228
	v_rcp_f32_e32 v229, v229
	v_pk_mul_f32 v[222:223], v[238:239], v[222:223]
	v_pk_mul_f32 v[224:225], v[238:239], v[224:225]
	v_pk_mul_f32 v[230:231], v[238:239], v[230:231]
	v_pk_mul_f32 v[232:233], v[238:239], v[232:233]
	v_pk_mul_f32 v[222:223], v[218:219], v[222:223]
	v_pk_mul_f32 v[224:225], v[220:221], v[224:225]
	v_pk_mul_f32 v[230:231], v[226:227], v[230:231]
	v_pk_mul_f32 v[232:233], v[228:229], v[232:233]
	v_med3_f32 v222, v222, s26, v209
	v_med3_f32 v223, v223, s26, v209
	v_med3_f32 v224, v224, s26, v209
	v_med3_f32 v225, v225, s26, v209
	v_med3_f32 v230, v230, s26, v209
	v_med3_f32 v231, v231, s26, v209
	v_med3_f32 v232, v232, s26, v209
	v_med3_f32 v233, v233, s26, v209
	v_cvt_pk_fp8_f32 v4, v222, v223
	v_cvt_pk_fp8_f32 v4, v224, v225 op_sel:[0,0,1]
	v_cvt_pk_fp8_f32 v5, v230, v231
	v_cvt_pk_fp8_f32 v5, v232, v233 op_sel:[0,0,1]
	v_lshl_add_u64 v[2:3], s[12:13], 0, v[130:131]
	s_mov_b32 s12, 0x8000
	v_add_co_u32_e32 v6, vcc, s12, v2
	s_nop 0
	v_addc_co_u32_e32 v7, vcc, 0, v3, vcc
	global_store_dwordx2 v[6:7], v[4:5], off
	v_pk_mul_f32 v[218:219], v[106:107], v[234:235]
	v_pk_mul_f32 v[220:221], v[108:109], v[234:235]
	v_pk_mul_f32 v[226:227], v[98:99], v[234:235]
	v_pk_mul_f32 v[228:229], v[100:101], v[234:235]
	v_exp_f32_e32 v218, v218
	v_exp_f32_e32 v219, v219
	v_exp_f32_e32 v220, v220
	v_exp_f32_e32 v221, v221
	v_exp_f32_e32 v226, v226
	v_exp_f32_e32 v227, v227
	v_exp_f32_e32 v228, v228
	v_exp_f32_e32 v229, v229
	v_pk_mul_f32 v[222:223], v[106:107], v[110:111]
	v_pk_mul_f32 v[224:225], v[108:109], v[112:113]
	v_pk_mul_f32 v[230:231], v[98:99], v[102:103]
	v_pk_mul_f32 v[232:233], v[100:101], v[104:105]
	v_pk_add_f32 v[218:219], v[236:237], v[218:219]
	v_pk_add_f32 v[220:221], v[236:237], v[220:221]
	v_pk_add_f32 v[226:227], v[236:237], v[226:227]
	v_pk_add_f32 v[228:229], v[236:237], v[228:229]
	v_rcp_f32_e32 v218, v218
	v_rcp_f32_e32 v219, v219
	v_rcp_f32_e32 v220, v220
	v_rcp_f32_e32 v221, v221
	v_rcp_f32_e32 v226, v226
	v_rcp_f32_e32 v227, v227
	v_rcp_f32_e32 v228, v228
	v_rcp_f32_e32 v229, v229
	v_pk_mul_f32 v[222:223], v[238:239], v[222:223]
	v_pk_mul_f32 v[224:225], v[238:239], v[224:225]
	v_pk_mul_f32 v[230:231], v[238:239], v[230:231]
	v_pk_mul_f32 v[232:233], v[238:239], v[232:233]
	v_pk_mul_f32 v[222:223], v[218:219], v[222:223]
	v_pk_mul_f32 v[224:225], v[220:221], v[224:225]
	v_pk_mul_f32 v[230:231], v[226:227], v[230:231]
	v_pk_mul_f32 v[232:233], v[228:229], v[232:233]
	v_med3_f32 v222, v222, s26, v209
	v_med3_f32 v223, v223, s26, v209
	v_med3_f32 v224, v224, s26, v209
	v_med3_f32 v225, v225, s26, v209
	v_med3_f32 v230, v230, s26, v209
	v_med3_f32 v231, v231, s26, v209
	v_med3_f32 v232, v232, s26, v209
	v_med3_f32 v233, v233, s26, v209
	v_cvt_pk_fp8_f32 v4, v222, v223
	v_cvt_pk_fp8_f32 v4, v224, v225 op_sel:[0,0,1]
	v_cvt_pk_fp8_f32 v5, v230, v231
	v_cvt_pk_fp8_f32 v5, v232, v233 op_sel:[0,0,1]
	s_mov_b32 s12, 0x10000
	v_add_co_u32_e32 v6, vcc, s12, v2
	s_nop 0
	v_addc_co_u32_e32 v7, vcc, 0, v3, vcc
	global_store_dwordx2 v[6:7], v[4:5], off
	v_pk_mul_f32 v[218:219], v[90:91], v[234:235]
	v_pk_mul_f32 v[220:221], v[92:93], v[234:235]
	v_pk_mul_f32 v[226:227], v[78:79], v[234:235]
	v_pk_mul_f32 v[228:229], v[80:81], v[234:235]
	v_exp_f32_e32 v218, v218
	v_exp_f32_e32 v219, v219
	v_exp_f32_e32 v220, v220
	v_exp_f32_e32 v221, v221
	v_exp_f32_e32 v226, v226
	v_exp_f32_e32 v227, v227
	v_exp_f32_e32 v228, v228
	v_exp_f32_e32 v229, v229
	v_pk_mul_f32 v[222:223], v[90:91], v[94:95]
	v_pk_mul_f32 v[224:225], v[92:93], v[96:97]
	v_pk_mul_f32 v[230:231], v[78:79], v[86:87]
	v_pk_mul_f32 v[232:233], v[80:81], v[88:89]
	v_pk_add_f32 v[218:219], v[236:237], v[218:219]
	v_pk_add_f32 v[220:221], v[236:237], v[220:221]
	v_pk_add_f32 v[226:227], v[236:237], v[226:227]
	v_pk_add_f32 v[228:229], v[236:237], v[228:229]
	v_rcp_f32_e32 v218, v218
	v_rcp_f32_e32 v219, v219
	v_rcp_f32_e32 v220, v220
	v_rcp_f32_e32 v221, v221
	v_rcp_f32_e32 v226, v226
	v_rcp_f32_e32 v227, v227
	v_rcp_f32_e32 v228, v228
	v_rcp_f32_e32 v229, v229
	v_pk_mul_f32 v[222:223], v[238:239], v[222:223]
	v_pk_mul_f32 v[224:225], v[238:239], v[224:225]
	v_pk_mul_f32 v[230:231], v[238:239], v[230:231]
	v_pk_mul_f32 v[232:233], v[238:239], v[232:233]
	v_pk_mul_f32 v[222:223], v[218:219], v[222:223]
	v_pk_mul_f32 v[224:225], v[220:221], v[224:225]
	v_pk_mul_f32 v[230:231], v[226:227], v[230:231]
	v_pk_mul_f32 v[232:233], v[228:229], v[232:233]
	v_med3_f32 v222, v222, s26, v209
	v_med3_f32 v223, v223, s26, v209
	v_med3_f32 v224, v224, s26, v209
	v_med3_f32 v225, v225, s26, v209
	v_med3_f32 v230, v230, s26, v209
	v_med3_f32 v231, v231, s26, v209
	v_med3_f32 v232, v232, s26, v209
	v_med3_f32 v233, v233, s26, v209
	v_cvt_pk_fp8_f32 v4, v222, v223
	v_cvt_pk_fp8_f32 v4, v224, v225 op_sel:[0,0,1]
	v_cvt_pk_fp8_f32 v5, v230, v231
	v_cvt_pk_fp8_f32 v5, v232, v233 op_sel:[0,0,1]
	s_mov_b32 s12, 0x18000
	v_add_co_u32_e32 v6, vcc, s12, v2
	s_nop 0
	v_addc_co_u32_e32 v7, vcc, 0, v3, vcc
	global_store_dwordx2 v[6:7], v[4:5], off
	v_pk_mul_f32 v[218:219], v[74:75], v[234:235]
	v_pk_mul_f32 v[220:221], v[76:77], v[234:235]
	v_pk_mul_f32 v[226:227], v[66:67], v[234:235]
	v_pk_mul_f32 v[228:229], v[68:69], v[234:235]
	v_exp_f32_e32 v218, v218
	v_exp_f32_e32 v219, v219
	v_exp_f32_e32 v220, v220
	v_exp_f32_e32 v221, v221
	v_exp_f32_e32 v226, v226
	v_exp_f32_e32 v227, v227
	v_exp_f32_e32 v228, v228
	v_exp_f32_e32 v229, v229
	v_pk_mul_f32 v[222:223], v[74:75], v[82:83]
	v_pk_mul_f32 v[224:225], v[76:77], v[84:85]
	v_pk_mul_f32 v[230:231], v[66:67], v[70:71]
	v_pk_mul_f32 v[232:233], v[68:69], v[72:73]
	v_pk_add_f32 v[218:219], v[236:237], v[218:219]
	v_pk_add_f32 v[220:221], v[236:237], v[220:221]
	v_pk_add_f32 v[226:227], v[236:237], v[226:227]
	v_pk_add_f32 v[228:229], v[236:237], v[228:229]
	v_rcp_f32_e32 v218, v218
	v_rcp_f32_e32 v219, v219
	v_rcp_f32_e32 v220, v220
	v_rcp_f32_e32 v221, v221
	v_rcp_f32_e32 v226, v226
	v_rcp_f32_e32 v227, v227
	v_rcp_f32_e32 v228, v228
	v_rcp_f32_e32 v229, v229
	v_pk_mul_f32 v[222:223], v[238:239], v[222:223]
	v_pk_mul_f32 v[224:225], v[238:239], v[224:225]
	v_pk_mul_f32 v[230:231], v[238:239], v[230:231]
	v_pk_mul_f32 v[232:233], v[238:239], v[232:233]
	v_pk_mul_f32 v[222:223], v[218:219], v[222:223]
	v_pk_mul_f32 v[224:225], v[220:221], v[224:225]
	v_pk_mul_f32 v[230:231], v[226:227], v[230:231]
	v_pk_mul_f32 v[232:233], v[228:229], v[232:233]
	v_med3_f32 v222, v222, s26, v209
	v_med3_f32 v223, v223, s26, v209
	v_med3_f32 v224, v224, s26, v209
	v_med3_f32 v225, v225, s26, v209
	v_med3_f32 v230, v230, s26, v209
	v_med3_f32 v231, v231, s26, v209
	v_med3_f32 v232, v232, s26, v209
	v_med3_f32 v233, v233, s26, v209
	v_cvt_pk_fp8_f32 v4, v222, v223
	v_cvt_pk_fp8_f32 v4, v224, v225 op_sel:[0,0,1]
	v_cvt_pk_fp8_f32 v5, v230, v231
	v_cvt_pk_fp8_f32 v5, v232, v233 op_sel:[0,0,1]
	s_mov_b32 s12, 0x40000
	v_add_co_u32_e32 v6, vcc, s12, v2
	s_nop 0
	v_addc_co_u32_e32 v7, vcc, 0, v3, vcc
	global_store_dwordx2 v[6:7], v[4:5], off
	v_pk_mul_f32 v[218:219], v[58:59], v[234:235]
	v_pk_mul_f32 v[220:221], v[60:61], v[234:235]
	v_pk_mul_f32 v[226:227], v[50:51], v[234:235]
	v_pk_mul_f32 v[228:229], v[52:53], v[234:235]
	v_exp_f32_e32 v218, v218
	v_exp_f32_e32 v219, v219
	v_exp_f32_e32 v220, v220
	v_exp_f32_e32 v221, v221
	v_exp_f32_e32 v226, v226
	v_exp_f32_e32 v227, v227
	v_exp_f32_e32 v228, v228
	v_exp_f32_e32 v229, v229
	v_pk_mul_f32 v[222:223], v[58:59], v[62:63]
	v_pk_mul_f32 v[224:225], v[60:61], v[64:65]
	v_pk_mul_f32 v[230:231], v[50:51], v[54:55]
	v_pk_mul_f32 v[232:233], v[52:53], v[56:57]
	v_pk_add_f32 v[218:219], v[236:237], v[218:219]
	v_pk_add_f32 v[220:221], v[236:237], v[220:221]
	v_pk_add_f32 v[226:227], v[236:237], v[226:227]
	v_pk_add_f32 v[228:229], v[236:237], v[228:229]
	v_rcp_f32_e32 v218, v218
	v_rcp_f32_e32 v219, v219
	v_rcp_f32_e32 v220, v220
	v_rcp_f32_e32 v221, v221
	v_rcp_f32_e32 v226, v226
	v_rcp_f32_e32 v227, v227
	v_rcp_f32_e32 v228, v228
	v_rcp_f32_e32 v229, v229
	v_pk_mul_f32 v[222:223], v[238:239], v[222:223]
	v_pk_mul_f32 v[224:225], v[238:239], v[224:225]
	v_pk_mul_f32 v[230:231], v[238:239], v[230:231]
	v_pk_mul_f32 v[232:233], v[238:239], v[232:233]
	v_pk_mul_f32 v[222:223], v[218:219], v[222:223]
	v_pk_mul_f32 v[224:225], v[220:221], v[224:225]
	v_pk_mul_f32 v[230:231], v[226:227], v[230:231]
	v_pk_mul_f32 v[232:233], v[228:229], v[232:233]
	v_med3_f32 v222, v222, s26, v209
	v_med3_f32 v223, v223, s26, v209
	v_med3_f32 v224, v224, s26, v209
	v_med3_f32 v225, v225, s26, v209
	v_med3_f32 v230, v230, s26, v209
	v_med3_f32 v231, v231, s26, v209
	v_med3_f32 v232, v232, s26, v209
	v_med3_f32 v233, v233, s26, v209
	v_cvt_pk_fp8_f32 v4, v222, v223
	v_cvt_pk_fp8_f32 v4, v224, v225 op_sel:[0,0,1]
	v_cvt_pk_fp8_f32 v5, v230, v231
	v_cvt_pk_fp8_f32 v5, v232, v233 op_sel:[0,0,1]
	s_mov_b32 s12, 0x48000
	v_add_co_u32_e32 v6, vcc, s12, v2
	s_nop 0
	v_addc_co_u32_e32 v7, vcc, 0, v3, vcc
	global_store_dwordx2 v[6:7], v[4:5], off
	v_pk_mul_f32 v[218:219], v[42:43], v[234:235]
	v_pk_mul_f32 v[220:221], v[44:45], v[234:235]
	v_pk_mul_f32 v[226:227], v[34:35], v[234:235]
	v_pk_mul_f32 v[228:229], v[36:37], v[234:235]
	v_exp_f32_e32 v218, v218
	v_exp_f32_e32 v219, v219
	v_exp_f32_e32 v220, v220
	v_exp_f32_e32 v221, v221
	v_exp_f32_e32 v226, v226
	v_exp_f32_e32 v227, v227
	v_exp_f32_e32 v228, v228
	v_exp_f32_e32 v229, v229
	v_pk_mul_f32 v[222:223], v[42:43], v[46:47]
	v_pk_mul_f32 v[224:225], v[44:45], v[48:49]
	v_pk_mul_f32 v[230:231], v[34:35], v[38:39]
	v_pk_mul_f32 v[232:233], v[36:37], v[40:41]
	v_pk_add_f32 v[218:219], v[236:237], v[218:219]
	v_pk_add_f32 v[220:221], v[236:237], v[220:221]
	v_pk_add_f32 v[226:227], v[236:237], v[226:227]
	v_pk_add_f32 v[228:229], v[236:237], v[228:229]
	v_rcp_f32_e32 v218, v218
	v_rcp_f32_e32 v219, v219
	v_rcp_f32_e32 v220, v220
	v_rcp_f32_e32 v221, v221
	v_rcp_f32_e32 v226, v226
	v_rcp_f32_e32 v227, v227
	v_rcp_f32_e32 v228, v228
	v_rcp_f32_e32 v229, v229
	v_pk_mul_f32 v[222:223], v[238:239], v[222:223]
	v_pk_mul_f32 v[224:225], v[238:239], v[224:225]
	v_pk_mul_f32 v[230:231], v[238:239], v[230:231]
	v_pk_mul_f32 v[232:233], v[238:239], v[232:233]
	v_pk_mul_f32 v[222:223], v[218:219], v[222:223]
	v_pk_mul_f32 v[224:225], v[220:221], v[224:225]
	v_pk_mul_f32 v[230:231], v[226:227], v[230:231]
	v_pk_mul_f32 v[232:233], v[228:229], v[232:233]
	v_med3_f32 v222, v222, s26, v209
	v_med3_f32 v223, v223, s26, v209
	v_med3_f32 v224, v224, s26, v209
	v_med3_f32 v225, v225, s26, v209
	v_med3_f32 v230, v230, s26, v209
	v_med3_f32 v231, v231, s26, v209
	v_med3_f32 v232, v232, s26, v209
	v_med3_f32 v233, v233, s26, v209
	v_cvt_pk_fp8_f32 v4, v222, v223
	v_cvt_pk_fp8_f32 v4, v224, v225 op_sel:[0,0,1]
	v_cvt_pk_fp8_f32 v5, v230, v231
	v_cvt_pk_fp8_f32 v5, v232, v233 op_sel:[0,0,1]
	s_mov_b32 s12, 0x50000
	v_add_co_u32_e32 v6, vcc, s12, v2
	s_nop 0
	v_addc_co_u32_e32 v7, vcc, 0, v3, vcc
	global_store_dwordx2 v[6:7], v[4:5], off
	v_pk_mul_f32 v[218:219], v[26:27], v[234:235]
	v_pk_mul_f32 v[220:221], v[28:29], v[234:235]
	v_pk_mul_f32 v[226:227], v[18:19], v[234:235]
	v_pk_mul_f32 v[228:229], v[20:21], v[234:235]
	v_exp_f32_e32 v218, v218
	v_exp_f32_e32 v219, v219
	v_exp_f32_e32 v220, v220
	v_exp_f32_e32 v221, v221
	v_exp_f32_e32 v226, v226
	v_exp_f32_e32 v227, v227
	v_exp_f32_e32 v228, v228
	v_exp_f32_e32 v229, v229
	v_pk_mul_f32 v[222:223], v[26:27], v[30:31]
	v_pk_mul_f32 v[224:225], v[28:29], v[32:33]
	v_pk_mul_f32 v[230:231], v[18:19], v[22:23]
	v_pk_mul_f32 v[232:233], v[20:21], v[24:25]
	v_pk_add_f32 v[218:219], v[236:237], v[218:219]
	v_pk_add_f32 v[220:221], v[236:237], v[220:221]
	v_pk_add_f32 v[226:227], v[236:237], v[226:227]
	v_pk_add_f32 v[228:229], v[236:237], v[228:229]
	v_rcp_f32_e32 v218, v218
	v_rcp_f32_e32 v219, v219
	v_rcp_f32_e32 v220, v220
	v_rcp_f32_e32 v221, v221
	v_rcp_f32_e32 v226, v226
	v_rcp_f32_e32 v227, v227
	v_rcp_f32_e32 v228, v228
	v_rcp_f32_e32 v229, v229
	v_pk_mul_f32 v[222:223], v[238:239], v[222:223]
	v_pk_mul_f32 v[224:225], v[238:239], v[224:225]
	v_pk_mul_f32 v[230:231], v[238:239], v[230:231]
	v_pk_mul_f32 v[232:233], v[238:239], v[232:233]
	v_pk_mul_f32 v[222:223], v[218:219], v[222:223]
	v_pk_mul_f32 v[224:225], v[220:221], v[224:225]
	v_pk_mul_f32 v[230:231], v[226:227], v[230:231]
	v_pk_mul_f32 v[232:233], v[228:229], v[232:233]
	v_med3_f32 v222, v222, s26, v209
	v_med3_f32 v223, v223, s26, v209
	v_med3_f32 v224, v224, s26, v209
	v_med3_f32 v225, v225, s26, v209
	v_med3_f32 v230, v230, s26, v209
	v_med3_f32 v231, v231, s26, v209
	v_med3_f32 v232, v232, s26, v209
	v_med3_f32 v233, v233, s26, v209
	v_cvt_pk_fp8_f32 v4, v222, v223
	v_cvt_pk_fp8_f32 v4, v224, v225 op_sel:[0,0,1]
	v_cvt_pk_fp8_f32 v5, v230, v231
	v_cvt_pk_fp8_f32 v5, v232, v233 op_sel:[0,0,1]
	v_add_co_u32_e32 v2, vcc, 0x58000, v2
	s_nop 0
	v_addc_co_u32_e32 v3, vcc, 0, v3, vcc
	s_and_b64 vcc, exec, s[4:5]
	s_mov_b32 s12, s6
	s_mov_b32 s59, s7
	s_mov_b64 s[60:61], s[8:9]
	s_mov_b64 s[18:19], s[10:11]
	global_store_dwordx2 v[2:3], v[4:5], off
	s_cbranch_vccz .LBB0_1416
	s_waitcnt vmcnt(0)
	s_setprio 0
	s_cmpk_gt_u32 s27, 0xff
	s_movk_i32 s47, 0x900
	s_cbranch_scc1 .LBB0_1423
	s_barrier

.LBB0_1479:
	s_add_u32 s46, s4, 0x67d68000
	v_and_b32_e32 v17, 15, v16
	v_and_b32_e32 v18, 48, v16
	v_lshlrev_b32_e32 v16, 2, v16
	s_addc_u32 s47, s5, 0
	s_and_b32 s7, s7, 3
	s_lshl_b32 s4, s6, 13
	v_lshl_or_b32 v19, v17, 6, v18
	v_and_b32_e32 v16, 32, v16
	s_add_i32 m0, s17, 0x18000
	v_lshl_add_u64 v[8:9], v[8:9], 0, s[30:31]
	v_bitop3_b32 v20, v19, s4, v16 bitop3:0xde
	s_lshl_b32 s4, s7, 12
	s_waitcnt vmcnt(4)
	s_barrier
	v_readfirstlane_b32 s100, v0
	s_cmp_lt_u32 s100, 0x100
	s_cbranch_scc1 .Lmy_sp_down
	s_setprio 1
.Lmy_sp_down:
	global_load_lds_dwordx4 v[8:9], off
	v_lshl_add_u64 v[6:7], v[6:7], 0, s[30:31]
	s_add_i32 m0, s17, 0x1a000
	s_add_i32 s50, s17, 0x8000
	s_add_i32 s51, s17, 0xa000
	v_bitop3_b32 v168, v19, s4, v16 bitop3:0xde
	global_load_lds_dwordx4 v[6:7], off
	v_lshl_add_u64 v[4:5], v[4:5], 0, s[30:31]
	s_mov_b32 m0, s50
	s_add_u32 s4, s64, 0x4080
	global_load_lds_dwordx4 v[4:5], off
	v_lshl_add_u64 v[2:3], v[2:3], 0, s[30:31]
	s_mov_b32 m0, s51
	s_addc_u32 s5, s65, 0
	global_load_lds_dwordx4 v[2:3], off
	s_add_i32 m0, s17, 0x1c000
	v_lshl_add_u64 v[2:3], s[4:5], 0, v[154:155]
	global_load_lds_dwordx4 v[2:3], off
	v_lshl_add_u64 v[2:3], s[4:5], 0, v[150:151]
	s_add_i32 m0, s17, 0x1e000
	s_lshl_b32 s4, s7, 6
	global_load_lds_dwordx4 v[2:3], off
	v_lshlrev_b32_e32 v2, 10, v17
	v_lshl_or_b32 v2, s6, 16, v2
	v_or3_b32 v169, v2, s4, v18
	v_lshlrev_b32_e32 v2, 14, v14
	v_and_b32_e32 v2, 0xffff8000, v2
	v_lshl_add_u32 v2, v13, 11, v2
	v_and_b32_e32 v3, 1, v14
	v_lshl_or_b32 v2, v3, 6, v2
	v_lshl_add_u32 v156, v15, 1, v2
	v_lshlrev_b32_e32 v2, 14, v10
	v_and_b32_e32 v2, 0xffff8000, v2
	s_waitcnt vmcnt(6)
	v_lshl_add_u32 v2, v11, 11, v2
	v_and_b32_e32 v3, 1, v10
	v_lshl_or_b32 v2, v3, 6, v2
	v_mov_b32_e32 v157, v131
	v_lshl_add_u32 v158, v12, 1, v2
	v_mov_b32_e32 v159, v131
	s_mov_b32 s53, 0
	v_add_u32_e32 v170, 0, v20
	s_barrier

.LBB0_1482:
	s_add_i32 s15, 0, 0x10000
	v_add_u32_e32 v130, s15, v168
	ds_read_b128 v[2:5], v130
	ds_read_b128 v[6:9], v130 offset:1024
	ds_read_b128 v[10:13], v130 offset:2048
	ds_read_b128 v[14:17], v130 offset:3072
	s_add_u32 s58, s62, 0x40080
	s_addc_u32 s59, s63, 0
	s_add_i32 s7, s17, 0xc000
	v_lshl_add_u64 v[50:51], s[58:59], 0, v[152:153]
	s_mov_b32 m0, s7
	s_add_i32 s9, s17, 0xe000
	ds_read_b128 v[18:21], v170
	ds_read_b128 v[22:25], v170 offset:1024
	ds_read_b128 v[26:29], v170 offset:2048
	ds_read_b128 v[30:33], v170 offset:3072
	ds_read_b128 v[34:37], v170 offset:4096
	ds_read_b128 v[38:41], v170 offset:5120
	ds_read_b128 v[42:45], v170 offset:6144
	ds_read_b128 v[46:49], v170 offset:7168
	global_load_lds_dwordx4 v[50:51], off
	v_lshl_add_u64 v[50:51], s[58:59], 0, v[148:149]
	s_mov_b32 m0, s9
	s_nop 0
	global_load_lds_dwordx4 v[50:51], off
	s_waitcnt lgkmcnt(8)
	s_waitcnt vmcnt(10)
	s_barrier
	s_waitcnt lgkmcnt(6)
	v_mfma_scale_f32_16x16x128_f8f6f4 v[132:135], v[2:9], v[18:25], 0, v205, v205 op_sel_hi:[0,0,0]
	v_mfma_scale_f32_16x16x128_f8f6f4 v[136:139], v[10:17], v[18:25], 0, v205, v205 op_sel_hi:[0,0,0]
	s_waitcnt lgkmcnt(4)
	v_mfma_scale_f32_16x16x128_f8f6f4 v[118:121], v[2:9], v[26:33], 0, v205, v205 op_sel_hi:[0,0,0]
	v_mfma_scale_f32_16x16x128_f8f6f4 v[114:117], v[10:17], v[26:33], 0, v205, v205 op_sel_hi:[0,0,0]
	s_waitcnt lgkmcnt(2)
	v_mfma_scale_f32_16x16x128_f8f6f4 v[102:105], v[2:9], v[34:41], 0, v205, v205 op_sel_hi:[0,0,0]
	v_mfma_scale_f32_16x16x128_f8f6f4 v[98:101], v[10:17], v[34:41], 0, v205, v205 op_sel_hi:[0,0,0]
	s_waitcnt lgkmcnt(0)
	v_mfma_scale_f32_16x16x128_f8f6f4 v[70:73], v[2:9], v[42:49], 0, v205, v205 op_sel_hi:[0,0,0]
	v_mfma_scale_f32_16x16x128_f8f6f4 v[66:69], v[10:17], v[42:49], 0, v205, v205 op_sel_hi:[0,0,0]
	s_barrier
	s_add_i32 s58, 0, 0x14000
	v_lshl_add_u64 v[164:165], s[64:65], 0, v[154:155]
	s_mov_b64 s[66:67], 0x100
	s_add_i32 s15, s15, s38
	v_add_u32_e32 v171, s58, v168
	v_lshl_add_u64 v[50:51], v[164:165], 0, s[66:67]
	s_mov_b32 m0, s15
	v_lshl_add_u64 v[166:167], s[64:65], 0, v[150:151]
	s_add_i32 s57, s15, 0x2000
	ds_read_b128 v[178:181], v171
	ds_read_b128 v[182:185], v171 offset:1024
	ds_read_b128 v[186:189], v171 offset:2048
	ds_read_b128 v[190:193], v171 offset:3072
	global_load_lds_dwordx4 v[50:51], off
	v_lshl_add_u64 v[50:51], v[166:167], 0, s[66:67]
	s_mov_b32 m0, s57
	s_nop 0
	global_load_lds_dwordx4 v[50:51], off
	s_waitcnt vmcnt(10)
	s_barrier
	s_waitcnt lgkmcnt(2)
	v_mfma_scale_f32_16x16x128_f8f6f4 v[140:143], v[178:185], v[18:25], 0, v205, v205 op_sel_hi:[0,0,0]
	s_waitcnt lgkmcnt(0)
	v_mfma_scale_f32_16x16x128_f8f6f4 v[144:147], v[186:193], v[18:25], 0, v205, v205 op_sel_hi:[0,0,0]
	v_mfma_scale_f32_16x16x128_f8f6f4 v[126:129], v[178:185], v[26:33], 0, v205, v205 op_sel_hi:[0,0,0]
	v_mfma_scale_f32_16x16x128_f8f6f4 v[122:125], v[186:193], v[26:33], 0, v205, v205 op_sel_hi:[0,0,0]
	v_mfma_scale_f32_16x16x128_f8f6f4 v[110:113], v[178:185], v[34:41], 0, v205, v205 op_sel_hi:[0,0,0]
	v_mfma_scale_f32_16x16x128_f8f6f4 v[106:109], v[186:193], v[34:41], 0, v205, v205 op_sel_hi:[0,0,0]
	v_mfma_scale_f32_16x16x128_f8f6f4 v[86:89], v[178:185], v[42:49], 0, v205, v205 op_sel_hi:[0,0,0]
	v_mfma_scale_f32_16x16x128_f8f6f4 v[82:85], v[186:193], v[42:49], 0, v205, v205 op_sel_hi:[0,0,0]
	v_lshl_add_u64 v[160:161], s[62:63], 0, v[152:153]
	s_mov_b32 m0, s17
	v_lshl_add_u64 v[26:27], v[160:161], 0, s[66:67]
	v_lshl_add_u64 v[162:163], s[62:63], 0, v[148:149]
	s_barrier
	ds_read_b128 v[18:21], v170 offset:16384
	ds_read_b128 v[22:25], v170 offset:17408
	ds_read_b128 v[42:45], v170 offset:18432
	ds_read_b128 v[46:49], v170 offset:19456
	ds_read_b128 v[194:197], v170 offset:20480
	ds_read_b128 v[198:201], v170 offset:21504
	ds_read_b128 v[218:221], v170 offset:22528
	ds_read_b128 v[222:225], v170 offset:23552
	global_load_lds_dwordx4 v[26:27], off
	v_lshl_add_u64 v[26:27], v[162:163], 0, s[66:67]
	s_mov_b32 m0, s43
	s_nop 0
	global_load_lds_dwordx4 v[26:27], off
	s_barrier
	s_waitcnt lgkmcnt(6)
	v_mfma_scale_f32_16x16x128_f8f6f4 v[78:81], v[2:9], v[18:25], 0, v205, v205 op_sel_hi:[0,0,0]
	v_mfma_scale_f32_16x16x128_f8f6f4 v[74:77], v[10:17], v[18:25], 0, v205, v205 op_sel_hi:[0,0,0]
	s_waitcnt lgkmcnt(4)
	v_mfma_scale_f32_16x16x128_f8f6f4 v[54:57], v[2:9], v[42:49], 0, v205, v205 op_sel_hi:[0,0,0]
	v_mfma_scale_f32_16x16x128_f8f6f4 v[50:53], v[10:17], v[42:49], 0, v205, v205 op_sel_hi:[0,0,0]
	s_waitcnt lgkmcnt(2)
	v_mfma_scale_f32_16x16x128_f8f6f4 v[38:41], v[2:9], v[194:201], 0, v205, v205 op_sel_hi:[0,0,0]
	v_mfma_scale_f32_16x16x128_f8f6f4 v[34:37], v[10:17], v[194:201], 0, v205, v205 op_sel_hi:[0,0,0]
	s_waitcnt lgkmcnt(0)
	v_mfma_scale_f32_16x16x128_f8f6f4 v[30:33], v[2:9], v[218:225], 0, v205, v205 op_sel_hi:[0,0,0]
	v_mfma_scale_f32_16x16x128_f8f6f4 v[26:29], v[10:17], v[218:225], 0, v205, v205 op_sel_hi:[0,0,0]
	s_barrier
	s_add_u32 s66, s64, 0x4100
	s_addc_u32 s67, s65, 0
	s_add_i32 s58, s58, s38
	v_lshl_add_u64 v[2:3], s[66:67], 0, v[154:155]
	s_mov_b32 m0, s58
	s_add_i32 s59, s58, 0x2000
	global_load_lds_dwordx4 v[2:3], off
	v_lshl_add_u64 v[2:3], s[66:67], 0, v[150:151]
	s_mov_b32 m0, s59
	s_nop 0
	global_load_lds_dwordx4 v[2:3], off
	s_waitcnt vmcnt(10)
	s_barrier
	v_mfma_scale_f32_16x16x128_f8f6f4 v[94:97], v[178:185], v[18:25], 0, v205, v205 op_sel_hi:[0,0,0]
	v_mfma_scale_f32_16x16x128_f8f6f4 v[90:93], v[186:193], v[18:25], 0, v205, v205 op_sel_hi:[0,0,0]
	v_mfma_scale_f32_16x16x128_f8f6f4 v[62:65], v[178:185], v[42:49], 0, v205, v205 op_sel_hi:[0,0,0]
	v_mfma_scale_f32_16x16x128_f8f6f4 v[58:61], v[186:193], v[42:49], 0, v205, v205 op_sel_hi:[0,0,0]
	v_mfma_scale_f32_16x16x128_f8f6f4 v[46:49], v[178:185], v[194:201], 0, v205, v205 op_sel_hi:[0,0,0]
	v_mfma_scale_f32_16x16x128_f8f6f4 v[42:45], v[186:193], v[194:201], 0, v205, v205 op_sel_hi:[0,0,0]
	v_mfma_scale_f32_16x16x128_f8f6f4 v[22:25], v[178:185], v[218:225], 0, v205, v205 op_sel_hi:[0,0,0]
	v_mfma_scale_f32_16x16x128_f8f6f4 v[18:21], v[186:193], v[218:225], 0, v205, v205 op_sel_hi:[0,0,0]
	s_add_i32 s68, 0, 0x18000
	v_add_u32_e32 v172, s68, v168
	s_barrier
	ds_read_b128 v[10:13], v172
	ds_read_b128 v[14:17], v172 offset:1024
	ds_read_b128 v[2:5], v172 offset:2048
	ds_read_b128 v[6:9], v172 offset:3072
	s_add_u32 s66, s62, 0x40100
	s_addc_u32 s67, s63, 0
	s_mov_b32 m0, s44
	v_lshl_add_u64 v[174:175], s[66:67], 0, v[152:153]
	ds_read_b128 v[178:181], v170 offset:32768
	ds_read_b128 v[182:185], v170 offset:33792
	ds_read_b128 v[186:189], v170 offset:34816
	ds_read_b128 v[190:193], v170 offset:35840
	ds_read_b128 v[194:197], v170 offset:36864
	ds_read_b128 v[198:201], v170 offset:37888
	ds_read_b128 v[218:221], v170 offset:38912
	ds_read_b128 v[222:225], v170 offset:39936
	global_load_lds_dwordx4 v[174:175], off
	v_lshl_add_u64 v[174:175], s[66:67], 0, v[148:149]
	s_mov_b32 m0, s45
	s_nop 0
	global_load_lds_dwordx4 v[174:175], off
	s_waitcnt lgkmcnt(8)
	s_waitcnt vmcnt(10)
	s_barrier
	s_waitcnt lgkmcnt(6)
	v_mfma_scale_f32_16x16x128_f8f6f4 v[132:135], v[10:17], v[178:185], v[132:135], v205, v205 op_sel_hi:[0,0,0]
	v_mfma_scale_f32_16x16x128_f8f6f4 v[136:139], v[2:9], v[178:185], v[136:139], v205, v205 op_sel_hi:[0,0,0]
	s_waitcnt lgkmcnt(4)
	v_mfma_scale_f32_16x16x128_f8f6f4 v[118:121], v[10:17], v[186:193], v[118:121], v205, v205 op_sel_hi:[0,0,0]
	v_mfma_scale_f32_16x16x128_f8f6f4 v[114:117], v[2:9], v[186:193], v[114:117], v205, v205 op_sel_hi:[0,0,0]
	s_waitcnt lgkmcnt(2)
	v_mfma_scale_f32_16x16x128_f8f6f4 v[102:105], v[10:17], v[194:201], v[102:105], v205, v205 op_sel_hi:[0,0,0]
	v_mfma_scale_f32_16x16x128_f8f6f4 v[98:101], v[2:9], v[194:201], v[98:101], v205, v205 op_sel_hi:[0,0,0]
	s_waitcnt lgkmcnt(0)
	v_mfma_scale_f32_16x16x128_f8f6f4 v[70:73], v[10:17], v[218:225], v[70:73], v205, v205 op_sel_hi:[0,0,0]
	v_mfma_scale_f32_16x16x128_f8f6f4 v[66:69], v[2:9], v[218:225], v[66:69], v205, v205 op_sel_hi:[0,0,0]
	s_barrier
	s_add_i32 s70, 0, 0x1c000
	s_mov_b64 s[66:67], 0x180
	s_add_i32 s68, s68, s38
	v_add_u32_e32 v173, s70, v168
	v_lshl_add_u64 v[164:165], v[164:165], 0, s[66:67]
	s_mov_b32 m0, s68
	s_add_i32 s69, s68, 0x2000
	ds_read_b128 v[226:229], v173
	ds_read_b128 v[230:233], v173 offset:1024
	ds_read_b128 v[234:237], v173 offset:2048
	ds_read_b128 v[238:241], v173 offset:3072
	global_load_lds_dwordx4 v[164:165], off
	v_lshl_add_u64 v[164:165], v[166:167], 0, s[66:67]
	s_mov_b32 m0, s69
	s_nop 0
	global_load_lds_dwordx4 v[164:165], off
	s_waitcnt vmcnt(10)
	s_barrier
	s_waitcnt lgkmcnt(2)
	v_mfma_scale_f32_16x16x128_f8f6f4 v[140:143], v[226:233], v[178:185], v[140:143], v205, v205 op_sel_hi:[0,0,0]
	s_waitcnt lgkmcnt(0)
	v_mfma_scale_f32_16x16x128_f8f6f4 v[144:147], v[234:241], v[178:185], v[144:147], v205, v205 op_sel_hi:[0,0,0]
	v_mfma_scale_f32_16x16x128_f8f6f4 v[126:129], v[226:233], v[186:193], v[126:129], v205, v205 op_sel_hi:[0,0,0]
	v_mfma_scale_f32_16x16x128_f8f6f4 v[122:125], v[234:241], v[186:193], v[122:125], v205, v205 op_sel_hi:[0,0,0]
	v_mfma_scale_f32_16x16x128_f8f6f4 v[110:113], v[226:233], v[194:201], v[110:113], v205, v205 op_sel_hi:[0,0,0]
	v_mfma_scale_f32_16x16x128_f8f6f4 v[106:109], v[234:241], v[194:201], v[106:109], v205, v205 op_sel_hi:[0,0,0]
	v_mfma_scale_f32_16x16x128_f8f6f4 v[86:89], v[226:233], v[218:225], v[86:89], v205, v205 op_sel_hi:[0,0,0]
	v_mfma_scale_f32_16x16x128_f8f6f4 v[82:85], v[234:241], v[218:225], v[82:85], v205, v205 op_sel_hi:[0,0,0]
	s_mov_b32 m0, s50
	v_lshl_add_u64 v[160:161], v[160:161], 0, s[66:67]
	s_barrier
	ds_read_b128 v[178:181], v170 offset:49152
	ds_read_b128 v[182:185], v170 offset:50176
	ds_read_b128 v[186:189], v170 offset:51200
	ds_read_b128 v[190:193], v170 offset:52224
	ds_read_b128 v[194:197], v170 offset:53248
	ds_read_b128 v[198:201], v170 offset:54272
	ds_read_b128 v[218:221], v170 offset:55296
	ds_read_b128 v[222:225], v170 offset:56320
	global_load_lds_dwordx4 v[160:161], off
	v_lshl_add_u64 v[160:161], v[162:163], 0, s[66:67]
	s_mov_b32 m0, s51
	s_nop 0
	global_load_lds_dwordx4 v[160:161], off
	s_barrier
	s_waitcnt lgkmcnt(6)
	v_mfma_scale_f32_16x16x128_f8f6f4 v[78:81], v[10:17], v[178:185], v[78:81], v205, v205 op_sel_hi:[0,0,0]
	v_mfma_scale_f32_16x16x128_f8f6f4 v[74:77], v[2:9], v[178:185], v[74:77], v205, v205 op_sel_hi:[0,0,0]
	s_waitcnt lgkmcnt(4)
	v_mfma_scale_f32_16x16x128_f8f6f4 v[54:57], v[10:17], v[186:193], v[54:57], v205, v205 op_sel_hi:[0,0,0]
	v_mfma_scale_f32_16x16x128_f8f6f4 v[50:53], v[2:9], v[186:193], v[50:53], v205, v205 op_sel_hi:[0,0,0]
	s_waitcnt lgkmcnt(2)
	v_mfma_scale_f32_16x16x128_f8f6f4 v[38:41], v[10:17], v[194:201], v[38:41], v205, v205 op_sel_hi:[0,0,0]
	v_mfma_scale_f32_16x16x128_f8f6f4 v[34:37], v[2:9], v[194:201], v[34:37], v205, v205 op_sel_hi:[0,0,0]
	s_waitcnt lgkmcnt(0)
	v_mfma_scale_f32_16x16x128_f8f6f4 v[30:33], v[10:17], v[218:225], v[30:33], v205, v205 op_sel_hi:[0,0,0]
	v_mfma_scale_f32_16x16x128_f8f6f4 v[26:29], v[2:9], v[218:225], v[26:29], v205, v205 op_sel_hi:[0,0,0]
	s_barrier
	s_add_u32 s66, s64, 0x4180
	s_addc_u32 s67, s65, 0
	s_add_i32 s70, s70, s38
	v_lshl_add_u64 v[2:3], s[66:67], 0, v[154:155]
	s_mov_b32 m0, s70
	s_add_i32 s71, s70, 0x2000
	global_load_lds_dwordx4 v[2:3], off
	v_lshl_add_u64 v[2:3], s[66:67], 0, v[150:151]
	s_mov_b32 m0, s71
	s_nop 0
	global_load_lds_dwordx4 v[2:3], off
	s_waitcnt vmcnt(10)
	s_barrier
	v_mfma_scale_f32_16x16x128_f8f6f4 v[94:97], v[226:233], v[178:185], v[94:97], v205, v205 op_sel_hi:[0,0,0]
	v_mfma_scale_f32_16x16x128_f8f6f4 v[90:93], v[234:241], v[178:185], v[90:93], v205, v205 op_sel_hi:[0,0,0]
	v_mfma_scale_f32_16x16x128_f8f6f4 v[62:65], v[226:233], v[186:193], v[62:65], v205, v205 op_sel_hi:[0,0,0]
	v_mfma_scale_f32_16x16x128_f8f6f4 v[58:61], v[234:241], v[186:193], v[58:61], v205, v205 op_sel_hi:[0,0,0]
	v_mfma_scale_f32_16x16x128_f8f6f4 v[46:49], v[226:233], v[194:201], v[46:49], v205, v205 op_sel_hi:[0,0,0]
	v_mfma_scale_f32_16x16x128_f8f6f4 v[42:45], v[234:241], v[194:201], v[42:45], v205, v205 op_sel_hi:[0,0,0]
	v_mfma_scale_f32_16x16x128_f8f6f4 v[22:25], v[226:233], v[218:225], v[22:25], v205, v205 op_sel_hi:[0,0,0]
	v_mfma_scale_f32_16x16x128_f8f6f4 v[18:21], v[234:241], v[218:225], v[18:21], v205, v205 op_sel_hi:[0,0,0]
	s_add_u32 s62, s62, 0x40180
	s_addc_u32 s63, s63, 0
	s_add_u32 s72, s64, 0x200
	s_addc_u32 s73, s65, 0
	s_mov_b32 s74, 0
	s_barrier
.LBB0_1483:
	ds_read_b128 v[10:13], v130
	ds_read_b128 v[14:17], v130 offset:1024
	ds_read_b128 v[160:163], v130 offset:2048
	ds_read_b128 v[164:167], v130 offset:3072
	s_add_u32 s64, s62, 0xfffc0080
	s_addc_u32 s65, s63, -1
	s_cmp_eq_u32 s74, 12
	s_cselect_b32 s67, s19, s65
	s_cselect_b32 s66, s18, s64
	s_cselect_b32 s65, s61, s73
	s_cselect_b32 s64, s60, s72
	s_mov_b32 m0, s7
	v_lshl_add_u64 v[2:3], s[62:63], 0, v[156:157]
	ds_read_b128 v[178:181], v170
	ds_read_b128 v[182:185], v170 offset:1024
	ds_read_b128 v[186:189], v170 offset:2048
	ds_read_b128 v[190:193], v170 offset:3072
	ds_read_b128 v[194:197], v170 offset:4096
	ds_read_b128 v[198:201], v170 offset:5120
	ds_read_b128 v[218:221], v170 offset:6144
	ds_read_b128 v[222:225], v170 offset:7168
	global_load_lds_dwordx4 v[2:3], off
	v_lshl_add_u64 v[2:3], s[62:63], 0, v[158:159]
	s_mov_b32 m0, s9
	s_nop 0
	global_load_lds_dwordx4 v[2:3], off
	s_waitcnt lgkmcnt(8)
	s_waitcnt vmcnt(10)
	s_barrier
	s_waitcnt lgkmcnt(6)
	v_mfma_scale_f32_16x16x128_f8f6f4 v[132:135], v[10:17], v[178:185], v[132:135], v205, v205 op_sel_hi:[0,0,0]
	v_mfma_scale_f32_16x16x128_f8f6f4 v[136:139], v[160:167], v[178:185], v[136:139], v205, v205 op_sel_hi:[0,0,0]
	s_waitcnt lgkmcnt(4)
	v_mfma_scale_f32_16x16x128_f8f6f4 v[118:121], v[10:17], v[186:193], v[118:121], v205, v205 op_sel_hi:[0,0,0]
	v_mfma_scale_f32_16x16x128_f8f6f4 v[114:117], v[160:167], v[186:193], v[114:117], v205, v205 op_sel_hi:[0,0,0]
	s_waitcnt lgkmcnt(2)
	v_mfma_scale_f32_16x16x128_f8f6f4 v[102:105], v[10:17], v[194:201], v[102:105], v205, v205 op_sel_hi:[0,0,0]
	v_mfma_scale_f32_16x16x128_f8f6f4 v[98:101], v[160:167], v[194:201], v[98:101], v205, v205 op_sel_hi:[0,0,0]
	s_waitcnt lgkmcnt(0)
	v_mfma_scale_f32_16x16x128_f8f6f4 v[70:73], v[10:17], v[218:225], v[70:73], v205, v205 op_sel_hi:[0,0,0]
	v_mfma_scale_f32_16x16x128_f8f6f4 v[66:69], v[160:167], v[218:225], v[66:69], v205, v205 op_sel_hi:[0,0,0]
	s_barrier
	s_mov_b32 m0, s15
	v_lshl_add_u64 v[6:7], s[64:65], 0, v[154:155]
	ds_read_b128 v[226:229], v171
	ds_read_b128 v[230:233], v171 offset:1024
	ds_read_b128 v[234:237], v171 offset:2048
	ds_read_b128 v[238:241], v171 offset:3072
	global_load_lds_dwordx4 v[6:7], off
	v_lshl_add_u64 v[8:9], s[64:65], 0, v[150:151]
	s_mov_b32 m0, s57
	s_nop 0
	global_load_lds_dwordx4 v[8:9], off
	s_waitcnt vmcnt(10)
	s_barrier
	s_waitcnt lgkmcnt(2)
	v_mfma_scale_f32_16x16x128_f8f6f4 v[140:143], v[226:233], v[178:185], v[140:143], v205, v205 op_sel_hi:[0,0,0]
	s_waitcnt lgkmcnt(0)
	v_mfma_scale_f32_16x16x128_f8f6f4 v[144:147], v[234:241], v[178:185], v[144:147], v205, v205 op_sel_hi:[0,0,0]
	v_mfma_scale_f32_16x16x128_f8f6f4 v[126:129], v[226:233], v[186:193], v[126:129], v205, v205 op_sel_hi:[0,0,0]
	v_mfma_scale_f32_16x16x128_f8f6f4 v[122:125], v[234:241], v[186:193], v[122:125], v205, v205 op_sel_hi:[0,0,0]
	v_mfma_scale_f32_16x16x128_f8f6f4 v[110:113], v[226:233], v[194:201], v[110:113], v205, v205 op_sel_hi:[0,0,0]
	v_mfma_scale_f32_16x16x128_f8f6f4 v[106:109], v[234:241], v[194:201], v[106:109], v205, v205 op_sel_hi:[0,0,0]
	v_mfma_scale_f32_16x16x128_f8f6f4 v[86:89], v[226:233], v[218:225], v[86:89], v205, v205 op_sel_hi:[0,0,0]
	v_mfma_scale_f32_16x16x128_f8f6f4 v[82:85], v[234:241], v[218:225], v[82:85], v205, v205 op_sel_hi:[0,0,0]
	s_mov_b32 m0, s17
	v_lshl_add_u64 v[2:3], s[66:67], 0, v[152:153]
	s_barrier
	ds_read_b128 v[178:181], v170 offset:16384
	ds_read_b128 v[182:185], v170 offset:17408
	ds_read_b128 v[186:189], v170 offset:18432
	ds_read_b128 v[190:193], v170 offset:19456
	ds_read_b128 v[194:197], v170 offset:20480
	ds_read_b128 v[198:201], v170 offset:21504
	ds_read_b128 v[218:221], v170 offset:22528
	ds_read_b128 v[222:225], v170 offset:23552
	global_load_lds_dwordx4 v[2:3], off
	v_lshl_add_u64 v[4:5], s[66:67], 0, v[148:149]
	s_mov_b32 m0, s43
	s_nop 0
	global_load_lds_dwordx4 v[4:5], off
	s_barrier
	s_waitcnt lgkmcnt(6)
	v_mfma_scale_f32_16x16x128_f8f6f4 v[78:81], v[10:17], v[178:185], v[78:81], v205, v205 op_sel_hi:[0,0,0]
	v_mfma_scale_f32_16x16x128_f8f6f4 v[74:77], v[160:167], v[178:185], v[74:77], v205, v205 op_sel_hi:[0,0,0]
	s_waitcnt lgkmcnt(4)
	v_mfma_scale_f32_16x16x128_f8f6f4 v[54:57], v[10:17], v[186:193], v[54:57], v205, v205 op_sel_hi:[0,0,0]
	v_mfma_scale_f32_16x16x128_f8f6f4 v[50:53], v[160:167], v[186:193], v[50:53], v205, v205 op_sel_hi:[0,0,0]
	s_waitcnt lgkmcnt(2)
	v_mfma_scale_f32_16x16x128_f8f6f4 v[38:41], v[10:17], v[194:201], v[38:41], v205, v205 op_sel_hi:[0,0,0]
	v_mfma_scale_f32_16x16x128_f8f6f4 v[34:37], v[160:167], v[194:201], v[34:37], v205, v205 op_sel_hi:[0,0,0]
	s_waitcnt lgkmcnt(0)
	v_mfma_scale_f32_16x16x128_f8f6f4 v[30:33], v[10:17], v[218:225], v[30:33], v205, v205 op_sel_hi:[0,0,0]
	v_mfma_scale_f32_16x16x128_f8f6f4 v[26:29], v[160:167], v[218:225], v[26:29], v205, v205 op_sel_hi:[0,0,0]
	s_barrier
	s_add_u32 s76, s64, 0x4000
	s_addc_u32 s77, s65, 0
	s_mov_b32 m0, s58
	v_lshl_add_u64 v[10:11], s[76:77], 0, v[154:155]
	global_load_lds_dwordx4 v[10:11], off
	v_lshl_add_u64 v[10:11], s[76:77], 0, v[150:151]
	s_mov_b32 m0, s59
	s_nop 0
	global_load_lds_dwordx4 v[10:11], off
	s_waitcnt vmcnt(10)
	s_barrier
	v_mfma_scale_f32_16x16x128_f8f6f4 v[94:97], v[226:233], v[178:185], v[94:97], v205, v205 op_sel_hi:[0,0,0]
	v_mfma_scale_f32_16x16x128_f8f6f4 v[90:93], v[234:241], v[178:185], v[90:93], v205, v205 op_sel_hi:[0,0,0]
	v_mfma_scale_f32_16x16x128_f8f6f4 v[62:65], v[226:233], v[186:193], v[62:65], v205, v205 op_sel_hi:[0,0,0]
	v_mfma_scale_f32_16x16x128_f8f6f4 v[58:61], v[234:241], v[186:193], v[58:61], v205, v205 op_sel_hi:[0,0,0]
	v_mfma_scale_f32_16x16x128_f8f6f4 v[46:49], v[226:233], v[194:201], v[46:49], v205, v205 op_sel_hi:[0,0,0]
	v_mfma_scale_f32_16x16x128_f8f6f4 v[42:45], v[234:241], v[194:201], v[42:45], v205, v205 op_sel_hi:[0,0,0]
	v_mfma_scale_f32_16x16x128_f8f6f4 v[22:25], v[226:233], v[218:225], v[22:25], v205, v205 op_sel_hi:[0,0,0]
	v_mfma_scale_f32_16x16x128_f8f6f4 v[18:21], v[234:241], v[218:225], v[18:21], v205, v205 op_sel_hi:[0,0,0]
	s_barrier
	ds_read_b128 v[10:13], v172
	ds_read_b128 v[14:17], v172 offset:1024
	ds_read_b128 v[160:163], v172 offset:2048
	ds_read_b128 v[164:167], v172 offset:3072
	s_add_u32 s66, s66, 0x40000
	s_addc_u32 s67, s67, 0
	s_mov_b32 m0, s44
	v_lshl_add_u64 v[174:175], s[66:67], 0, v[152:153]
	ds_read_b128 v[178:181], v170 offset:32768
	ds_read_b128 v[182:185], v170 offset:33792
	ds_read_b128 v[186:189], v170 offset:34816
	ds_read_b128 v[190:193], v170 offset:35840
	ds_read_b128 v[194:197], v170 offset:36864
	ds_read_b128 v[198:201], v170 offset:37888
	ds_read_b128 v[218:221], v170 offset:38912
	ds_read_b128 v[222:225], v170 offset:39936
	global_load_lds_dwordx4 v[174:175], off
	v_lshl_add_u64 v[174:175], s[66:67], 0, v[148:149]
	s_mov_b32 m0, s45
	s_nop 0
	global_load_lds_dwordx4 v[174:175], off
	s_waitcnt lgkmcnt(8)
	s_waitcnt vmcnt(10)
	s_barrier
	s_waitcnt lgkmcnt(6)
	v_mfma_scale_f32_16x16x128_f8f6f4 v[132:135], v[10:17], v[178:185], v[132:135], v205, v205 op_sel_hi:[0,0,0]
	v_mfma_scale_f32_16x16x128_f8f6f4 v[136:139], v[160:167], v[178:185], v[136:139], v205, v205 op_sel_hi:[0,0,0]
	s_waitcnt lgkmcnt(4)
	v_mfma_scale_f32_16x16x128_f8f6f4 v[118:121], v[10:17], v[186:193], v[118:121], v205, v205 op_sel_hi:[0,0,0]
	v_mfma_scale_f32_16x16x128_f8f6f4 v[114:117], v[160:167], v[186:193], v[114:117], v205, v205 op_sel_hi:[0,0,0]
	s_waitcnt lgkmcnt(2)
	v_mfma_scale_f32_16x16x128_f8f6f4 v[102:105], v[10:17], v[194:201], v[102:105], v205, v205 op_sel_hi:[0,0,0]
	v_mfma_scale_f32_16x16x128_f8f6f4 v[98:101], v[160:167], v[194:201], v[98:101], v205, v205 op_sel_hi:[0,0,0]
	s_waitcnt lgkmcnt(0)
	v_mfma_scale_f32_16x16x128_f8f6f4 v[70:73], v[10:17], v[218:225], v[70:73], v205, v205 op_sel_hi:[0,0,0]
	v_mfma_scale_f32_16x16x128_f8f6f4 v[66:69], v[160:167], v[218:225], v[66:69], v205, v205 op_sel_hi:[0,0,0]
	s_barrier
	s_mov_b32 m0, s68
	v_lshl_add_u64 v[6:7], v[6:7], 0, s[30:31]
	ds_read_b128 v[226:229], v173
	ds_read_b128 v[230:233], v173 offset:1024
	ds_read_b128 v[234:237], v173 offset:2048
	ds_read_b128 v[238:241], v173 offset:3072
	global_load_lds_dwordx4 v[6:7], off
	v_lshl_add_u64 v[6:7], v[8:9], 0, s[30:31]
	s_mov_b32 m0, s69
	s_nop 0
	global_load_lds_dwordx4 v[6:7], off
	s_waitcnt vmcnt(10)
	s_barrier
	s_waitcnt lgkmcnt(2)
	v_mfma_scale_f32_16x16x128_f8f6f4 v[140:143], v[226:233], v[178:185], v[140:143], v205, v205 op_sel_hi:[0,0,0]
	s_waitcnt lgkmcnt(0)
	v_mfma_scale_f32_16x16x128_f8f6f4 v[144:147], v[234:241], v[178:185], v[144:147], v205, v205 op_sel_hi:[0,0,0]
	v_mfma_scale_f32_16x16x128_f8f6f4 v[126:129], v[226:233], v[186:193], v[126:129], v205, v205 op_sel_hi:[0,0,0]
	v_mfma_scale_f32_16x16x128_f8f6f4 v[122:125], v[234:241], v[186:193], v[122:125], v205, v205 op_sel_hi:[0,0,0]
	v_mfma_scale_f32_16x16x128_f8f6f4 v[110:113], v[226:233], v[194:201], v[110:113], v205, v205 op_sel_hi:[0,0,0]
	v_mfma_scale_f32_16x16x128_f8f6f4 v[106:109], v[234:241], v[194:201], v[106:109], v205, v205 op_sel_hi:[0,0,0]
	v_mfma_scale_f32_16x16x128_f8f6f4 v[86:89], v[226:233], v[218:225], v[86:89], v205, v205 op_sel_hi:[0,0,0]
	v_mfma_scale_f32_16x16x128_f8f6f4 v[82:85], v[234:241], v[218:225], v[82:85], v205, v205 op_sel_hi:[0,0,0]
	s_mov_b32 m0, s50
	v_lshl_add_u64 v[2:3], v[2:3], 0, s[30:31]
	s_barrier
	ds_read_b128 v[178:181], v170 offset:49152
	ds_read_b128 v[182:185], v170 offset:50176
	ds_read_b128 v[186:189], v170 offset:51200
	ds_read_b128 v[190:193], v170 offset:52224
	ds_read_b128 v[194:197], v170 offset:53248
	ds_read_b128 v[198:201], v170 offset:54272
	ds_read_b128 v[218:221], v170 offset:55296
	ds_read_b128 v[222:225], v170 offset:56320
	global_load_lds_dwordx4 v[2:3], off
	v_lshl_add_u64 v[2:3], v[4:5], 0, s[30:31]
	s_mov_b32 m0, s51
	s_nop 0
	global_load_lds_dwordx4 v[2:3], off
	s_barrier
	s_waitcnt lgkmcnt(6)
	v_mfma_scale_f32_16x16x128_f8f6f4 v[78:81], v[10:17], v[178:185], v[78:81], v205, v205 op_sel_hi:[0,0,0]
	v_mfma_scale_f32_16x16x128_f8f6f4 v[74:77], v[160:167], v[178:185], v[74:77], v205, v205 op_sel_hi:[0,0,0]
	s_waitcnt lgkmcnt(4)
	v_mfma_scale_f32_16x16x128_f8f6f4 v[54:57], v[10:17], v[186:193], v[54:57], v205, v205 op_sel_hi:[0,0,0]
	v_mfma_scale_f32_16x16x128_f8f6f4 v[50:53], v[160:167], v[186:193], v[50:53], v205, v205 op_sel_hi:[0,0,0]
	s_waitcnt lgkmcnt(2)
	v_mfma_scale_f32_16x16x128_f8f6f4 v[38:41], v[10:17], v[194:201], v[38:41], v205, v205 op_sel_hi:[0,0,0]
	v_mfma_scale_f32_16x16x128_f8f6f4 v[34:37], v[160:167], v[194:201], v[34:37], v205, v205 op_sel_hi:[0,0,0]
	s_waitcnt lgkmcnt(0)
	v_mfma_scale_f32_16x16x128_f8f6f4 v[30:33], v[10:17], v[218:225], v[30:33], v205, v205 op_sel_hi:[0,0,0]
	v_mfma_scale_f32_16x16x128_f8f6f4 v[26:29], v[160:167], v[218:225], v[26:29], v205, v205 op_sel_hi:[0,0,0]
	s_barrier
	s_add_u32 s64, s64, 0x4080
	s_addc_u32 s65, s65, 0
	s_mov_b32 m0, s70
	v_lshl_add_u64 v[2:3], s[64:65], 0, v[154:155]
	global_load_lds_dwordx4 v[2:3], off
	v_lshl_add_u64 v[2:3], s[64:65], 0, v[150:151]
	s_mov_b32 m0, s71
	s_nop 0
	global_load_lds_dwordx4 v[2:3], off
	s_waitcnt vmcnt(10)
	s_barrier
	v_mfma_scale_f32_16x16x128_f8f6f4 v[94:97], v[226:233], v[178:185], v[94:97], v205, v205 op_sel_hi:[0,0,0]
	v_mfma_scale_f32_16x16x128_f8f6f4 v[90:93], v[234:241], v[178:185], v[90:93], v205, v205 op_sel_hi:[0,0,0]
	v_mfma_scale_f32_16x16x128_f8f6f4 v[62:65], v[226:233], v[186:193], v[62:65], v205, v205 op_sel_hi:[0,0,0]
	v_mfma_scale_f32_16x16x128_f8f6f4 v[58:61], v[234:241], v[186:193], v[58:61], v205, v205 op_sel_hi:[0,0,0]
	v_mfma_scale_f32_16x16x128_f8f6f4 v[46:49], v[226:233], v[194:201], v[46:49], v205, v205 op_sel_hi:[0,0,0]
	v_mfma_scale_f32_16x16x128_f8f6f4 v[42:45], v[234:241], v[194:201], v[42:45], v205, v205 op_sel_hi:[0,0,0]
	v_mfma_scale_f32_16x16x128_f8f6f4 v[22:25], v[226:233], v[218:225], v[22:25], v205, v205 op_sel_hi:[0,0,0]
	v_mfma_scale_f32_16x16x128_f8f6f4 v[18:21], v[234:241], v[218:225], v[18:21], v205, v205 op_sel_hi:[0,0,0]
	s_setprio 0
	s_add_i32 s74, s74, 2
	s_add_u32 s62, s62, 0x100
	s_addc_u32 s63, s63, 0
	s_add_u32 s72, s72, 0x100
	s_addc_u32 s73, s73, 0
	s_cmp_gt_u32 s74, 13
	s_barrier
	s_cbranch_scc0 .LBB0_1483
	v_pk_mul_f32 v[4:5], v[132:133], s[56:57] op_sel_hi:[1,0]
	v_pk_mul_f32 v[6:7], v[134:135], s[56:57] op_sel_hi:[1,0]
	v_med3_f32 v12, v4, s26, v209
	v_med3_f32 v5, v5, s26, v209
	v_mov_b32_e32 v4, v131
	v_cvt_pk_fp8_f32 v4, v12, v5
	v_pk_mul_f32 v[10:11], v[136:137], s[56:57] op_sel_hi:[1,0]
	v_med3_f32 v5, v6, s26, v209
	v_med3_f32 v6, v7, s26, v209
	v_cvt_pk_fp8_f32 v4, v5, v6 op_sel:[0,0,1]
	v_med3_f32 v6, v10, s26, v209
	v_med3_f32 v7, v11, s26, v209
	v_mov_b32_e32 v5, v131
	v_cvt_pk_fp8_f32 v5, v6, v7
	v_pk_mul_f32 v[8:9], v[138:139], s[56:57] op_sel_hi:[1,0]
	v_pk_mul_f32 v[12:13], v[144:145], s[56:57] op_sel_hi:[1,0]
	v_med3_f32 v6, v8, s26, v209
	v_med3_f32 v7, v9, s26, v209
	v_cvt_pk_fp8_f32 v5, v6, v7 op_sel:[0,0,1]
	v_pk_mul_f32 v[6:7], v[140:141], s[56:57] op_sel_hi:[1,0]
	v_pk_mul_f32 v[8:9], v[142:143], s[56:57] op_sel_hi:[1,0]
	v_med3_f32 v14, v6, s26, v209
	v_med3_f32 v7, v7, s26, v209
	v_mov_b32_e32 v6, v131
	v_cvt_pk_fp8_f32 v6, v14, v7
	v_med3_f32 v7, v8, s26, v209
	v_med3_f32 v8, v9, s26, v209
	v_med3_f32 v9, v13, s26, v209
	v_cvt_pk_fp8_f32 v6, v7, v8 op_sel:[0,0,1]
	v_med3_f32 v8, v12, s26, v209
	v_mov_b32_e32 v7, v131
	v_cvt_pk_fp8_f32 v7, v8, v9
	s_ashr_i32 s15, s14, 31
	v_pk_mul_f32 v[10:11], v[146:147], s[56:57] op_sel_hi:[1,0]
	s_lshl_b64 s[14:15], s[14:15], 10
	v_med3_f32 v8, v10, s26, v209
	v_med3_f32 v9, v11, s26, v209
	s_add_u32 s7, s46, s14
	v_cvt_pk_fp8_f32 v7, v8, v9 op_sel:[0,0,1]
	s_addc_u32 s9, s47, s15
	s_ashr_i32 s15, s16, 31
	s_add_u32 s14, s7, s16
	s_addc_u32 s15, s9, s15
	v_mov_b32_e32 v130, v169
	s_nop 15
	s_nop 15
	global_store_dwordx4 v130, v[4:7], s[14:15]
	v_pk_mul_f32 v[10:11], v[114:115], s[56:57] op_sel_hi:[1,0]
	v_pk_mul_f32 v[8:9], v[116:117], s[56:57] op_sel_hi:[1,0]
	v_pk_mul_f32 v[4:5], v[118:119], s[56:57] op_sel_hi:[1,0]
	v_pk_mul_f32 v[6:7], v[120:121], s[56:57] op_sel_hi:[1,0]
	v_med3_f32 v12, v4, s26, v209
	v_med3_f32 v5, v5, s26, v209
	v_mov_b32_e32 v4, v131
	v_cvt_pk_fp8_f32 v4, v12, v5
	v_med3_f32 v5, v6, s26, v209
	v_med3_f32 v6, v7, s26, v209
	v_med3_f32 v7, v11, s26, v209
	v_cvt_pk_fp8_f32 v4, v5, v6 op_sel:[0,0,1]
	v_med3_f32 v6, v10, s26, v209
	v_mov_b32_e32 v5, v131
	v_cvt_pk_fp8_f32 v5, v6, v7
	v_med3_f32 v6, v8, s26, v209
	v_med3_f32 v7, v9, s26, v209
	v_pk_mul_f32 v[8:9], v[128:129], s[56:57] op_sel_hi:[1,0]
	v_cvt_pk_fp8_f32 v5, v6, v7 op_sel:[0,0,1]
	v_pk_mul_f32 v[6:7], v[126:127], s[56:57] op_sel_hi:[1,0]
	v_pk_mul_f32 v[12:13], v[122:123], s[56:57] op_sel_hi:[1,0]
	v_med3_f32 v14, v6, s26, v209
	v_med3_f32 v7, v7, s26, v209
	v_mov_b32_e32 v6, v131
	v_cvt_pk_fp8_f32 v6, v14, v7
	v_med3_f32 v7, v8, s26, v209
	v_med3_f32 v8, v9, s26, v209
	v_med3_f32 v9, v13, s26, v209
	v_cvt_pk_fp8_f32 v6, v7, v8 op_sel:[0,0,1]
	v_med3_f32 v8, v12, s26, v209
	v_mov_b32_e32 v7, v131
	v_cvt_pk_fp8_f32 v7, v8, v9
	v_pk_mul_f32 v[10:11], v[124:125], s[56:57] op_sel_hi:[1,0]
	v_lshl_add_u64 v[2:3], s[14:15], 0, v[130:131]
	v_med3_f32 v8, v10, s26, v209
	v_med3_f32 v9, v11, s26, v209
	v_cvt_pk_fp8_f32 v7, v8, v9 op_sel:[0,0,1]
	v_add_co_u32_e32 v8, vcc, s90, v2
	v_pk_mul_f32 v[10:11], v[98:99], s[56:57] op_sel_hi:[1,0]
	s_nop 0
	v_addc_co_u32_e32 v9, vcc, 0, v3, vcc
	global_store_dwordx4 v[8:9], v[4:7], off
	v_pk_mul_f32 v[8:9], v[100:101], s[56:57] op_sel_hi:[1,0]
	s_mov_b32 s7, 0x8000
	v_pk_mul_f32 v[4:5], v[102:103], s[56:57] op_sel_hi:[1,0]
	v_pk_mul_f32 v[6:7], v[104:105], s[56:57] op_sel_hi:[1,0]
	v_med3_f32 v12, v4, s26, v209
	v_med3_f32 v5, v5, s26, v209
	v_mov_b32_e32 v4, v131
	v_cvt_pk_fp8_f32 v4, v12, v5
	v_med3_f32 v5, v6, s26, v209
	v_med3_f32 v6, v7, s26, v209
	v_med3_f32 v7, v11, s26, v209
	v_cvt_pk_fp8_f32 v4, v5, v6 op_sel:[0,0,1]
	v_med3_f32 v6, v10, s26, v209
	v_mov_b32_e32 v5, v131
	v_cvt_pk_fp8_f32 v5, v6, v7
	v_med3_f32 v6, v8, s26, v209
	v_med3_f32 v7, v9, s26, v209
	v_pk_mul_f32 v[8:9], v[112:113], s[56:57] op_sel_hi:[1,0]
	v_cvt_pk_fp8_f32 v5, v6, v7 op_sel:[0,0,1]
	v_pk_mul_f32 v[6:7], v[110:111], s[56:57] op_sel_hi:[1,0]
	v_pk_mul_f32 v[12:13], v[106:107], s[56:57] op_sel_hi:[1,0]
	v_med3_f32 v14, v6, s26, v209
	v_med3_f32 v7, v7, s26, v209
	v_mov_b32_e32 v6, v131
	v_cvt_pk_fp8_f32 v6, v14, v7
	v_med3_f32 v7, v8, s26, v209
	v_med3_f32 v8, v9, s26, v209
	v_med3_f32 v9, v13, s26, v209
	v_cvt_pk_fp8_f32 v6, v7, v8 op_sel:[0,0,1]
	v_med3_f32 v8, v12, s26, v209
	v_mov_b32_e32 v7, v131
	v_cvt_pk_fp8_f32 v7, v8, v9
	v_pk_mul_f32 v[10:11], v[108:109], s[56:57] op_sel_hi:[1,0]
	s_mov_b32 s14, s6
	v_med3_f32 v8, v10, s26, v209
	v_med3_f32 v9, v11, s26, v209
	v_cvt_pk_fp8_f32 v7, v8, v9 op_sel:[0,0,1]
	v_add_co_u32_e32 v8, vcc, s7, v2
	v_pk_mul_f32 v[10:11], v[66:67], s[56:57] op_sel_hi:[1,0]
	s_nop 0
	v_addc_co_u32_e32 v9, vcc, 0, v3, vcc
	global_store_dwordx4 v[8:9], v[4:7], off
	v_pk_mul_f32 v[8:9], v[68:69], s[56:57] op_sel_hi:[1,0]
	s_mov_b32 s7, 0xc000
	v_pk_mul_f32 v[4:5], v[70:71], s[56:57] op_sel_hi:[1,0]
	v_pk_mul_f32 v[6:7], v[72:73], s[56:57] op_sel_hi:[1,0]
	v_med3_f32 v12, v4, s26, v209
	v_med3_f32 v5, v5, s26, v209
	v_mov_b32_e32 v4, v131
	v_cvt_pk_fp8_f32 v4, v12, v5
	v_med3_f32 v5, v6, s26, v209
	v_med3_f32 v6, v7, s26, v209
	v_med3_f32 v7, v11, s26, v209
	v_cvt_pk_fp8_f32 v4, v5, v6 op_sel:[0,0,1]
	v_med3_f32 v6, v10, s26, v209
	v_mov_b32_e32 v5, v131
	v_cvt_pk_fp8_f32 v5, v6, v7
	v_med3_f32 v6, v8, s26, v209
	v_med3_f32 v7, v9, s26, v209
	v_pk_mul_f32 v[8:9], v[88:89], s[56:57] op_sel_hi:[1,0]
	v_cvt_pk_fp8_f32 v5, v6, v7 op_sel:[0,0,1]
	v_pk_mul_f32 v[6:7], v[86:87], s[56:57] op_sel_hi:[1,0]
	v_pk_mul_f32 v[12:13], v[82:83], s[56:57] op_sel_hi:[1,0]
	v_med3_f32 v14, v6, s26, v209
	v_med3_f32 v7, v7, s26, v209
	v_mov_b32_e32 v6, v131
	v_cvt_pk_fp8_f32 v6, v14, v7
	v_med3_f32 v7, v8, s26, v209
	v_med3_f32 v8, v9, s26, v209
	v_med3_f32 v9, v13, s26, v209
	v_cvt_pk_fp8_f32 v6, v7, v8 op_sel:[0,0,1]
	v_med3_f32 v8, v12, s26, v209
	v_mov_b32_e32 v7, v131
	v_cvt_pk_fp8_f32 v7, v8, v9
	v_pk_mul_f32 v[10:11], v[84:85], s[56:57] op_sel_hi:[1,0]
	s_mov_b32 s16, s8
	v_med3_f32 v8, v10, s26, v209
	v_med3_f32 v9, v11, s26, v209
	v_cvt_pk_fp8_f32 v7, v8, v9 op_sel:[0,0,1]
	v_add_co_u32_e32 v8, vcc, s7, v2
	v_pk_mul_f32 v[10:11], v[74:75], s[56:57] op_sel_hi:[1,0]
	s_nop 0
	v_addc_co_u32_e32 v9, vcc, 0, v3, vcc
	global_store_dwordx4 v[8:9], v[4:7], off
	v_pk_mul_f32 v[8:9], v[76:77], s[56:57] op_sel_hi:[1,0]
	s_mov_b32 s7, 0x20000
	v_pk_mul_f32 v[4:5], v[78:79], s[56:57] op_sel_hi:[1,0]
	v_pk_mul_f32 v[6:7], v[80:81], s[56:57] op_sel_hi:[1,0]
	v_med3_f32 v12, v4, s26, v209
	v_med3_f32 v5, v5, s26, v209
	v_mov_b32_e32 v4, v131
	v_cvt_pk_fp8_f32 v4, v12, v5
	v_med3_f32 v5, v6, s26, v209
	v_med3_f32 v6, v7, s26, v209
	v_med3_f32 v7, v11, s26, v209
	v_cvt_pk_fp8_f32 v4, v5, v6 op_sel:[0,0,1]
	v_med3_f32 v6, v10, s26, v209
	v_mov_b32_e32 v5, v131
	v_cvt_pk_fp8_f32 v5, v6, v7
	v_med3_f32 v6, v8, s26, v209
	v_med3_f32 v7, v9, s26, v209
	v_pk_mul_f32 v[8:9], v[96:97], s[56:57] op_sel_hi:[1,0]
	v_cvt_pk_fp8_f32 v5, v6, v7 op_sel:[0,0,1]
	v_pk_mul_f32 v[6:7], v[94:95], s[56:57] op_sel_hi:[1,0]
	v_pk_mul_f32 v[12:13], v[90:91], s[56:57] op_sel_hi:[1,0]
	v_med3_f32 v14, v6, s26, v209
	v_med3_f32 v7, v7, s26, v209
	v_mov_b32_e32 v6, v131
	v_cvt_pk_fp8_f32 v6, v14, v7
	v_med3_f32 v7, v8, s26, v209
	v_med3_f32 v8, v9, s26, v209
	v_med3_f32 v9, v13, s26, v209
	v_cvt_pk_fp8_f32 v6, v7, v8 op_sel:[0,0,1]
	v_med3_f32 v8, v12, s26, v209
	v_mov_b32_e32 v7, v131
	v_cvt_pk_fp8_f32 v7, v8, v9
	v_pk_mul_f32 v[10:11], v[92:93], s[56:57] op_sel_hi:[1,0]
	s_mov_b64 s[64:65], s[10:11]
	v_med3_f32 v8, v10, s26, v209
	v_med3_f32 v9, v11, s26, v209
	v_cvt_pk_fp8_f32 v7, v8, v9 op_sel:[0,0,1]
	v_add_co_u32_e32 v8, vcc, s7, v2
	v_pk_mul_f32 v[10:11], v[50:51], s[56:57] op_sel_hi:[1,0]
	s_nop 0
	v_addc_co_u32_e32 v9, vcc, 0, v3, vcc
	global_store_dwordx4 v[8:9], v[4:7], off
	v_pk_mul_f32 v[8:9], v[52:53], s[56:57] op_sel_hi:[1,0]
	s_mov_b32 s7, 0x24000
	v_pk_mul_f32 v[4:5], v[54:55], s[56:57] op_sel_hi:[1,0]
	v_pk_mul_f32 v[6:7], v[56:57], s[56:57] op_sel_hi:[1,0]
	v_med3_f32 v12, v4, s26, v209
	v_med3_f32 v5, v5, s26, v209
	v_mov_b32_e32 v4, v131
	v_cvt_pk_fp8_f32 v4, v12, v5
	v_med3_f32 v5, v6, s26, v209
	v_med3_f32 v6, v7, s26, v209
	v_med3_f32 v7, v11, s26, v209
	v_cvt_pk_fp8_f32 v4, v5, v6 op_sel:[0,0,1]
	v_med3_f32 v6, v10, s26, v209
	v_mov_b32_e32 v5, v131
	v_cvt_pk_fp8_f32 v5, v6, v7
	v_med3_f32 v6, v8, s26, v209
	v_med3_f32 v7, v9, s26, v209
	v_pk_mul_f32 v[8:9], v[64:65], s[56:57] op_sel_hi:[1,0]
	v_cvt_pk_fp8_f32 v5, v6, v7 op_sel:[0,0,1]
	v_pk_mul_f32 v[6:7], v[62:63], s[56:57] op_sel_hi:[1,0]
	v_pk_mul_f32 v[12:13], v[58:59], s[56:57] op_sel_hi:[1,0]
	v_med3_f32 v14, v6, s26, v209
	v_med3_f32 v7, v7, s26, v209
	v_mov_b32_e32 v6, v131
	v_cvt_pk_fp8_f32 v6, v14, v7
	v_med3_f32 v7, v8, s26, v209
	v_med3_f32 v8, v9, s26, v209
	v_med3_f32 v9, v13, s26, v209
	v_cvt_pk_fp8_f32 v6, v7, v8 op_sel:[0,0,1]
	v_med3_f32 v8, v12, s26, v209
	v_mov_b32_e32 v7, v131
	v_cvt_pk_fp8_f32 v7, v8, v9
	v_pk_mul_f32 v[10:11], v[60:61], s[56:57] op_sel_hi:[1,0]
	s_mov_b64 s[62:63], s[12:13]
	v_med3_f32 v8, v10, s26, v209
	v_med3_f32 v9, v11, s26, v209
	v_cvt_pk_fp8_f32 v7, v8, v9 op_sel:[0,0,1]
	v_add_co_u32_e32 v8, vcc, s7, v2
	v_pk_mul_f32 v[10:11], v[34:35], s[56:57] op_sel_hi:[1,0]
	s_nop 0
	v_addc_co_u32_e32 v9, vcc, 0, v3, vcc
	global_store_dwordx4 v[8:9], v[4:7], off
	v_pk_mul_f32 v[8:9], v[36:37], s[56:57] op_sel_hi:[1,0]
	s_mov_b32 s7, 0x28000
	v_pk_mul_f32 v[4:5], v[38:39], s[56:57] op_sel_hi:[1,0]
	v_pk_mul_f32 v[6:7], v[40:41], s[56:57] op_sel_hi:[1,0]
	v_med3_f32 v12, v4, s26, v209
	v_med3_f32 v5, v5, s26, v209
	v_mov_b32_e32 v4, v131
	v_cvt_pk_fp8_f32 v4, v12, v5
	v_med3_f32 v5, v6, s26, v209
	v_med3_f32 v6, v7, s26, v209
	v_med3_f32 v7, v11, s26, v209
	v_cvt_pk_fp8_f32 v4, v5, v6 op_sel:[0,0,1]
	v_med3_f32 v6, v10, s26, v209
	v_mov_b32_e32 v5, v131
	v_cvt_pk_fp8_f32 v5, v6, v7
	v_med3_f32 v6, v8, s26, v209
	v_med3_f32 v7, v9, s26, v209
	v_pk_mul_f32 v[8:9], v[48:49], s[56:57] op_sel_hi:[1,0]
	v_cvt_pk_fp8_f32 v5, v6, v7 op_sel:[0,0,1]
	v_pk_mul_f32 v[6:7], v[46:47], s[56:57] op_sel_hi:[1,0]
	v_pk_mul_f32 v[12:13], v[42:43], s[56:57] op_sel_hi:[1,0]
	v_med3_f32 v14, v6, s26, v209
	v_med3_f32 v7, v7, s26, v209
	v_mov_b32_e32 v6, v131
	v_cvt_pk_fp8_f32 v6, v14, v7
	v_med3_f32 v7, v8, s26, v209
	v_med3_f32 v8, v9, s26, v209
	v_med3_f32 v9, v13, s26, v209
	v_cvt_pk_fp8_f32 v6, v7, v8 op_sel:[0,0,1]
	v_med3_f32 v8, v12, s26, v209
	v_mov_b32_e32 v7, v131
	v_cvt_pk_fp8_f32 v7, v8, v9
	v_pk_mul_f32 v[10:11], v[44:45], s[56:57] op_sel_hi:[1,0]
	s_nop 0
	v_med3_f32 v8, v10, s26, v209
	v_med3_f32 v9, v11, s26, v209
	v_cvt_pk_fp8_f32 v7, v8, v9 op_sel:[0,0,1]
	v_add_co_u32_e32 v8, vcc, s7, v2
	v_pk_mul_f32 v[10:11], v[26:27], s[56:57] op_sel_hi:[1,0]
	s_nop 0
	v_addc_co_u32_e32 v9, vcc, 0, v3, vcc
	global_store_dwordx4 v[8:9], v[4:7], off
	v_pk_mul_f32 v[8:9], v[28:29], s[56:57] op_sel_hi:[1,0]
	v_add_co_u32_e32 v2, vcc, 0x2c000, v2
	v_pk_mul_f32 v[4:5], v[30:31], s[56:57] op_sel_hi:[1,0]
	v_pk_mul_f32 v[6:7], v[32:33], s[56:57] op_sel_hi:[1,0]
	v_med3_f32 v12, v4, s26, v209
	v_med3_f32 v5, v5, s26, v209
	v_mov_b32_e32 v4, v131
	v_cvt_pk_fp8_f32 v4, v12, v5
	v_med3_f32 v5, v6, s26, v209
	v_med3_f32 v6, v7, s26, v209
	v_med3_f32 v7, v11, s26, v209
	v_cvt_pk_fp8_f32 v4, v5, v6 op_sel:[0,0,1]
	v_med3_f32 v6, v10, s26, v209
	v_mov_b32_e32 v5, v131
	v_cvt_pk_fp8_f32 v5, v6, v7
	v_med3_f32 v6, v8, s26, v209
	v_med3_f32 v7, v9, s26, v209
	v_pk_mul_f32 v[8:9], v[24:25], s[56:57] op_sel_hi:[1,0]
	v_cvt_pk_fp8_f32 v5, v6, v7 op_sel:[0,0,1]
	v_pk_mul_f32 v[6:7], v[22:23], s[56:57] op_sel_hi:[1,0]
	v_pk_mul_f32 v[12:13], v[18:19], s[56:57] op_sel_hi:[1,0]
	v_med3_f32 v14, v6, s26, v209
	v_med3_f32 v7, v7, s26, v209
	v_mov_b32_e32 v6, v131
	v_cvt_pk_fp8_f32 v6, v14, v7
	v_med3_f32 v7, v8, s26, v209
	v_med3_f32 v8, v9, s26, v209
	v_med3_f32 v9, v13, s26, v209
	v_cvt_pk_fp8_f32 v6, v7, v8 op_sel:[0,0,1]
	v_med3_f32 v8, v12, s26, v209
	v_mov_b32_e32 v7, v131
	v_cvt_pk_fp8_f32 v7, v8, v9
	v_pk_mul_f32 v[10:11], v[20:21], s[56:57] op_sel_hi:[1,0]
	v_addc_co_u32_e32 v3, vcc, 0, v3, vcc
	v_med3_f32 v8, v10, s26, v209
	v_med3_f32 v9, v11, s26, v209
	v_cvt_pk_fp8_f32 v7, v8, v9 op_sel:[0,0,1]
	s_and_b64 vcc, exec, s[4:5]
	global_store_dwordx4 v[2:3], v[4:7], off
	s_cbranch_vccz .LBB0_1480
	s_waitcnt vmcnt(0)
	s_setprio 0
	s_cmpk_gt_u32 s27, 0xff
	s_movk_i32 s47, 0x900
	s_cbranch_scc1 .LBB0_1487
	s_barrier
